# two conversion tiles kept in flight in the expert-weight streams on top of XCD-aware dn deal
# baseline (speedup 1.0000x reference)
; DEVI int opaque_tid() { int t = threadIdx.x; asm volatile("" : "+v"(t)); return t; }
; DEVI void cvt8_load(const Params& p, int L, int t, CvtIn& in) {
;     const int which = t / 4096, r = t % 4096, le = L * 16 + r / 256, kt = (r % 256) / 16, nt = r % 16;
;     const float* src = (which == 2 ? p.w_down : (which == 0 ? p.w_gate : p.w_up)) + (size_t)le * 2048 * 2048;
;     const int tid = opaque_tid(), nq = tid & 31, kq0 = tid >> 5;
; #pragma unroll
;     for (int it = 0; it < 2; ++it)
; #pragma unroll
;         for (int kk = 0; kk < 4; ++kk) in.v[it * 4 + kk] = __builtin_nontemporal_load((const f32x4*)(src + (size_t)(kt * 128 + (kq0 + it * 16) * 4 + kk) * 2048 + nt * 128 + nq * 4));
; }
; DEVI void cvt8_stream3(const Params& p, int L, int t0, int step, int count, char* smem) {
;     if (count <= 0) return;
;     CvtIn a, b; cvt8_load(p, L, t0, a);
;     if (count > 1) cvt8_load(p, L, t0 + step, b);
.LBB0_313:
	s_waitcnt lgkmcnt(0)
	s_cmpk_eq_i32 s14, 0x100
	s_cselect_b64 s[4:5], -1, 0
	v_readlane_b32 s6, v255, 0
	v_readlane_b32 s7, v255, 1
	v_cndmask_b32_e64 v1, 0, 1, s[4:5]
	s_mov_b64 s[16:17], -1
	s_and_b64 vcc, exec, s[6:7]
	v_cmp_ne_u32_e64 s[38:39], 1, v1
	v_readlane_b32 s4, v254, 61
	v_readlane_b32 s5, v254, 62
	s_cbranch_vccz .LBB0_326
	s_and_b64 vcc, exec, s[38:39]
	s_cbranch_vccnz .LBB0_325
	s_mov_b32 s4, s2
	s_cmpk_lt_i32 s4, 0x88
	v_readlane_b32 s4, v254, 61
	v_readlane_b32 s5, v254, 62
	s_cbranch_scc1 .LBB0_325
	s_mov_b32 s5, s2
	s_add_i32 s4, s5, 0x478
	s_and_b32 s6, s4, 0xfffff000
	s_add_i32 s7, s5, 0x1477
	s_cmpk_lt_u32 s7, 0x1fff
	s_cselect_b32 s7, s64, 0x80
	s_cmpk_lg_i32 s6, 0x2000
	s_cselect_b32 s6, s7, 0x88
	s_add_u32 s6, s0, s6
	s_addc_u32 s7, s1, 0
	s_ashr_i32 s15, s4, 31
	s_lshr_b32 s15, s15, 20
	s_add_i32 s15, s4, s15
	s_and_b32 s15, s15, 0xf000
	s_sub_i32 s4, s4, s15
	s_sext_i32_i16 s15, s4
	s_lshr_b32 s15, s15, 15
	s_bfe_u32 s16, s15, 0x4000c
	s_add_i32 s16, s4, s16
	s_and_b32 s16, s16, 0xfff0
	s_bfe_u32 s15, s15, 0x80008
	s_sub_i32 s16, s4, s16
	s_add_i32 s15, s4, s15
	s_sext_i32_i16 s18, s16
	s_sext_i32_i16 s16, s15
	s_and_b32 s15, s15, 0xff00
	s_load_dwordx2 s[6:7], s[6:7], 0x0
	s_ashr_i32 s16, s16, 8
	s_sub_i32 s4, s4, s15
	s_sext_i32_i16 s15, s4
	s_add_i32 s16, s16, 16
	s_bfe_u32 s15, s15, 0x4001b
	s_and_b32 s52, s16, 0xffff
	s_add_i32 s4, s4, s15
	s_lshl_b64 s[16:17], s[52:53], 24
	s_waitcnt lgkmcnt(0)
	s_add_u32 s15, s6, s16
	s_sext_i32_i16 s4, s4
	s_addc_u32 s16, s7, s17
	v_mov_b32_e32 v1, v0
	s_lshl_b32 s6, s18, 7
	s_lshl_b32 s4, s4, 3
	v_ashrrev_i32_e32 v2, 3, v1
	s_ashr_i32 s7, s6, 31
	s_and_b32 s4, s4, 0xffffff80
	v_and_b32_e32 v2, -4, v2
	s_lshl_b64 s[6:7], s[6:7], 2
	s_waitcnt vmcnt(0)
	v_add_u32_e32 v4, s4, v2
	s_add_u32 s6, s15, s6
	v_lshlrev_b32_e32 v1, 4, v1
	s_addc_u32 s7, s16, s7
	v_and_b32_e32 v2, 0x1f0, v1
	v_ashrrev_i32_e32 v5, 31, v4
	v_lshl_add_u64 v[6:7], s[6:7], 0, v[2:3]
	v_lshlrev_b64 v[8:9], 13, v[4:5]
	v_lshl_add_u64 v[12:13], v[6:7], 0, v[8:9]
	v_or_b32_e32 v8, 1, v4
	v_ashrrev_i32_e32 v9, 31, v8
	v_lshlrev_b64 v[8:9], 13, v[8:9]
	v_lshl_add_u64 v[8:9], v[6:7], 0, v[8:9]
	global_load_dwordx4 v[20:23], v[12:13], off nt
	global_load_dwordx4 v[24:27], v[8:9], off nt
	v_or_b32_e32 v8, 2, v4
	v_or_b32_e32 v4, 3, v4
	v_ashrrev_i32_e32 v9, 31, v8
	v_ashrrev_i32_e32 v5, 31, v4
	v_lshlrev_b64 v[8:9], 13, v[8:9]
	v_lshlrev_b64 v[4:5], 13, v[4:5]
	v_lshl_add_u64 v[8:9], v[6:7], 0, v[8:9]
	v_lshl_add_u64 v[4:5], v[6:7], 0, v[4:5]
	global_load_dwordx4 v[28:31], v[8:9], off nt
	global_load_dwordx4 v[32:35], v[4:5], off nt
	v_add_co_u32_e32 v4, vcc, s94, v12
	s_mov_b32 s19, 0x82000
	s_nop 0
	v_addc_co_u32_e32 v5, vcc, 0, v13, vcc
	v_add_co_u32_e32 v8, vcc, s19, v12
	s_mov_b32 s4, 0x84000
	s_nop 0
	v_addc_co_u32_e32 v9, vcc, 0, v13, vcc
	v_add_co_u32_e32 v14, vcc, s4, v12
	s_mov_b32 s4, 0x86000
	s_nop 0
	v_addc_co_u32_e32 v15, vcc, 0, v13, vcc
	v_add_co_u32_e32 v16, vcc, s4, v12
	s_add_i32 s4, s5, 0x4f0
	s_and_b32 s6, s4, 0xfffff000
	s_add_i32 s7, s5, 0x14ef
	s_cmpk_lt_u32 s7, 0x1fff
	s_cselect_b32 s7, s64, 0x80
	s_cmpk_lg_i32 s6, 0x2000
	s_cselect_b32 s6, s7, 0x88
	s_add_u32 s6, s0, s6
	s_addc_u32 s7, s1, 0
	s_ashr_i32 s15, s4, 31
	s_lshr_b32 s15, s15, 20
	s_add_i32 s15, s4, s15
	s_and_b32 s15, s15, 0xf000
	s_sub_i32 s4, s4, s15
	s_sext_i32_i16 s15, s4
	s_lshr_b32 s15, s15, 15
	s_bfe_u32 s16, s15, 0x4000c
	s_add_i32 s16, s4, s16
	s_and_b32 s16, s16, 0xfff0
	s_bfe_u32 s15, s15, 0x80008
	v_addc_co_u32_e32 v17, vcc, 0, v13, vcc
	s_sub_i32 s16, s4, s16
	s_add_i32 s15, s4, s15
	global_load_dwordx4 v[4:7], v[4:5], off nt
	s_nop 0
	global_load_dwordx4 v[8:11], v[8:9], off nt
	s_nop 0
	global_load_dwordx4 v[12:15], v[14:15], off nt
	s_nop 0
	global_load_dwordx4 v[16:19], v[16:17], off nt
	s_sext_i32_i16 s18, s16
	s_sext_i32_i16 s16, s15
	s_and_b32 s15, s15, 0xff00
	s_load_dwordx2 s[6:7], s[6:7], 0x0
	s_ashr_i32 s16, s16, 8
	s_sub_i32 s4, s4, s15
	s_sext_i32_i16 s15, s4
	s_add_i32 s16, s16, 16
	s_bfe_u32 s15, s15, 0x4001b
	s_and_b32 s52, s16, 0xffff
	s_add_i32 s4, s4, s15
	s_lshl_b64 s[16:17], s[52:53], 24
	s_waitcnt lgkmcnt(0)
	s_add_u32 s15, s6, s16
	s_sext_i32_i16 s4, s4
	s_addc_u32 s16, s7, s17
	v_mov_b32_e32 v1, v0
	s_lshl_b32 s6, s18, 7
	s_lshl_b32 s4, s4, 3
	v_ashrrev_i32_e32 v2, 3, v1
	s_ashr_i32 s7, s6, 31
	s_and_b32 s4, s4, 0xffffff80
	v_and_b32_e32 v2, -4, v2
	s_lshl_b64 s[6:7], s[6:7], 2
	v_add_u32_e32 v44, s4, v2
	s_add_u32 s6, s15, s6
	v_lshlrev_b32_e32 v1, 4, v1
	s_addc_u32 s7, s16, s7
	v_and_b32_e32 v2, 0x1f0, v1
	v_ashrrev_i32_e32 v45, 31, v44
	v_lshl_add_u64 v[46:47], s[6:7], 0, v[2:3]
	v_lshlrev_b64 v[36:37], 13, v[44:45]
	v_lshl_add_u64 v[48:49], v[46:47], 0, v[36:37]
	v_or_b32_e32 v36, 1, v44
	v_or_b32_e32 v50, 2, v44
	v_or_b32_e32 v44, 3, v44
	v_ashrrev_i32_e32 v37, 31, v36
	v_ashrrev_i32_e32 v51, 31, v50
	v_ashrrev_i32_e32 v45, 31, v44
	v_lshlrev_b64 v[36:37], 13, v[36:37]
	v_lshlrev_b64 v[50:51], 13, v[50:51]
	v_lshlrev_b64 v[44:45], 13, v[44:45]
	v_lshl_add_u64 v[40:41], v[46:47], 0, v[36:37]
	v_lshl_add_u64 v[50:51], v[46:47], 0, v[50:51]
	v_lshl_add_u64 v[44:45], v[46:47], 0, v[44:45]
	global_load_dwordx4 v[36:39], v[48:49], off nt
	s_nop 0
	global_load_dwordx4 v[40:43], v[40:41], off nt
	s_nop 0
	global_load_dwordx4 v[72:75], v[50:51], off nt
	global_load_dwordx4 v[76:79], v[44:45], off nt
	v_add_co_u32_e32 v44, vcc, s94, v48
	s_mov_b32 s4, 0
	s_nop 0
	v_addc_co_u32_e32 v45, vcc, 0, v49, vcc
	v_add_co_u32_e32 v46, vcc, s19, v48
	s_addk_i32 s5, 0x1567
	s_nop 0
	v_addc_co_u32_e32 v47, vcc, 0, v49, vcc
	global_load_dwordx4 v[84:87], v[44:45], off nt
	global_load_dwordx4 v[88:91], v[46:47], off nt
	v_add_co_u32_e32 v44, vcc, 0x84000, v48
	s_nop 1
	v_addc_co_u32_e32 v45, vcc, 0, v49, vcc
	v_add_co_u32_e32 v46, vcc, 0x86000, v48
	s_nop 1
	v_addc_co_u32_e32 v47, vcc, 0, v49, vcc
	global_load_dwordx4 v[92:95], v[44:45], off nt
	global_load_dwordx4 v[96:99], v[46:47], off nt
	s_waitcnt vmcnt(8)
	s_branch .LBB0_318
; DEVI int opaque_tid() { int t = threadIdx.x; asm volatile("" : "+v"(t)); return t; }
; DEVI unsigned cvt4_fp8(float a, float b, float c, float d) { int w = 0; w = __builtin_amdgcn_cvt_pk_fp8_f32(a, b, w, false); w = __builtin_amdgcn_cvt_pk_fp8_f32(c, d, w, true); return (unsigned)w; }
; DEVI void cvt8_finish(const Params& p, int L, int t, const CvtIn& in, char* smem) {
;     const int which = t / 4096, r = t % 4096, le = L * 16 + r / 256, kt = (r % 256) / 16, nt = r % 16;
;     unsigned char* dst = (which == 2) ? (unsigned char*)(p.ws + WS_WDN) + (size_t)le * 2048 * 2048 + (size_t)(nt * 128) * 2048
;                                       : (unsigned char*)(p.ws + WS_WGU) + (size_t)le * 4096 * 2048 + (size_t)(nt * 256 + which * 128) * 2048;
;     unsigned char* T = (unsigned char*)smem;
;     const int tid = opaque_tid(), nq = tid & 31, kq0 = tid >> 5;
; #pragma unroll
;     for (int it = 0; it < 2; ++it) { const int kq = kq0 + it * 16;
; #pragma unroll
;         for (int j = 0; j < 4; ++j) *(unsigned*)(T + (nq * 4 + j) * 144 + kq * 4) =
;             cvt4_fp8(in.v[it * 4][j] * W8_SCALE, in.v[it * 4 + 1][j] * W8_SCALE, in.v[it * 4 + 2][j] * W8_SCALE, in.v[it * 4 + 3][j] * W8_SCALE); }
;     __syncthreads();
; #pragma unroll
;     for (int i = 0; i < 2; ++i) { const int nl = (tid >> 3) + 64 * i, kc = (tid & 7) * 16;
;         *(u32x4*)(dst + (size_t)nl * 2048 + kt * 128 + kc) = *(const u32x4*)(T + nl * 144 + kc); }
;     __syncthreads();
; }
.LBB0_317:
	v_mul_f32_e32 v20, 0x42800000, v20
	v_mul_f32_e32 v24, 0x42800000, v24
	v_mov_b32_e32 v101, v3
	v_cvt_pk_fp8_f32 v101, v20, v24
	v_mul_f32_e32 v24, 0x42800000, v28
	v_mul_f32_e32 v28, 0x42800000, v32
	v_mov_b32_e32 v1, v0
	v_cvt_pk_fp8_f32 v101, v24, v28 op_sel:[0,0,1]
	v_mul_f32_e32 v21, 0x42800000, v21
	v_mul_f32_e32 v24, 0x42800000, v25
	v_mov_b32_e32 v25, v3
	v_cvt_pk_fp8_f32 v25, v21, v24
	v_lshlrev_b32_e32 v2, 2, v1
	v_and_b32_e32 v2, 0x7c, v2
	v_ashrrev_i32_e32 v100, 3, v1
	v_and_b32_e32 v20, -4, v100
	v_mul_u32_u24_e32 v2, 0x90, v2
	v_add3_u32 v2, 0, v20, v2
	v_mul_f32_e32 v20, 0x42800000, v29
	v_mul_f32_e32 v21, 0x42800000, v33
	v_cvt_pk_fp8_f32 v25, v20, v21 op_sel:[0,0,1]
	v_mul_f32_e32 v20, 0x42800000, v22
	v_mul_f32_e32 v21, 0x42800000, v26
	v_mov_b32_e32 v26, v3
	v_cvt_pk_fp8_f32 v26, v20, v21
	v_mul_f32_e32 v20, 0x42800000, v23
	v_mul_f32_e32 v21, 0x42800000, v27
	v_mov_b32_e32 v23, v3
	v_cvt_pk_fp8_f32 v23, v20, v21
	v_mul_f32_e32 v20, 0x42800000, v31
	v_mul_f32_e32 v21, 0x42800000, v35
	v_mul_f32_e32 v4, 0x42800000, v4
	v_cvt_pk_fp8_f32 v23, v20, v21 op_sel:[0,0,1]
	v_mul_f32_e32 v8, 0x42800000, v8
	v_mov_b32_e32 v20, v3
	v_cvt_pk_fp8_f32 v20, v4, v8
	v_mul_f32_e32 v4, 0x42800000, v5
	v_mul_f32_e32 v5, 0x42800000, v9
	v_mov_b32_e32 v8, v3
	v_cvt_pk_fp8_f32 v8, v4, v5
	s_lshl_b32 s7, s7, 8
	v_mul_f32_e32 v4, 0x42800000, v13
	v_mul_f32_e32 v5, 0x42800000, v17
	s_sub_i32 s6, s6, s7
	v_cvt_pk_fp8_f32 v8, v4, v5 op_sel:[0,0,1]
	v_mul_f32_e32 v4, 0x42800000, v6
	v_mul_f32_e32 v5, 0x42800000, v10
	v_mov_b32_e32 v10, v3
	s_sext_i32_i16 s7, s6
	v_cvt_pk_fp8_f32 v10, v4, v5
	v_mul_f32_e32 v4, 0x42800000, v7
	v_mul_f32_e32 v5, 0x42800000, v11
	v_mov_b32_e32 v7, v3
	s_bfe_u32 s7, s7, 0x4001b
	v_mul_f32_e32 v12, 0x42800000, v12
	v_mul_f32_e32 v16, 0x42800000, v16
	v_cvt_pk_fp8_f32 v7, v4, v5
	s_add_i32 s6, s6, s7
	v_cvt_pk_fp8_f32 v20, v12, v16 op_sel:[0,0,1]
	s_sext_i32_i16 s6, s6
	v_mul_f32_e32 v22, 0x42800000, v30
	v_mul_f32_e32 v24, 0x42800000, v34
	v_mul_f32_e32 v6, 0x42800000, v14
	v_mul_f32_e32 v9, 0x42800000, v18
	v_cvt_pk_fp8_f32 v26, v22, v24 op_sel:[0,0,1]
	v_cvt_pk_fp8_f32 v10, v6, v9 op_sel:[0,0,1]
	v_mul_f32_e32 v4, 0x42800000, v15
	v_mul_f32_e32 v5, 0x42800000, v19
	s_lshl_b32 s6, s6, 3
	v_cvt_pk_fp8_f32 v7, v4, v5 op_sel:[0,0,1]
	v_lshlrev_b32_e32 v1, 4, v1
	s_and_b32 s6, s6, 0xffffff80
	ds_write2_b32 v2, v101, v20 offset1:16
	ds_write2_b32 v2, v25, v8 offset0:36 offset1:52
	ds_write2_b32 v2, v26, v10 offset0:72 offset1:88
	ds_write2_b32 v2, v23, v7 offset0:108 offset1:124
	v_and_b32_e32 v2, 0x70, v1
	s_ashr_i32 s7, s6, 31
	v_mul_lo_u32 v1, v100, s91
	s_add_u32 s6, s16, s6
	v_add3_u32 v1, 0, v2, v1
	s_waitcnt lgkmcnt(0)
	s_barrier
	s_addc_u32 s7, s17, s7
	ds_read_b128 v[4:7], v1
	v_ashrrev_i32_e32 v101, 31, v100
	v_lshl_add_u64 v[8:9], s[6:7], 0, v[2:3]
	v_lshlrev_b64 v[10:11], 11, v[100:101]
	v_lshl_add_u64 v[12:13], v[8:9], 0, v[10:11]
	ds_read_b128 v[8:11], v1 offset:9216
	s_waitcnt lgkmcnt(1)
	global_store_dwordx4 v[12:13], v[4:7], off
	s_add_i32 s4, s4, 1
	s_addk_i32 s5, 0x78
	v_add_co_u32_e32 v4, vcc, 0x20000, v12
	s_nop 0
	v_addc_co_u32_e32 v5, vcc, 0, v13, vcc
	s_waitcnt lgkmcnt(0)
	global_store_dwordx4 v[4:5], v[8:11], off
	s_cmp_lg_u32 s4, 18
	s_cbranch_scc1 .Lstrm0_cont
	s_barrier
	s_branch .LBB0_324
.Lstrm0_cont:
	s_cmp_gt_u32 s4, 16
	s_cbranch_scc1 .Lstrm0_w2
	s_waitcnt vmcnt(10)
	s_branch .Lstrm0_wd

; DEVI void cvt8_stream3(const Params& p, int L, int t0, int step, int count, char* smem) {
;     ...
;     for (int i = 0; i < count; ++i) { CvtIn c;
;         if (i + 2 < count) cvt8_load(p, L, t0 + (i + 2) * step, c);
;         cvt8_finish(p, L, t0 + i * step, a, smem);
;         a = b; b = c; }
.Lstrm0_wd:
	s_bitcmp1_b32 s4, 0
	s_cbranch_scc1 .Lstrm0_cc
	v_mov_b64_e32 v[20:21], v[80:81]
	v_mov_b64_e32 v[24:25], v[68:69]
	v_mov_b64_e32 v[28:29], v[64:65]
	v_mov_b64_e32 v[32:33], v[60:61]
	v_mov_b64_e32 v[4:5], v[56:57]
	v_mov_b64_e32 v[8:9], v[52:53]
	v_mov_b64_e32 v[12:13], v[48:49]
	v_mov_b64_e32 v[16:17], v[44:45]
	v_mov_b64_e32 v[22:23], v[82:83]
	v_mov_b64_e32 v[26:27], v[70:71]
	v_mov_b64_e32 v[30:31], v[66:67]
	v_mov_b64_e32 v[34:35], v[62:63]
	v_mov_b64_e32 v[6:7], v[58:59]
	v_mov_b64_e32 v[10:11], v[54:55]
	v_mov_b64_e32 v[14:15], v[50:51]
	v_mov_b64_e32 v[18:19], v[46:47]
	s_branch .Lstrm0_cd
.Lstrm0_cc:
	v_mov_b64_e32 v[4:5], v[84:85]
	v_mov_b64_e32 v[6:7], v[86:87]
	v_mov_b64_e32 v[8:9], v[88:89]
	v_mov_b64_e32 v[10:11], v[90:91]
	v_mov_b64_e32 v[12:13], v[92:93]
	v_mov_b64_e32 v[14:15], v[94:95]
	v_mov_b64_e32 v[16:17], v[96:97]
	v_mov_b64_e32 v[18:19], v[98:99]
	v_mov_b64_e32 v[20:21], v[36:37]
	v_mov_b64_e32 v[22:23], v[38:39]
	v_mov_b64_e32 v[24:25], v[40:41]
	v_mov_b64_e32 v[26:27], v[42:43]
	v_mov_b64_e32 v[28:29], v[72:73]
	v_mov_b64_e32 v[30:31], v[74:75]
	v_mov_b64_e32 v[32:33], v[76:77]
	v_mov_b64_e32 v[34:35], v[78:79]

; DEVI int opaque_tid() { int t = threadIdx.x; asm volatile("" : "+v"(t)); return t; }
; DEVI void cvt8_load(const Params& p, int L, int t, CvtIn& in) {
;     const int which = t / 4096, r = t % 4096, le = L * 16 + r / 256, kt = (r % 256) / 16, nt = r % 16;
;     const float* src = (which == 2 ? p.w_down : (which == 0 ? p.w_gate : p.w_up)) + (size_t)le * 2048 * 2048;
;     const int tid = opaque_tid(), nq = tid & 31, kq0 = tid >> 5;
; #pragma unroll
;     for (int it = 0; it < 2; ++it)
; #pragma unroll
;         for (int kk = 0; kk < 4; ++kk) in.v[it * 4 + kk] = __builtin_nontemporal_load((const f32x4*)(src + (size_t)(kt * 128 + (kq0 + it * 16) * 4 + kk) * 2048 + nt * 128 + nq * 4));
; }
; DEVI void cvt8_stream3(const Params& p, int L, int t0, int step, int count, char* smem) {
;     ...
;     for (int i = 0; i < count; ++i) { CvtIn c;
;         if (i + 2 < count) cvt8_load(p, L, t0 + (i + 2) * step, c);
.LBB0_318:
	s_cmp_gt_u32 s4, 15
	s_cbranch_scc1 .LBB0_320
	s_bitcmp1_b32 s4, 0
	s_cbranch_scc0 .Lstrm0_lb
	s_add_i32 s15, s5, 0xfffff001
	s_and_b32 s6, s15, 0xfffff000
	s_cmpk_lt_u32 s5, 0x1fff
	s_cselect_b32 s7, s64, 0x80
	s_cmpk_lg_i32 s6, 0x2000
	s_cselect_b32 s6, s7, 0x88
	s_add_u32 s6, s0, s6
	s_addc_u32 s7, s1, 0
	s_ashr_i32 s16, s15, 31
	s_lshr_b32 s16, s16, 20
	s_add_i32 s16, s15, s16
	s_and_b32 s16, s16, 0xf000
	s_sub_i32 s15, s15, s16
	s_sext_i32_i16 s16, s15
	s_lshr_b32 s16, s16, 15
	s_bfe_u32 s17, s16, 0x4000c
	s_add_i32 s17, s15, s17
	s_and_b32 s17, s17, 0xfff0
	s_bfe_u32 s16, s16, 0x80008
	s_sub_i32 s17, s15, s17
	s_add_i32 s16, s15, s16
	s_sext_i32_i16 s18, s17
	s_sext_i32_i16 s17, s16
	s_and_b32 s16, s16, 0xff00
	s_load_dwordx2 s[6:7], s[6:7], 0x0
	s_ashr_i32 s17, s17, 8
	s_sub_i32 s15, s15, s16
	s_sext_i32_i16 s16, s15
	s_add_i32 s17, s17, 16
	s_bfe_u32 s16, s16, 0x4001b
	s_and_b32 s52, s17, 0xffff
	s_add_i32 s15, s15, s16
	s_lshl_b64 s[16:17], s[52:53], 24
	s_sext_i32_i16 s15, s15
	s_waitcnt lgkmcnt(0)
	s_add_u32 s16, s6, s16
	v_mov_b32_e32 v1, v0
	s_addc_u32 s17, s7, s17
	s_lshl_b32 s6, s15, 3
	v_ashrrev_i32_e32 v2, 3, v1
	s_and_b32 s6, s6, 0xffffff80
	v_and_b32_e32 v2, -4, v2
	v_add_u32_e32 v72, s6, v2
	s_lshl_b32 s6, s18, 7
	s_ashr_i32 s7, s6, 31
	s_lshl_b64 s[6:7], s[6:7], 2
	s_add_u32 s6, s16, s6
	v_lshlrev_b32_e32 v1, 4, v1
	s_addc_u32 s7, s17, s7
	v_and_b32_e32 v2, 0x1f0, v1
	v_ashrrev_i32_e32 v73, 31, v72
	v_lshl_add_u64 v[74:75], s[6:7], 0, v[2:3]
	v_lshlrev_b64 v[36:37], 13, v[72:73]
	v_lshl_add_u64 v[92:93], v[74:75], 0, v[36:37]
	v_add_co_u32_e32 v84, vcc, s94, v92
	v_or_b32_e32 v36, 1, v72
	s_nop 0
	v_addc_co_u32_e32 v85, vcc, 0, v93, vcc
	v_add_co_u32_e32 v88, vcc, 0x82000, v92
	v_or_b32_e32 v76, 2, v72
	s_nop 0
	v_addc_co_u32_e32 v89, vcc, 0, v93, vcc
	v_or_b32_e32 v72, 3, v72
	v_add_co_u32_e32 v94, vcc, 0x84000, v92
	v_ashrrev_i32_e32 v37, 31, v36
	v_ashrrev_i32_e32 v77, 31, v76
	v_ashrrev_i32_e32 v73, 31, v72
	v_addc_co_u32_e32 v95, vcc, 0, v93, vcc
	v_lshlrev_b64 v[36:37], 13, v[36:37]
	v_lshlrev_b64 v[76:77], 13, v[76:77]
	v_lshlrev_b64 v[72:73], 13, v[72:73]
	v_add_co_u32_e32 v96, vcc, 0x86000, v92
	v_lshl_add_u64 v[40:41], v[74:75], 0, v[36:37]
	v_lshl_add_u64 v[76:77], v[74:75], 0, v[76:77]
	v_lshl_add_u64 v[78:79], v[74:75], 0, v[72:73]
	v_addc_co_u32_e32 v97, vcc, 0, v93, vcc
	global_load_dwordx4 v[36:39], v[92:93], off nt
	s_nop 0
	global_load_dwordx4 v[40:43], v[40:41], off nt
	s_nop 0
	global_load_dwordx4 v[72:75], v[76:77], off nt
	s_nop 0
	global_load_dwordx4 v[76:79], v[78:79], off nt
	s_nop 0
	global_load_dwordx4 v[84:87], v[84:85], off nt
	s_nop 0
	global_load_dwordx4 v[88:91], v[88:89], off nt
	s_nop 0
	global_load_dwordx4 v[92:95], v[94:95], off nt
	s_nop 0
	global_load_dwordx4 v[96:99], v[96:97], off nt
	s_branch .LBB0_320
.Lstrm0_lb:
	s_add_i32 s15, s5, 0xfffff001
	s_and_b32 s6, s15, 0xfffff000
	s_cmpk_lt_u32 s5, 0x1fff
	s_cselect_b32 s7, s64, 0x80
	s_cmpk_lg_i32 s6, 0x2000
	s_cselect_b32 s6, s7, 0x88
	s_add_u32 s6, s0, s6
	s_addc_u32 s7, s1, 0
	s_ashr_i32 s16, s15, 31
	s_lshr_b32 s16, s16, 20
	s_add_i32 s16, s15, s16
	s_and_b32 s16, s16, 0xf000
	s_sub_i32 s15, s15, s16
	s_sext_i32_i16 s16, s15
	s_lshr_b32 s16, s16, 15
	s_bfe_u32 s17, s16, 0x4000c
	s_add_i32 s17, s15, s17
	s_and_b32 s17, s17, 0xfff0
	s_bfe_u32 s16, s16, 0x80008
	s_sub_i32 s17, s15, s17
	s_add_i32 s16, s15, s16
	s_sext_i32_i16 s18, s17
	s_sext_i32_i16 s17, s16
	s_and_b32 s16, s16, 0xff00
	s_load_dwordx2 s[6:7], s[6:7], 0x0
	s_ashr_i32 s17, s17, 8
	s_sub_i32 s15, s15, s16
	s_sext_i32_i16 s16, s15
	s_add_i32 s17, s17, 16
	s_bfe_u32 s16, s16, 0x4001b
	s_and_b32 s52, s17, 0xffff
	s_add_i32 s15, s15, s16
	s_lshl_b64 s[16:17], s[52:53], 24
	s_sext_i32_i16 s15, s15
	s_waitcnt lgkmcnt(0)
	s_add_u32 s16, s6, s16
	v_mov_b32_e32 v1, v0
	s_addc_u32 s17, s7, s17
	s_lshl_b32 s6, s15, 3
	v_ashrrev_i32_e32 v2, 3, v1
	s_and_b32 s6, s6, 0xffffff80
	v_and_b32_e32 v2, -4, v2
	v_add_u32_e32 v64, s6, v2
	s_lshl_b32 s6, s18, 7
	s_ashr_i32 s7, s6, 31
	s_lshl_b64 s[6:7], s[6:7], 2
	s_add_u32 s6, s16, s6
	v_lshlrev_b32_e32 v1, 4, v1
	s_addc_u32 s7, s17, s7
	v_and_b32_e32 v2, 0x1f0, v1
	v_ashrrev_i32_e32 v65, 31, v64
	v_lshl_add_u64 v[66:67], s[6:7], 0, v[2:3]
	v_lshlrev_b64 v[80:81], 13, v[64:65]
	v_lshl_add_u64 v[48:49], v[66:67], 0, v[80:81]
	v_add_co_u32_e32 v56, vcc, s94, v48
	v_or_b32_e32 v80, 1, v64
	s_nop 0
	v_addc_co_u32_e32 v57, vcc, 0, v49, vcc
	v_add_co_u32_e32 v52, vcc, 0x82000, v48
	v_or_b32_e32 v60, 2, v64
	s_nop 0
	v_addc_co_u32_e32 v53, vcc, 0, v49, vcc
	v_or_b32_e32 v64, 3, v64
	v_add_co_u32_e32 v50, vcc, 0x84000, v48
	v_ashrrev_i32_e32 v81, 31, v80
	v_ashrrev_i32_e32 v61, 31, v60
	v_ashrrev_i32_e32 v65, 31, v64
	v_addc_co_u32_e32 v51, vcc, 0, v49, vcc
	v_lshlrev_b64 v[80:81], 13, v[80:81]
	v_lshlrev_b64 v[60:61], 13, v[60:61]
	v_lshlrev_b64 v[64:65], 13, v[64:65]
	v_add_co_u32_e32 v44, vcc, 0x86000, v48
	v_lshl_add_u64 v[68:69], v[66:67], 0, v[80:81]
	v_lshl_add_u64 v[60:61], v[66:67], 0, v[60:61]
	v_lshl_add_u64 v[62:63], v[66:67], 0, v[64:65]
	v_addc_co_u32_e32 v45, vcc, 0, v49, vcc
	global_load_dwordx4 v[80:83], v[48:49], off nt
	s_nop 0
	global_load_dwordx4 v[68:71], v[68:69], off nt
	s_nop 0
	global_load_dwordx4 v[64:67], v[60:61], off nt
	s_nop 0
	global_load_dwordx4 v[60:63], v[62:63], off nt
	s_nop 0
	global_load_dwordx4 v[56:59], v[56:57], off nt
	s_nop 0
	global_load_dwordx4 v[52:55], v[52:53], off nt
	s_nop 0
	global_load_dwordx4 v[48:51], v[50:51], off nt
	s_nop 0
	global_load_dwordx4 v[44:47], v[44:45], off nt

; DEVI int opaque_tid() { int t = threadIdx.x; asm volatile("" : "+v"(t)); return t; }
; DEVI void cvt8_load(const Params& p, int L, int t, CvtIn& in) {
;     const int which = t / 4096, r = t % 4096, le = L * 16 + r / 256, kt = (r % 256) / 16, nt = r % 16;
;     const float* src = (which == 2 ? p.w_down : (which == 0 ? p.w_gate : p.w_up)) + (size_t)le * 2048 * 2048;
;     const int tid = opaque_tid(), nq = tid & 31, kq0 = tid >> 5;
; #pragma unroll
;     for (int it = 0; it < 2; ++it)
; #pragma unroll
;         for (int kk = 0; kk < 4; ++kk) in.v[it * 4 + kk] = __builtin_nontemporal_load((const f32x4*)(src + (size_t)(kt * 128 + (kq0 + it * 16) * 4 + kk) * 2048 + nt * 128 + nq * 4));
; }
; DEVI void cvt8_stream3(const Params& p, int L, int t0, int step, int count, char* smem) {
;     if (count <= 0) return;
;     CvtIn a, b; cvt8_load(p, L, t0, a);
;     if (count > 1) cvt8_load(p, L, t0 + step, b);
.LBB0_326:
	s_andn2_b64 vcc, exec, s[16:17]
	s_cbranch_vccnz .LBB0_338
	s_and_b64 vcc, exec, s[38:39]
	s_cbranch_vccnz .LBB0_338
	s_mov_b32 s4, s2
	s_cmpk_lt_i32 s4, 0x88
	v_readlane_b32 s4, v254, 61
	v_readlane_b32 s5, v254, 62
	s_cbranch_scc1 .LBB0_338
	s_mov_b32 s5, s2
	s_add_i32 s4, s5, 0xffffff78
	s_and_b32 s6, s4, 0xfffff000
	s_add_i32 s7, s5, 0xf77
	s_cmpk_lt_u32 s7, 0x1fff
	s_cselect_b32 s7, s64, 0x80
	s_cmpk_lg_i32 s6, 0x2000
	s_cselect_b32 s6, s7, 0x88
	s_add_u32 s6, s0, s6
	s_addc_u32 s7, s1, 0
	s_ashr_i32 s15, s4, 31
	s_lshr_b32 s15, s15, 20
	s_add_i32 s15, s4, s15
	s_and_b32 s15, s15, 0xf000
	s_sub_i32 s15, s4, s15
	s_sext_i32_i16 s16, s15
	s_lshr_b32 s16, s16, 15
	s_bfe_u32 s17, s16, 0x4000c
	s_add_i32 s17, s15, s17
	s_and_b32 s17, s17, 0xfff0
	s_sub_i32 s17, s15, s17
	s_bfe_u32 s16, s16, 0x80008
	s_sext_i32_i16 s18, s17
	s_add_i32 s17, s15, s16
	s_sext_i32_i16 s16, s17
	s_and_b32 s17, s17, 0xff00
	s_sub_i32 s15, s15, s17
	s_load_dwordx2 s[6:7], s[6:7], 0x0
	s_sext_i32_i16 s17, s15
	s_lshr_b32 s16, s16, 8
	s_bfe_u32 s17, s17, 0x4001b
	s_add_i32 s15, s15, s17
	s_bfe_i64 s[16:17], s[16:17], 0x100000
	s_lshl_b64 s[16:17], s[16:17], 24
	s_sext_i32_i16 s15, s15
	s_waitcnt lgkmcnt(0)
	s_add_u32 s16, s6, s16
	v_mov_b32_e32 v1, v0
	s_addc_u32 s17, s7, s17
	s_lshl_b32 s6, s15, 3
	v_ashrrev_i32_e32 v2, 3, v1
	s_and_b32 s6, s6, 0xffffff80
	v_and_b32_e32 v2, -4, v2
	s_waitcnt vmcnt(0)
	v_add_u32_e32 v4, s6, v2
	s_lshl_b32 s6, s18, 7
	s_ashr_i32 s7, s6, 31
	s_lshl_b64 s[6:7], s[6:7], 2
	s_add_u32 s6, s16, s6
	v_lshlrev_b32_e32 v1, 4, v1
	s_addc_u32 s7, s17, s7
	v_and_b32_e32 v2, 0x1f0, v1
	v_ashrrev_i32_e32 v5, 31, v4
	v_lshl_add_u64 v[6:7], s[6:7], 0, v[2:3]
	v_lshlrev_b64 v[8:9], 13, v[4:5]
	v_lshl_add_u64 v[12:13], v[6:7], 0, v[8:9]
	v_or_b32_e32 v8, 1, v4
	v_ashrrev_i32_e32 v9, 31, v8
	v_lshlrev_b64 v[8:9], 13, v[8:9]
	v_lshl_add_u64 v[8:9], v[6:7], 0, v[8:9]
	global_load_dwordx4 v[20:23], v[12:13], off nt
	global_load_dwordx4 v[24:27], v[8:9], off nt
	v_or_b32_e32 v8, 2, v4
	v_or_b32_e32 v4, 3, v4
	v_ashrrev_i32_e32 v9, 31, v8
	v_ashrrev_i32_e32 v5, 31, v4
	v_lshlrev_b64 v[8:9], 13, v[8:9]
	v_lshlrev_b64 v[4:5], 13, v[4:5]
	v_lshl_add_u64 v[8:9], v[6:7], 0, v[8:9]
	v_lshl_add_u64 v[4:5], v[6:7], 0, v[4:5]
	global_load_dwordx4 v[28:31], v[8:9], off nt
	global_load_dwordx4 v[32:35], v[4:5], off nt
	v_add_co_u32_e32 v4, vcc, s94, v12
	s_mov_b32 s6, 0x82000
	s_nop 0
	v_addc_co_u32_e32 v5, vcc, 0, v13, vcc
	v_add_co_u32_e32 v8, vcc, s6, v12
	s_mov_b32 s6, 0x84000
	s_nop 0
	v_addc_co_u32_e32 v9, vcc, 0, v13, vcc
	v_add_co_u32_e32 v14, vcc, s6, v12
	s_mov_b32 s6, 0x86000
	s_nop 0
	v_addc_co_u32_e32 v15, vcc, 0, v13, vcc
	s_add_i32 s15, s5, -16
	v_add_co_u32_e32 v16, vcc, s6, v12
	s_and_b32 s6, s15, 0xfffff000
	s_addk_i32 s5, 0xfef
	s_cmpk_lt_u32 s5, 0x1fff
	s_cselect_b32 s5, s64, 0x80
	s_cmpk_lg_i32 s6, 0x2000
	s_cselect_b32 s5, s5, 0x88
	s_add_u32 s6, s0, s5
	s_addc_u32 s7, s1, 0
	s_ashr_i32 s5, s15, 31
	s_lshr_b32 s5, s5, 20
	s_add_i32 s5, s15, s5
	s_and_b32 s5, s5, 0xf000
	s_sub_i32 s5, s15, s5
	s_sext_i32_i16 s15, s5
	s_lshr_b32 s15, s15, 15
	s_bfe_u32 s16, s15, 0x4000c
	s_add_i32 s16, s5, s16
	s_and_b32 s16, s16, 0xfff0
	s_bfe_u32 s15, s15, 0x80008
	v_addc_co_u32_e32 v17, vcc, 0, v13, vcc
	s_sub_i32 s16, s5, s16
	s_add_i32 s15, s5, s15
	global_load_dwordx4 v[4:7], v[4:5], off nt
	s_nop 0
	global_load_dwordx4 v[8:11], v[8:9], off nt
	s_nop 0
	global_load_dwordx4 v[12:15], v[14:15], off nt
	s_nop 0
	global_load_dwordx4 v[16:19], v[16:17], off nt
	s_sext_i32_i16 s18, s16
	s_sext_i32_i16 s16, s15
	s_and_b32 s15, s15, 0xff00
	s_load_dwordx2 s[6:7], s[6:7], 0x0
	s_sub_i32 s5, s5, s15
	s_lshr_b32 s16, s16, 8
	s_sext_i32_i16 s15, s5
	s_bfe_u32 s15, s15, 0x4001b
	s_bfe_i64 s[16:17], s[16:17], 0x100000
	s_add_i32 s5, s5, s15
	s_lshl_b64 s[16:17], s[16:17], 24
	s_waitcnt lgkmcnt(0)
	s_add_u32 s15, s6, s16
	s_sext_i32_i16 s5, s5
	s_addc_u32 s16, s7, s17
	v_mov_b32_e32 v1, v0
	s_lshl_b32 s6, s18, 7
	s_lshl_b32 s5, s5, 3
	v_ashrrev_i32_e32 v2, 3, v1
	s_ashr_i32 s7, s6, 31
	s_and_b32 s5, s5, 0xffffff80
	v_and_b32_e32 v2, -4, v2
	s_lshl_b64 s[6:7], s[6:7], 2
	v_add_u32_e32 v44, s5, v2
	s_add_u32 s6, s15, s6
	v_lshlrev_b32_e32 v1, 4, v1
	s_addc_u32 s7, s16, s7
	v_and_b32_e32 v2, 0x1f0, v1
	v_ashrrev_i32_e32 v45, 31, v44
	v_lshl_add_u64 v[46:47], s[6:7], 0, v[2:3]
	s_waitcnt vmcnt(0)
	v_lshlrev_b64 v[36:37], 13, v[44:45]
	v_lshl_add_u64 v[48:49], v[46:47], 0, v[36:37]
	v_or_b32_e32 v36, 1, v44
	v_or_b32_e32 v50, 2, v44
	v_or_b32_e32 v44, 3, v44
	v_ashrrev_i32_e32 v37, 31, v36
	v_ashrrev_i32_e32 v51, 31, v50
	v_ashrrev_i32_e32 v45, 31, v44
	v_lshlrev_b64 v[36:37], 13, v[36:37]
	v_lshlrev_b64 v[50:51], 13, v[50:51]
	v_lshlrev_b64 v[44:45], 13, v[44:45]
	v_lshl_add_u64 v[40:41], v[46:47], 0, v[36:37]
	v_lshl_add_u64 v[50:51], v[46:47], 0, v[50:51]
	v_lshl_add_u64 v[44:45], v[46:47], 0, v[44:45]
	global_load_dwordx4 v[36:39], v[48:49], off nt
	s_nop 0
	global_load_dwordx4 v[40:43], v[40:41], off nt
	s_nop 0
	global_load_dwordx4 v[72:75], v[50:51], off nt
	global_load_dwordx4 v[76:79], v[44:45], off nt
	v_add_co_u32_e32 v44, vcc, s94, v48
	s_mov_b32 s5, 0
	s_nop 0
	v_addc_co_u32_e32 v45, vcc, 0, v49, vcc
	v_add_co_u32_e32 v46, vcc, 0x82000, v48
	s_nop 1
	v_addc_co_u32_e32 v47, vcc, 0, v49, vcc
	global_load_dwordx4 v[84:87], v[44:45], off nt
	global_load_dwordx4 v[88:91], v[46:47], off nt
	v_add_co_u32_e32 v44, vcc, 0x84000, v48
	s_nop 1
	v_addc_co_u32_e32 v45, vcc, 0, v49, vcc
	v_add_co_u32_e32 v46, vcc, 0x86000, v48
	s_nop 1
	v_addc_co_u32_e32 v47, vcc, 0, v49, vcc
	global_load_dwordx4 v[92:95], v[44:45], off nt
	global_load_dwordx4 v[96:99], v[46:47], off nt
	s_waitcnt vmcnt(8)
	s_branch .LBB0_331
; DEVI int opaque_tid() { int t = threadIdx.x; asm volatile("" : "+v"(t)); return t; }
; DEVI unsigned cvt4_fp8(float a, float b, float c, float d) { int w = 0; w = __builtin_amdgcn_cvt_pk_fp8_f32(a, b, w, false); w = __builtin_amdgcn_cvt_pk_fp8_f32(c, d, w, true); return (unsigned)w; }
; DEVI void cvt8_finish(const Params& p, int L, int t, const CvtIn& in, char* smem) {
;     const int which = t / 4096, r = t % 4096, le = L * 16 + r / 256, kt = (r % 256) / 16, nt = r % 16;
;     unsigned char* dst = (which == 2) ? (unsigned char*)(p.ws + WS_WDN) + (size_t)le * 2048 * 2048 + (size_t)(nt * 128) * 2048
;                                       : (unsigned char*)(p.ws + WS_WGU) + (size_t)le * 4096 * 2048 + (size_t)(nt * 256 + which * 128) * 2048;
;     unsigned char* T = (unsigned char*)smem;
;     const int tid = opaque_tid(), nq = tid & 31, kq0 = tid >> 5;
; #pragma unroll
;     for (int it = 0; it < 2; ++it) { const int kq = kq0 + it * 16;
; #pragma unroll
;         for (int j = 0; j < 4; ++j) *(unsigned*)(T + (nq * 4 + j) * 144 + kq * 4) =
;             cvt4_fp8(in.v[it * 4][j] * W8_SCALE, in.v[it * 4 + 1][j] * W8_SCALE, in.v[it * 4 + 2][j] * W8_SCALE, in.v[it * 4 + 3][j] * W8_SCALE); }
;     __syncthreads();
; #pragma unroll
;     for (int i = 0; i < 2; ++i) { const int nl = (tid >> 3) + 64 * i, kc = (tid & 7) * 16;
;         *(u32x4*)(dst + (size_t)nl * 2048 + kt * 128 + kc) = *(const u32x4*)(T + nl * 144 + kc); }
;     __syncthreads();
; }
.LBB0_330:
	v_mul_f32_e32 v20, 0x42800000, v20
	v_mul_f32_e32 v24, 0x42800000, v24
	v_mov_b32_e32 v101, v3
	v_cvt_pk_fp8_f32 v101, v20, v24
	v_mul_f32_e32 v24, 0x42800000, v28
	v_mul_f32_e32 v28, 0x42800000, v32
	v_mov_b32_e32 v1, v0
	v_cvt_pk_fp8_f32 v101, v24, v28 op_sel:[0,0,1]
	v_mul_f32_e32 v21, 0x42800000, v21
	v_mul_f32_e32 v24, 0x42800000, v25
	v_mov_b32_e32 v25, v3
	v_cvt_pk_fp8_f32 v25, v21, v24
	v_lshlrev_b32_e32 v2, 2, v1
	v_and_b32_e32 v2, 0x7c, v2
	v_ashrrev_i32_e32 v100, 3, v1
	v_and_b32_e32 v20, -4, v100
	v_mul_u32_u24_e32 v2, 0x90, v2
	v_add3_u32 v2, 0, v20, v2
	v_mul_f32_e32 v20, 0x42800000, v29
	v_mul_f32_e32 v21, 0x42800000, v33
	v_cvt_pk_fp8_f32 v25, v20, v21 op_sel:[0,0,1]
	v_mul_f32_e32 v20, 0x42800000, v22
	v_mul_f32_e32 v21, 0x42800000, v26
	v_mov_b32_e32 v26, v3
	v_cvt_pk_fp8_f32 v26, v20, v21
	v_mul_f32_e32 v20, 0x42800000, v23
	v_mul_f32_e32 v21, 0x42800000, v27
	v_mov_b32_e32 v23, v3
	v_cvt_pk_fp8_f32 v23, v20, v21
	v_mul_f32_e32 v20, 0x42800000, v31
	v_mul_f32_e32 v21, 0x42800000, v35
	v_mul_f32_e32 v4, 0x42800000, v4
	v_cvt_pk_fp8_f32 v23, v20, v21 op_sel:[0,0,1]
	v_mul_f32_e32 v8, 0x42800000, v8
	v_mov_b32_e32 v20, v3
	v_cvt_pk_fp8_f32 v20, v4, v8
	v_mul_f32_e32 v4, 0x42800000, v5
	v_mul_f32_e32 v5, 0x42800000, v9
	v_mov_b32_e32 v8, v3
	v_cvt_pk_fp8_f32 v8, v4, v5
	s_lshl_b32 s7, s7, 8
	v_mul_f32_e32 v4, 0x42800000, v13
	v_mul_f32_e32 v5, 0x42800000, v17
	s_sub_i32 s6, s6, s7
	v_cvt_pk_fp8_f32 v8, v4, v5 op_sel:[0,0,1]
	v_mul_f32_e32 v4, 0x42800000, v6
	v_mul_f32_e32 v5, 0x42800000, v10
	v_mov_b32_e32 v10, v3
	s_sext_i32_i16 s7, s6
	v_cvt_pk_fp8_f32 v10, v4, v5
	v_mul_f32_e32 v4, 0x42800000, v7
	v_mul_f32_e32 v5, 0x42800000, v11
	v_mov_b32_e32 v7, v3
	s_bfe_u32 s7, s7, 0x4001b
	v_mul_f32_e32 v12, 0x42800000, v12
	v_mul_f32_e32 v16, 0x42800000, v16
	v_cvt_pk_fp8_f32 v7, v4, v5
	s_add_i32 s6, s6, s7
	v_cvt_pk_fp8_f32 v20, v12, v16 op_sel:[0,0,1]
	s_sext_i32_i16 s6, s6
	v_mul_f32_e32 v22, 0x42800000, v30
	v_mul_f32_e32 v24, 0x42800000, v34
	v_mul_f32_e32 v6, 0x42800000, v14
	v_mul_f32_e32 v9, 0x42800000, v18
	v_cvt_pk_fp8_f32 v26, v22, v24 op_sel:[0,0,1]
	v_cvt_pk_fp8_f32 v10, v6, v9 op_sel:[0,0,1]
	v_mul_f32_e32 v4, 0x42800000, v15
	v_mul_f32_e32 v5, 0x42800000, v19
	s_lshl_b32 s6, s6, 3
	v_cvt_pk_fp8_f32 v7, v4, v5 op_sel:[0,0,1]
	v_lshlrev_b32_e32 v1, 4, v1
	s_and_b32 s6, s6, 0xffffff80
	ds_write2_b32 v2, v101, v20 offset1:16
	ds_write2_b32 v2, v25, v8 offset0:36 offset1:52
	ds_write2_b32 v2, v26, v10 offset0:72 offset1:88
	ds_write2_b32 v2, v23, v7 offset0:108 offset1:124
	v_and_b32_e32 v2, 0x70, v1
	s_ashr_i32 s7, s6, 31
	v_mul_lo_u32 v1, v100, s91
	s_add_u32 s6, s16, s6
	v_add3_u32 v1, 0, v2, v1
	s_waitcnt lgkmcnt(0)
	s_barrier
	s_addc_u32 s7, s17, s7
	ds_read_b128 v[4:7], v1
	v_ashrrev_i32_e32 v101, 31, v100
	v_lshl_add_u64 v[8:9], s[6:7], 0, v[2:3]
	v_lshlrev_b64 v[10:11], 11, v[100:101]
	v_lshl_add_u64 v[12:13], v[8:9], 0, v[10:11]
	ds_read_b128 v[8:11], v1 offset:9216
	s_waitcnt lgkmcnt(1)
	global_store_dwordx4 v[12:13], v[4:7], off
	s_add_i32 s5, s5, 1
	s_addk_i32 s4, 0x78
	v_add_co_u32_e32 v4, vcc, 0x20000, v12
	s_nop 0
	v_addc_co_u32_e32 v5, vcc, 0, v13, vcc
	s_waitcnt lgkmcnt(0)
	global_store_dwordx4 v[4:5], v[8:11], off
	s_cmp_eq_u32 s5, 18
	s_cbranch_scc0 .Lstrm1_cont
	s_barrier
	s_branch .LBB0_337
.Lstrm1_cont:
	s_cmp_gt_u32 s5, 16
	s_cbranch_scc1 .Lstrm1_w2
	s_waitcnt vmcnt(10)
	s_branch .Lstrm1_wd

; DEVI void cvt8_stream3(const Params& p, int L, int t0, int step, int count, char* smem) {
;     ...
;     for (int i = 0; i < count; ++i) { CvtIn c;
;         if (i + 2 < count) cvt8_load(p, L, t0 + (i + 2) * step, c);
;         cvt8_finish(p, L, t0 + i * step, a, smem);
;         a = b; b = c; }
.Lstrm1_wd:
	s_bitcmp1_b32 s5, 0
	s_cbranch_scc1 .Lstrm1_cc
	v_mov_b64_e32 v[20:21], v[80:81]
	v_mov_b64_e32 v[24:25], v[68:69]
	v_mov_b64_e32 v[28:29], v[64:65]
	v_mov_b64_e32 v[32:33], v[60:61]
	v_mov_b64_e32 v[4:5], v[56:57]
	v_mov_b64_e32 v[8:9], v[52:53]
	v_mov_b64_e32 v[12:13], v[48:49]
	v_mov_b64_e32 v[16:17], v[44:45]
	v_mov_b64_e32 v[22:23], v[82:83]
	v_mov_b64_e32 v[26:27], v[70:71]
	v_mov_b64_e32 v[30:31], v[66:67]
	v_mov_b64_e32 v[34:35], v[62:63]
	v_mov_b64_e32 v[6:7], v[58:59]
	v_mov_b64_e32 v[10:11], v[54:55]
	v_mov_b64_e32 v[14:15], v[50:51]
	v_mov_b64_e32 v[18:19], v[46:47]
	s_branch .Lstrm1_cd

; DEVI int opaque_tid() { int t = threadIdx.x; asm volatile("" : "+v"(t)); return t; }
; DEVI void cvt8_load(const Params& p, int L, int t, CvtIn& in) {
;     const int which = t / 4096, r = t % 4096, le = L * 16 + r / 256, kt = (r % 256) / 16, nt = r % 16;
;     const float* src = (which == 2 ? p.w_down : (which == 0 ? p.w_gate : p.w_up)) + (size_t)le * 2048 * 2048;
;     const int tid = opaque_tid(), nq = tid & 31, kq0 = tid >> 5;
; #pragma unroll
;     for (int it = 0; it < 2; ++it)
; #pragma unroll
;         for (int kk = 0; kk < 4; ++kk) in.v[it * 4 + kk] = __builtin_nontemporal_load((const f32x4*)(src + (size_t)(kt * 128 + (kq0 + it * 16) * 4 + kk) * 2048 + nt * 128 + nq * 4));
; }
; DEVI void cvt8_stream3(const Params& p, int L, int t0, int step, int count, char* smem) {
;     ...
;     for (int i = 0; i < count; ++i) { CvtIn c;
;         if (i + 2 < count) cvt8_load(p, L, t0 + (i + 2) * step, c);
.LBB0_331:
	s_cmp_gt_u32 s5, 15
	s_cbranch_scc1 .LBB0_333
	s_bitcmp1_b32 s5, 0
	s_cbranch_scc0 .Lstrm1_lb
	s_add_i32 s15, s4, 0xf0
	s_and_b32 s6, s15, 0xfffff000
	s_add_i32 s7, s4, 0x10ef
	s_cmpk_lt_u32 s7, 0x1fff
	s_cselect_b32 s7, s64, 0x80
	s_cmpk_lg_i32 s6, 0x2000
	s_cselect_b32 s6, s7, 0x88
	s_add_u32 s6, s0, s6
	s_addc_u32 s7, s1, 0
	s_ashr_i32 s16, s15, 31
	s_lshr_b32 s16, s16, 20
	s_add_i32 s16, s15, s16
	s_and_b32 s16, s16, 0xf000
	s_sub_i32 s15, s15, s16
	s_sext_i32_i16 s16, s15
	s_lshr_b32 s16, s16, 15
	s_bfe_u32 s17, s16, 0x4000c
	s_add_i32 s17, s15, s17
	s_and_b32 s17, s17, 0xfff0
	s_sub_i32 s17, s15, s17
	s_bfe_u32 s16, s16, 0x80008
	s_sext_i32_i16 s18, s17
	s_add_i32 s17, s15, s16
	s_sext_i32_i16 s16, s17
	s_and_b32 s17, s17, 0xff00
	s_sub_i32 s15, s15, s17
	s_load_dwordx2 s[6:7], s[6:7], 0x0
	s_sext_i32_i16 s17, s15
	s_lshr_b32 s16, s16, 8
	s_bfe_u32 s17, s17, 0x4001b
	s_add_i32 s15, s15, s17
	s_bfe_i64 s[16:17], s[16:17], 0x100000
	s_lshl_b64 s[16:17], s[16:17], 24
	s_sext_i32_i16 s15, s15
	s_waitcnt lgkmcnt(0)
	s_add_u32 s16, s6, s16
	v_mov_b32_e32 v1, v0
	s_addc_u32 s17, s7, s17
	s_lshl_b32 s6, s15, 3
	v_ashrrev_i32_e32 v2, 3, v1
	s_and_b32 s6, s6, 0xffffff80
	v_and_b32_e32 v2, -4, v2
	v_add_u32_e32 v72, s6, v2
	s_lshl_b32 s6, s18, 7
	s_ashr_i32 s7, s6, 31
	s_lshl_b64 s[6:7], s[6:7], 2
	s_add_u32 s6, s16, s6
	v_lshlrev_b32_e32 v1, 4, v1
	s_addc_u32 s7, s17, s7
	v_and_b32_e32 v2, 0x1f0, v1
	v_ashrrev_i32_e32 v73, 31, v72
	v_lshl_add_u64 v[74:75], s[6:7], 0, v[2:3]
	v_lshlrev_b64 v[36:37], 13, v[72:73]
	v_lshl_add_u64 v[92:93], v[74:75], 0, v[36:37]
	v_add_co_u32_e32 v84, vcc, s94, v92
	v_or_b32_e32 v36, 1, v72
	s_nop 0
	v_addc_co_u32_e32 v85, vcc, 0, v93, vcc
	v_add_co_u32_e32 v88, vcc, 0x82000, v92
	v_or_b32_e32 v76, 2, v72
	s_nop 0
	v_addc_co_u32_e32 v89, vcc, 0, v93, vcc
	v_or_b32_e32 v72, 3, v72
	v_add_co_u32_e32 v94, vcc, 0x84000, v92
	v_ashrrev_i32_e32 v37, 31, v36
	v_ashrrev_i32_e32 v77, 31, v76
	v_ashrrev_i32_e32 v73, 31, v72
	v_addc_co_u32_e32 v95, vcc, 0, v93, vcc
	v_lshlrev_b64 v[36:37], 13, v[36:37]
	v_lshlrev_b64 v[76:77], 13, v[76:77]
	v_lshlrev_b64 v[72:73], 13, v[72:73]
	v_add_co_u32_e32 v96, vcc, 0x86000, v92
	v_lshl_add_u64 v[40:41], v[74:75], 0, v[36:37]
	v_lshl_add_u64 v[76:77], v[74:75], 0, v[76:77]
	v_lshl_add_u64 v[78:79], v[74:75], 0, v[72:73]
	v_addc_co_u32_e32 v97, vcc, 0, v93, vcc
	global_load_dwordx4 v[36:39], v[92:93], off nt
	s_nop 0
	global_load_dwordx4 v[40:43], v[40:41], off nt
	s_nop 0
	global_load_dwordx4 v[72:75], v[76:77], off nt
	s_nop 0
	global_load_dwordx4 v[76:79], v[78:79], off nt
	s_nop 0
	global_load_dwordx4 v[84:87], v[84:85], off nt
	s_nop 0
	global_load_dwordx4 v[88:91], v[88:89], off nt
	s_nop 0
	global_load_dwordx4 v[92:95], v[94:95], off nt
	s_nop 0
	global_load_dwordx4 v[96:99], v[96:97], off nt
	s_branch .LBB0_333
.Lstrm1_lb:
	s_add_i32 s15, s4, 0xf0
	s_and_b32 s6, s15, 0xfffff000
	s_add_i32 s7, s4, 0x10ef
	s_cmpk_lt_u32 s7, 0x1fff
	s_cselect_b32 s7, s64, 0x80
	s_cmpk_lg_i32 s6, 0x2000
	s_cselect_b32 s6, s7, 0x88
	s_add_u32 s6, s0, s6
	s_addc_u32 s7, s1, 0
	s_ashr_i32 s16, s15, 31
	s_lshr_b32 s16, s16, 20
	s_add_i32 s16, s15, s16
	s_and_b32 s16, s16, 0xf000
	s_sub_i32 s15, s15, s16
	s_sext_i32_i16 s16, s15
	s_lshr_b32 s16, s16, 15
	s_bfe_u32 s17, s16, 0x4000c
	s_add_i32 s17, s15, s17
	s_and_b32 s17, s17, 0xfff0
	s_sub_i32 s17, s15, s17
	s_bfe_u32 s16, s16, 0x80008
	s_sext_i32_i16 s18, s17
	s_add_i32 s17, s15, s16
	s_sext_i32_i16 s16, s17
	s_and_b32 s17, s17, 0xff00
	s_sub_i32 s15, s15, s17
	s_load_dwordx2 s[6:7], s[6:7], 0x0
	s_sext_i32_i16 s17, s15
	s_lshr_b32 s16, s16, 8
	s_bfe_u32 s17, s17, 0x4001b
	s_add_i32 s15, s15, s17
	s_bfe_i64 s[16:17], s[16:17], 0x100000
	s_lshl_b64 s[16:17], s[16:17], 24
	s_sext_i32_i16 s15, s15
	s_waitcnt lgkmcnt(0)
	s_add_u32 s16, s6, s16
	v_mov_b32_e32 v1, v0
	s_addc_u32 s17, s7, s17
	s_lshl_b32 s6, s15, 3
	v_ashrrev_i32_e32 v2, 3, v1
	s_and_b32 s6, s6, 0xffffff80
	v_and_b32_e32 v2, -4, v2
	v_add_u32_e32 v64, s6, v2
	s_lshl_b32 s6, s18, 7
	s_ashr_i32 s7, s6, 31
	s_lshl_b64 s[6:7], s[6:7], 2
	s_add_u32 s6, s16, s6
	v_lshlrev_b32_e32 v1, 4, v1
	s_addc_u32 s7, s17, s7
	v_and_b32_e32 v2, 0x1f0, v1
	v_ashrrev_i32_e32 v65, 31, v64
	v_lshl_add_u64 v[66:67], s[6:7], 0, v[2:3]
	v_lshlrev_b64 v[80:81], 13, v[64:65]
	v_lshl_add_u64 v[48:49], v[66:67], 0, v[80:81]
	v_add_co_u32_e32 v56, vcc, s94, v48
	v_or_b32_e32 v80, 1, v64
	s_nop 0
	v_addc_co_u32_e32 v57, vcc, 0, v49, vcc
	v_add_co_u32_e32 v52, vcc, 0x82000, v48
	v_or_b32_e32 v60, 2, v64
	s_nop 0
	v_addc_co_u32_e32 v53, vcc, 0, v49, vcc
	v_or_b32_e32 v64, 3, v64
	v_add_co_u32_e32 v50, vcc, 0x84000, v48
	v_ashrrev_i32_e32 v81, 31, v80
	v_ashrrev_i32_e32 v61, 31, v60
	v_ashrrev_i32_e32 v65, 31, v64
	v_addc_co_u32_e32 v51, vcc, 0, v49, vcc
	v_lshlrev_b64 v[80:81], 13, v[80:81]
	v_lshlrev_b64 v[60:61], 13, v[60:61]
	v_lshlrev_b64 v[64:65], 13, v[64:65]
	v_add_co_u32_e32 v44, vcc, 0x86000, v48
	v_lshl_add_u64 v[68:69], v[66:67], 0, v[80:81]
	v_lshl_add_u64 v[60:61], v[66:67], 0, v[60:61]
	v_lshl_add_u64 v[62:63], v[66:67], 0, v[64:65]
	v_addc_co_u32_e32 v45, vcc, 0, v49, vcc
	global_load_dwordx4 v[80:83], v[48:49], off nt
	s_nop 0
	global_load_dwordx4 v[68:71], v[68:69], off nt
	s_nop 0
	global_load_dwordx4 v[64:67], v[60:61], off nt
	s_nop 0
	global_load_dwordx4 v[60:63], v[62:63], off nt
	s_nop 0
	global_load_dwordx4 v[56:59], v[56:57], off nt
	s_nop 0
	global_load_dwordx4 v[52:55], v[52:53], off nt
	s_nop 0
	global_load_dwordx4 v[48:51], v[50:51], off nt
	s_nop 0
	global_load_dwordx4 v[44:47], v[44:45], off nt

; DEVI int opaque_tid() { int t = threadIdx.x; asm volatile("" : "+v"(t)); return t; }
; DEVI void cvt8_load(const Params& p, int L, int t, CvtIn& in) {
;     const int which = t / 4096, r = t % 4096, le = L * 16 + r / 256, kt = (r % 256) / 16, nt = r % 16;
;     const float* src = (which == 2 ? p.w_down : (which == 0 ? p.w_gate : p.w_up)) + (size_t)le * 2048 * 2048;
;     const int tid = opaque_tid(), nq = tid & 31, kq0 = tid >> 5;
; #pragma unroll
;     for (int it = 0; it < 2; ++it)
; #pragma unroll
;         for (int kk = 0; kk < 4; ++kk) in.v[it * 4 + kk] = __builtin_nontemporal_load((const f32x4*)(src + (size_t)(kt * 128 + (kq0 + it * 16) * 4 + kk) * 2048 + nt * 128 + nq * 4));
; }
; DEVI void cvt8_stream3(const Params& p, int L, int t0, int step, int count, char* smem) {
;     if (count <= 0) return;
;     CvtIn a, b; cvt8_load(p, L, t0, a);
;     if (count > 1) cvt8_load(p, L, t0 + step, b);
.LBB0_773:
	s_and_b64 vcc, exec, s[16:17]
	s_cbranch_vccz .LBB0_801
	v_readlane_b32 s4, v255, 0
	v_readlane_b32 s5, v255, 1
	s_mov_b32 s6, s2
	s_mov_b64 s[16:17], -1
	s_and_b64 vcc, exec, s[4:5]
	s_cbranch_vccz .LBB0_784
	s_add_i32 s7, s6, 0x1b50
	s_and_b32 s4, s7, 0xfffff000
	s_add_i32 s5, s6, 0x2b4f
	s_cmpk_lt_u32 s5, 0x1fff
	s_cselect_b32 s5, s64, 0x80
	s_cmpk_lg_i32 s4, 0x2000
	s_cselect_b32 s4, s5, 0x88
	s_add_u32 s4, s0, s4
	s_addc_u32 s5, s1, 0
	s_ashr_i32 s14, s7, 31
	s_lshr_b32 s14, s14, 20
	s_add_i32 s14, s7, s14
	s_and_b32 s14, s14, 0xf000
	s_sub_i32 s7, s7, s14
	s_sext_i32_i16 s14, s7
	s_lshr_b32 s14, s14, 15
	s_bfe_u32 s16, s14, 0x4000c
	s_add_i32 s16, s7, s16
	s_and_b32 s16, s16, 0xfff0
	s_bfe_u32 s14, s14, 0x80008
	s_sub_i32 s16, s7, s16
	s_add_i32 s14, s7, s14
	s_sext_i32_i16 s18, s16
	s_sext_i32_i16 s16, s14
	s_and_b32 s14, s14, 0xff00
	s_load_dwordx2 s[4:5], s[4:5], 0x0
	s_ashr_i32 s16, s16, 8
	s_sub_i32 s7, s7, s14
	s_sext_i32_i16 s14, s7
	s_add_i32 s16, s16, 16
	s_bfe_u32 s14, s14, 0x4001b
	s_and_b32 s52, s16, 0xffff
	s_add_i32 s7, s7, s14
	s_lshl_b64 s[16:17], s[52:53], 24
	s_sext_i32_i16 s7, s7
	s_waitcnt lgkmcnt(0)
	s_add_u32 s14, s4, s16
	v_mov_b32_e32 v1, v0
	s_addc_u32 s16, s5, s17
	s_lshl_b32 s4, s7, 3
	v_ashrrev_i32_e32 v2, 3, v1
	s_and_b32 s4, s4, 0xffffff80
	v_and_b32_e32 v2, -4, v2
	s_waitcnt vmcnt(2)
	v_add_u32_e32 v4, s4, v2
	s_lshl_b32 s4, s18, 7
	s_ashr_i32 s5, s4, 31
	s_lshl_b64 s[4:5], s[4:5], 2
	s_add_u32 s4, s14, s4
	v_lshlrev_b32_e32 v1, 4, v1
	s_addc_u32 s5, s16, s5
	v_and_b32_e32 v2, 0x1f0, v1
	v_ashrrev_i32_e32 v5, 31, v4
	v_lshl_add_u64 v[6:7], s[4:5], 0, v[2:3]
	s_waitcnt vmcnt(1)
	v_lshlrev_b64 v[8:9], 13, v[4:5]
	v_lshl_add_u64 v[12:13], v[6:7], 0, v[8:9]
	v_or_b32_e32 v8, 1, v4
	v_ashrrev_i32_e32 v9, 31, v8
	v_lshlrev_b64 v[8:9], 13, v[8:9]
	v_lshl_add_u64 v[8:9], v[6:7], 0, v[8:9]
	global_load_dwordx4 v[20:23], v[12:13], off nt
	global_load_dwordx4 v[24:27], v[8:9], off nt
	v_or_b32_e32 v8, 2, v4
	v_or_b32_e32 v4, 3, v4
	v_ashrrev_i32_e32 v9, 31, v8
	v_ashrrev_i32_e32 v5, 31, v4
	v_lshlrev_b64 v[8:9], 13, v[8:9]
	v_lshlrev_b64 v[4:5], 13, v[4:5]
	v_lshl_add_u64 v[8:9], v[6:7], 0, v[8:9]
	v_lshl_add_u64 v[4:5], v[6:7], 0, v[4:5]
	global_load_dwordx4 v[28:31], v[8:9], off nt
	global_load_dwordx4 v[32:35], v[4:5], off nt
	v_add_co_u32_e32 v4, vcc, s94, v12
	s_mov_b32 s19, 0x82000
	s_nop 0
	v_addc_co_u32_e32 v5, vcc, 0, v13, vcc
	v_add_co_u32_e32 v8, vcc, s19, v12
	s_mov_b32 s4, 0x84000
	s_nop 0
	v_addc_co_u32_e32 v9, vcc, 0, v13, vcc
	v_add_co_u32_e32 v14, vcc, s4, v12
	s_mov_b32 s4, 0x86000
	s_nop 0
	v_addc_co_u32_e32 v15, vcc, 0, v13, vcc
	s_add_i32 s7, s6, 0x1b70
	v_add_co_u32_e32 v16, vcc, s4, v12
	s_and_b32 s4, s7, 0xfffff000
	s_add_i32 s5, s6, 0x2b6f
	s_cmpk_lt_u32 s5, 0x1fff
	s_cselect_b32 s5, s64, 0x80
	s_cmpk_lg_i32 s4, 0x2000
	s_cselect_b32 s4, s5, 0x88
	s_add_u32 s4, s0, s4
	s_addc_u32 s5, s1, 0
	s_ashr_i32 s14, s7, 31
	s_lshr_b32 s14, s14, 20
	s_add_i32 s14, s7, s14
	s_and_b32 s14, s14, 0xf000
	s_sub_i32 s7, s7, s14
	s_sext_i32_i16 s14, s7
	s_lshr_b32 s14, s14, 15
	s_bfe_u32 s16, s14, 0x4000c
	s_add_i32 s16, s7, s16
	s_and_b32 s16, s16, 0xfff0
	s_bfe_u32 s14, s14, 0x80008
	v_addc_co_u32_e32 v17, vcc, 0, v13, vcc
	s_sub_i32 s16, s7, s16
	s_add_i32 s14, s7, s14
	global_load_dwordx4 v[4:7], v[4:5], off nt
	s_nop 0
	global_load_dwordx4 v[8:11], v[8:9], off nt
	s_nop 0
	global_load_dwordx4 v[12:15], v[14:15], off nt
	s_nop 0
	global_load_dwordx4 v[16:19], v[16:17], off nt
	s_sext_i32_i16 s18, s16
	s_sext_i32_i16 s16, s14
	s_and_b32 s14, s14, 0xff00
	s_load_dwordx2 s[4:5], s[4:5], 0x0
	s_ashr_i32 s16, s16, 8
	s_sub_i32 s7, s7, s14
	s_sext_i32_i16 s14, s7
	s_add_i32 s16, s16, 16
	s_bfe_u32 s14, s14, 0x4001b
	s_and_b32 s52, s16, 0xffff
	s_add_i32 s7, s7, s14
	s_lshl_b64 s[16:17], s[52:53], 24
	s_sext_i32_i16 s7, s7
	s_waitcnt lgkmcnt(0)
	s_add_u32 s14, s4, s16
	v_mov_b32_e32 v1, v0
	s_addc_u32 s16, s5, s17
	s_lshl_b32 s4, s7, 3
	v_ashrrev_i32_e32 v2, 3, v1
	s_and_b32 s4, s4, 0xffffff80
	v_and_b32_e32 v2, -4, v2
	v_add_u32_e32 v44, s4, v2
	s_lshl_b32 s4, s18, 7
	s_ashr_i32 s5, s4, 31
	s_lshl_b64 s[4:5], s[4:5], 2
	s_add_u32 s4, s14, s4
	v_lshlrev_b32_e32 v1, 4, v1
	s_addc_u32 s5, s16, s5
	v_and_b32_e32 v2, 0x1f0, v1
	v_ashrrev_i32_e32 v45, 31, v44
	v_lshl_add_u64 v[46:47], s[4:5], 0, v[2:3]
	v_lshlrev_b64 v[36:37], 13, v[44:45]
	v_lshl_add_u64 v[48:49], v[46:47], 0, v[36:37]
	v_or_b32_e32 v36, 1, v44
	v_or_b32_e32 v50, 2, v44
	v_or_b32_e32 v44, 3, v44
	v_ashrrev_i32_e32 v37, 31, v36
	v_ashrrev_i32_e32 v51, 31, v50
	v_ashrrev_i32_e32 v45, 31, v44
	v_lshlrev_b64 v[36:37], 13, v[36:37]
	v_lshlrev_b64 v[50:51], 13, v[50:51]
	v_lshlrev_b64 v[44:45], 13, v[44:45]
	v_lshl_add_u64 v[40:41], v[46:47], 0, v[36:37]
	v_lshl_add_u64 v[50:51], v[46:47], 0, v[50:51]
	v_lshl_add_u64 v[44:45], v[46:47], 0, v[44:45]
	global_load_dwordx4 v[36:39], v[48:49], off nt
	s_nop 0
	global_load_dwordx4 v[40:43], v[40:41], off nt
	s_nop 0
	global_load_dwordx4 v[72:75], v[50:51], off nt
	global_load_dwordx4 v[76:79], v[44:45], off nt
	v_add_co_u32_e32 v44, vcc, s94, v48
	s_mov_b32 s4, 0
	s_nop 0
	v_addc_co_u32_e32 v45, vcc, 0, v49, vcc
	v_add_co_u32_e32 v46, vcc, s19, v48
	s_add_i32 s5, s6, 0x2b8f
	s_nop 0
	v_addc_co_u32_e32 v47, vcc, 0, v49, vcc
	global_load_dwordx4 v[84:87], v[44:45], off nt
	global_load_dwordx4 v[88:91], v[46:47], off nt
	v_add_co_u32_e32 v44, vcc, 0x84000, v48
	s_nop 1
	v_addc_co_u32_e32 v45, vcc, 0, v49, vcc
	v_add_co_u32_e32 v46, vcc, 0x86000, v48
	s_nop 1
	v_addc_co_u32_e32 v47, vcc, 0, v49, vcc
	global_load_dwordx4 v[92:95], v[44:45], off nt
	global_load_dwordx4 v[96:99], v[46:47], off nt
	s_waitcnt vmcnt(8)
	s_branch .LBB0_777
; DEVI int opaque_tid() { int t = threadIdx.x; asm volatile("" : "+v"(t)); return t; }
; DEVI unsigned cvt4_fp8(float a, float b, float c, float d) { int w = 0; w = __builtin_amdgcn_cvt_pk_fp8_f32(a, b, w, false); w = __builtin_amdgcn_cvt_pk_fp8_f32(c, d, w, true); return (unsigned)w; }
; DEVI void cvt8_finish(const Params& p, int L, int t, const CvtIn& in, char* smem) {
;     const int which = t / 4096, r = t % 4096, le = L * 16 + r / 256, kt = (r % 256) / 16, nt = r % 16;
;     unsigned char* dst = (which == 2) ? (unsigned char*)(p.ws + WS_WDN) + (size_t)le * 2048 * 2048 + (size_t)(nt * 128) * 2048
;                                       : (unsigned char*)(p.ws + WS_WGU) + (size_t)le * 4096 * 2048 + (size_t)(nt * 256 + which * 128) * 2048;
;     unsigned char* T = (unsigned char*)smem;
;     const int tid = opaque_tid(), nq = tid & 31, kq0 = tid >> 5;
; #pragma unroll
;     for (int it = 0; it < 2; ++it) { const int kq = kq0 + it * 16;
; #pragma unroll
;         for (int j = 0; j < 4; ++j) *(unsigned*)(T + (nq * 4 + j) * 144 + kq * 4) =
;             cvt4_fp8(in.v[it * 4][j] * W8_SCALE, in.v[it * 4 + 1][j] * W8_SCALE, in.v[it * 4 + 2][j] * W8_SCALE, in.v[it * 4 + 3][j] * W8_SCALE); }
;     __syncthreads();
; #pragma unroll
;     for (int i = 0; i < 2; ++i) { const int nl = (tid >> 3) + 64 * i, kc = (tid & 7) * 16;
;         *(u32x4*)(dst + (size_t)nl * 2048 + kt * 128 + kc) = *(const u32x4*)(T + nl * 144 + kc); }
;     __syncthreads();
; }
.LBB0_776:
	v_mul_f32_e32 v20, 0x42800000, v20
	v_mul_f32_e32 v24, 0x42800000, v24
	v_mov_b32_e32 v101, v3
	v_cvt_pk_fp8_f32 v101, v20, v24
	v_mul_f32_e32 v24, 0x42800000, v28
	v_mul_f32_e32 v28, 0x42800000, v32
	v_mov_b32_e32 v1, v0
	v_cvt_pk_fp8_f32 v101, v24, v28 op_sel:[0,0,1]
	v_mul_f32_e32 v21, 0x42800000, v21
	v_mul_f32_e32 v24, 0x42800000, v25
	v_mov_b32_e32 v25, v3
	v_cvt_pk_fp8_f32 v25, v21, v24
	v_lshlrev_b32_e32 v2, 2, v1
	v_and_b32_e32 v2, 0x7c, v2
	v_ashrrev_i32_e32 v100, 3, v1
	v_and_b32_e32 v20, -4, v100
	v_mul_u32_u24_e32 v2, 0x90, v2
	v_add3_u32 v2, 0, v20, v2
	v_mul_f32_e32 v20, 0x42800000, v29
	v_mul_f32_e32 v21, 0x42800000, v33
	v_cvt_pk_fp8_f32 v25, v20, v21 op_sel:[0,0,1]
	v_mul_f32_e32 v20, 0x42800000, v22
	v_mul_f32_e32 v21, 0x42800000, v26
	v_mov_b32_e32 v26, v3
	v_cvt_pk_fp8_f32 v26, v20, v21
	v_mul_f32_e32 v20, 0x42800000, v23
	v_mul_f32_e32 v21, 0x42800000, v27
	v_mov_b32_e32 v23, v3
	v_cvt_pk_fp8_f32 v23, v20, v21
	v_mul_f32_e32 v20, 0x42800000, v31
	v_mul_f32_e32 v21, 0x42800000, v35
	v_mul_f32_e32 v4, 0x42800000, v4
	v_cvt_pk_fp8_f32 v23, v20, v21 op_sel:[0,0,1]
	v_mul_f32_e32 v8, 0x42800000, v8
	v_mov_b32_e32 v20, v3
	v_cvt_pk_fp8_f32 v20, v4, v8
	v_mul_f32_e32 v4, 0x42800000, v5
	v_mul_f32_e32 v5, 0x42800000, v9
	v_mov_b32_e32 v8, v3
	v_cvt_pk_fp8_f32 v8, v4, v5
	s_lshl_b32 s14, s14, 8
	v_mul_f32_e32 v4, 0x42800000, v13
	v_mul_f32_e32 v5, 0x42800000, v17
	s_sub_i32 s7, s7, s14
	v_cvt_pk_fp8_f32 v8, v4, v5 op_sel:[0,0,1]
	v_mul_f32_e32 v4, 0x42800000, v6
	v_mul_f32_e32 v5, 0x42800000, v10
	v_mov_b32_e32 v10, v3
	s_sext_i32_i16 s14, s7
	v_cvt_pk_fp8_f32 v10, v4, v5
	v_mul_f32_e32 v4, 0x42800000, v7
	v_mul_f32_e32 v5, 0x42800000, v11
	v_mov_b32_e32 v7, v3
	s_bfe_u32 s14, s14, 0x4001b
	v_mul_f32_e32 v12, 0x42800000, v12
	v_mul_f32_e32 v16, 0x42800000, v16
	v_cvt_pk_fp8_f32 v7, v4, v5
	s_add_i32 s7, s7, s14
	v_cvt_pk_fp8_f32 v20, v12, v16 op_sel:[0,0,1]
	s_sext_i32_i16 s7, s7
	v_mul_f32_e32 v22, 0x42800000, v30
	v_mul_f32_e32 v24, 0x42800000, v34
	v_mul_f32_e32 v6, 0x42800000, v14
	v_mul_f32_e32 v9, 0x42800000, v18
	v_cvt_pk_fp8_f32 v26, v22, v24 op_sel:[0,0,1]
	v_cvt_pk_fp8_f32 v10, v6, v9 op_sel:[0,0,1]
	v_mul_f32_e32 v4, 0x42800000, v15
	v_mul_f32_e32 v5, 0x42800000, v19
	s_lshl_b32 s7, s7, 3
	v_cvt_pk_fp8_f32 v7, v4, v5 op_sel:[0,0,1]
	v_lshlrev_b32_e32 v1, 4, v1
	s_and_b32 s7, s7, 0xffffff80
	ds_write2_b32 v2, v101, v20 offset1:16
	ds_write2_b32 v2, v25, v8 offset0:36 offset1:52
	ds_write2_b32 v2, v26, v10 offset0:72 offset1:88
	ds_write2_b32 v2, v23, v7 offset0:108 offset1:124
	v_and_b32_e32 v2, 0x70, v1
	s_ashr_i32 s14, s7, 31
	v_mul_lo_u32 v1, v100, s91
	s_add_u32 s16, s16, s7
	v_add3_u32 v1, 0, v2, v1
	s_waitcnt lgkmcnt(0)
	s_barrier
	s_addc_u32 s17, s17, s14
	ds_read_b128 v[4:7], v1
	v_ashrrev_i32_e32 v101, 31, v100
	v_lshl_add_u64 v[8:9], s[16:17], 0, v[2:3]
	v_lshlrev_b64 v[10:11], 11, v[100:101]
	v_lshl_add_u64 v[12:13], v[8:9], 0, v[10:11]
	ds_read_b128 v[8:11], v1 offset:9216
	s_waitcnt lgkmcnt(1)
	global_store_dwordx4 v[12:13], v[4:7], off
	s_add_i32 s4, s4, 1
	s_add_i32 s5, s5, 32
	v_add_co_u32_e32 v4, vcc, 0x20000, v12
	s_nop 0
	v_addc_co_u32_e32 v5, vcc, 0, v13, vcc
	s_waitcnt lgkmcnt(0)
	global_store_dwordx4 v[4:5], v[8:11], off
	s_cmpk_eq_i32 s4, 0x5a
	s_cbranch_scc0 .Lstrm2_cont
	s_barrier
	s_branch .LBB0_783
.Lstrm2_cont:
	s_cmp_gt_u32 s4, 88
	s_cbranch_scc1 .Lstrm2_w2
	s_waitcnt vmcnt(10)
	s_branch .Lstrm2_wd

; DEVI int opaque_tid() { int t = threadIdx.x; asm volatile("" : "+v"(t)); return t; }
; DEVI void cvt8_load(const Params& p, int L, int t, CvtIn& in) {
;     const int which = t / 4096, r = t % 4096, le = L * 16 + r / 256, kt = (r % 256) / 16, nt = r % 16;
;     const float* src = (which == 2 ? p.w_down : (which == 0 ? p.w_gate : p.w_up)) + (size_t)le * 2048 * 2048;
;     const int tid = opaque_tid(), nq = tid & 31, kq0 = tid >> 5;
; #pragma unroll
;     for (int it = 0; it < 2; ++it)
; #pragma unroll
;         for (int kk = 0; kk < 4; ++kk) in.v[it * 4 + kk] = __builtin_nontemporal_load((const f32x4*)(src + (size_t)(kt * 128 + (kq0 + it * 16) * 4 + kk) * 2048 + nt * 128 + nq * 4));
; }
; DEVI void cvt8_stream3(const Params& p, int L, int t0, int step, int count, char* smem) {
;     ...
;     for (int i = 0; i < count; ++i) { CvtIn c;
;         if (i + 2 < count) cvt8_load(p, L, t0 + (i + 2) * step, c);
.LBB0_777:
	s_cmpk_gt_u32 s4, 0x57
	s_cbranch_scc1 .LBB0_779
	s_bitcmp1_b32 s4, 0
	s_cbranch_scc0 .Lstrm2_lb
	s_add_i32 s7, s5, 0xfffff001
	s_and_b32 s14, s7, 0xfffff000
	s_cmpk_lt_u32 s5, 0x1fff
	s_cselect_b32 s16, s64, 0x80
	s_cmpk_lg_i32 s14, 0x2000
	s_cselect_b32 s14, s16, 0x88
	s_add_u32 s16, s0, s14
	s_addc_u32 s17, s1, 0
	s_ashr_i32 s14, s7, 31
	s_lshr_b32 s14, s14, 20
	s_add_i32 s14, s7, s14
	s_and_b32 s14, s14, 0xf000
	s_sub_i32 s7, s7, s14
	s_sext_i32_i16 s14, s7
	s_lshr_b32 s14, s14, 15
	s_bfe_u32 s18, s14, 0x4000c
	s_add_i32 s18, s7, s18
	s_and_b32 s18, s18, 0xfff0
	s_bfe_u32 s14, s14, 0x80008
	s_sub_i32 s18, s7, s18
	s_add_i32 s14, s7, s14
	s_sext_i32_i16 s23, s18
	s_sext_i32_i16 s18, s14
	s_and_b32 s14, s14, 0xff00
	s_load_dwordx2 s[16:17], s[16:17], 0x0
	s_ashr_i32 s18, s18, 8
	s_sub_i32 s7, s7, s14
	s_sext_i32_i16 s14, s7
	s_add_i32 s18, s18, 16
	s_bfe_u32 s14, s14, 0x4001b
	s_and_b32 s52, s18, 0xffff
	s_add_i32 s7, s7, s14
	s_lshl_b64 s[18:19], s[52:53], 24
	s_waitcnt lgkmcnt(0)
	s_add_u32 s14, s16, s18
	s_sext_i32_i16 s7, s7
	s_addc_u32 s18, s17, s19
	v_mov_b32_e32 v1, v0
	s_lshl_b32 s16, s23, 7
	s_lshl_b32 s7, s7, 3
	v_ashrrev_i32_e32 v2, 3, v1
	s_ashr_i32 s17, s16, 31
	s_and_b32 s7, s7, 0xffffff80
	v_and_b32_e32 v2, -4, v2
	s_lshl_b64 s[16:17], s[16:17], 2
	v_add_u32_e32 v72, s7, v2
	s_add_u32 s16, s14, s16
	v_lshlrev_b32_e32 v1, 4, v1
	s_addc_u32 s17, s18, s17
	v_and_b32_e32 v2, 0x1f0, v1
	v_ashrrev_i32_e32 v73, 31, v72
	v_lshl_add_u64 v[74:75], s[16:17], 0, v[2:3]
	v_lshlrev_b64 v[36:37], 13, v[72:73]
	v_lshl_add_u64 v[92:93], v[74:75], 0, v[36:37]
	v_add_co_u32_e32 v84, vcc, s94, v92
	v_or_b32_e32 v36, 1, v72
	s_nop 0
	v_addc_co_u32_e32 v85, vcc, 0, v93, vcc
	v_add_co_u32_e32 v88, vcc, 0x82000, v92
	v_or_b32_e32 v76, 2, v72
	s_nop 0
	v_addc_co_u32_e32 v89, vcc, 0, v93, vcc
	v_or_b32_e32 v72, 3, v72
	v_add_co_u32_e32 v94, vcc, 0x84000, v92
	v_ashrrev_i32_e32 v37, 31, v36
	v_ashrrev_i32_e32 v77, 31, v76
	v_ashrrev_i32_e32 v73, 31, v72
	v_addc_co_u32_e32 v95, vcc, 0, v93, vcc
	v_lshlrev_b64 v[36:37], 13, v[36:37]
	v_lshlrev_b64 v[76:77], 13, v[76:77]
	v_lshlrev_b64 v[72:73], 13, v[72:73]
	v_add_co_u32_e32 v96, vcc, 0x86000, v92
	v_lshl_add_u64 v[40:41], v[74:75], 0, v[36:37]
	v_lshl_add_u64 v[76:77], v[74:75], 0, v[76:77]
	v_lshl_add_u64 v[78:79], v[74:75], 0, v[72:73]
	v_addc_co_u32_e32 v97, vcc, 0, v93, vcc
	global_load_dwordx4 v[36:39], v[92:93], off nt
	s_nop 0
	global_load_dwordx4 v[40:43], v[40:41], off nt
	s_nop 0
	global_load_dwordx4 v[72:75], v[76:77], off nt
	s_nop 0
	global_load_dwordx4 v[76:79], v[78:79], off nt
	s_nop 0
	global_load_dwordx4 v[84:87], v[84:85], off nt
	s_nop 0
	global_load_dwordx4 v[88:91], v[88:89], off nt
	s_nop 0
	global_load_dwordx4 v[92:95], v[94:95], off nt
	s_nop 0
	global_load_dwordx4 v[96:99], v[96:97], off nt
	s_branch .LBB0_779
.Lstrm2_lb:
	s_add_i32 s7, s5, 0xfffff001
	s_and_b32 s14, s7, 0xfffff000
	s_cmpk_lt_u32 s5, 0x1fff
	s_cselect_b32 s16, s64, 0x80
	s_cmpk_lg_i32 s14, 0x2000
	s_cselect_b32 s14, s16, 0x88
	s_add_u32 s16, s0, s14
	s_addc_u32 s17, s1, 0
	s_ashr_i32 s14, s7, 31
	s_lshr_b32 s14, s14, 20
	s_add_i32 s14, s7, s14
	s_and_b32 s14, s14, 0xf000
	s_sub_i32 s7, s7, s14
	s_sext_i32_i16 s14, s7
	s_lshr_b32 s14, s14, 15
	s_bfe_u32 s18, s14, 0x4000c
	s_add_i32 s18, s7, s18
	s_and_b32 s18, s18, 0xfff0
	s_bfe_u32 s14, s14, 0x80008
	s_sub_i32 s18, s7, s18
	s_add_i32 s14, s7, s14
	s_sext_i32_i16 s23, s18
	s_sext_i32_i16 s18, s14
	s_and_b32 s14, s14, 0xff00
	s_load_dwordx2 s[16:17], s[16:17], 0x0
	s_ashr_i32 s18, s18, 8
	s_sub_i32 s7, s7, s14
	s_sext_i32_i16 s14, s7
	s_add_i32 s18, s18, 16
	s_bfe_u32 s14, s14, 0x4001b
	s_and_b32 s52, s18, 0xffff
	s_add_i32 s7, s7, s14
	s_lshl_b64 s[18:19], s[52:53], 24
	s_waitcnt lgkmcnt(0)
	s_add_u32 s14, s16, s18
	s_sext_i32_i16 s7, s7
	s_addc_u32 s18, s17, s19
	v_mov_b32_e32 v1, v0
	s_lshl_b32 s16, s23, 7
	s_lshl_b32 s7, s7, 3
	v_ashrrev_i32_e32 v2, 3, v1
	s_ashr_i32 s17, s16, 31
	s_and_b32 s7, s7, 0xffffff80
	v_and_b32_e32 v2, -4, v2
	s_lshl_b64 s[16:17], s[16:17], 2
	v_add_u32_e32 v64, s7, v2
	s_add_u32 s16, s14, s16
	v_lshlrev_b32_e32 v1, 4, v1
	s_addc_u32 s17, s18, s17
	v_and_b32_e32 v2, 0x1f0, v1
	v_ashrrev_i32_e32 v65, 31, v64
	v_lshl_add_u64 v[66:67], s[16:17], 0, v[2:3]
	v_lshlrev_b64 v[80:81], 13, v[64:65]
	v_lshl_add_u64 v[48:49], v[66:67], 0, v[80:81]
	v_add_co_u32_e32 v56, vcc, s94, v48
	v_or_b32_e32 v80, 1, v64
	s_nop 0
	v_addc_co_u32_e32 v57, vcc, 0, v49, vcc
	v_add_co_u32_e32 v52, vcc, 0x82000, v48
	v_or_b32_e32 v60, 2, v64
	s_nop 0
	v_addc_co_u32_e32 v53, vcc, 0, v49, vcc
	v_or_b32_e32 v64, 3, v64
	v_add_co_u32_e32 v50, vcc, 0x84000, v48
	v_ashrrev_i32_e32 v81, 31, v80
	v_ashrrev_i32_e32 v61, 31, v60
	v_ashrrev_i32_e32 v65, 31, v64
	v_addc_co_u32_e32 v51, vcc, 0, v49, vcc
	v_lshlrev_b64 v[80:81], 13, v[80:81]
	v_lshlrev_b64 v[60:61], 13, v[60:61]
	v_lshlrev_b64 v[64:65], 13, v[64:65]
	v_add_co_u32_e32 v44, vcc, 0x86000, v48
	v_lshl_add_u64 v[68:69], v[66:67], 0, v[80:81]
	v_lshl_add_u64 v[60:61], v[66:67], 0, v[60:61]
	v_lshl_add_u64 v[62:63], v[66:67], 0, v[64:65]
	v_addc_co_u32_e32 v45, vcc, 0, v49, vcc
	global_load_dwordx4 v[80:83], v[48:49], off nt
	s_nop 0
	global_load_dwordx4 v[68:71], v[68:69], off nt
	s_nop 0
	global_load_dwordx4 v[64:67], v[60:61], off nt
	s_nop 0
	global_load_dwordx4 v[60:63], v[62:63], off nt
	s_nop 0
	global_load_dwordx4 v[56:59], v[56:57], off nt
	s_nop 0
	global_load_dwordx4 v[52:55], v[52:53], off nt
	s_nop 0
	global_load_dwordx4 v[48:51], v[50:51], off nt
	s_nop 0
	global_load_dwordx4 v[44:47], v[44:45], off nt

; DEVI int opaque_tid() { int t = threadIdx.x; asm volatile("" : "+v"(t)); return t; }
; DEVI void cvt8_load(const Params& p, int L, int t, CvtIn& in) {
;     const int which = t / 4096, r = t % 4096, le = L * 16 + r / 256, kt = (r % 256) / 16, nt = r % 16;
;     const float* src = (which == 2 ? p.w_down : (which == 0 ? p.w_gate : p.w_up)) + (size_t)le * 2048 * 2048;
;     const int tid = opaque_tid(), nq = tid & 31, kq0 = tid >> 5;
; #pragma unroll
;     for (int it = 0; it < 2; ++it)
; #pragma unroll
;         for (int kk = 0; kk < 4; ++kk) in.v[it * 4 + kk] = __builtin_nontemporal_load((const f32x4*)(src + (size_t)(kt * 128 + (kq0 + it * 16) * 4 + kk) * 2048 + nt * 128 + nq * 4));
; }
; DEVI void cvt8_stream3(const Params& p, int L, int t0, int step, int count, char* smem) {
;     if (count <= 0) return;
;     CvtIn a, b; cvt8_load(p, L, t0, a);
;     if (count > 1) cvt8_load(p, L, t0 + step, b);
.LBB0_784:
	s_and_b64 vcc, exec, s[16:17]
	s_cbranch_vccz .LBB0_801
	s_add_i32 s7, s6, 0x1e50
	s_and_b32 s4, s7, 0xfffff000
	s_add_i32 s5, s6, 0x2e4f
	s_cmpk_lt_u32 s5, 0x1fff
	s_cselect_b32 s5, s64, 0x80
	s_cmpk_lg_i32 s4, 0x2000
	s_cselect_b32 s4, s5, 0x88
	s_add_u32 s4, s0, s4
	s_addc_u32 s5, s1, 0
	s_ashr_i32 s14, s7, 31
	s_lshr_b32 s14, s14, 20
	s_add_i32 s14, s7, s14
	s_and_b32 s14, s14, 0xf000
	s_sub_i32 s7, s7, s14
	s_sext_i32_i16 s14, s7
	s_lshr_b32 s14, s14, 15
	s_bfe_u32 s16, s14, 0x4000c
	s_add_i32 s16, s7, s16
	s_and_b32 s16, s16, 0xfff0
	s_sub_i32 s16, s7, s16
	s_bfe_u32 s14, s14, 0x80008
	s_sext_i32_i16 s18, s16
	s_add_i32 s16, s7, s14
	s_sext_i32_i16 s14, s16
	s_and_b32 s16, s16, 0xff00
	s_sub_i32 s7, s7, s16
	s_load_dwordx2 s[4:5], s[4:5], 0x0
	s_sext_i32_i16 s16, s7
	s_lshr_b32 s14, s14, 8
	s_bfe_u32 s16, s16, 0x4001b
	s_add_i32 s7, s7, s16
	s_bfe_i64 s[16:17], s[14:15], 0x100000
	s_lshl_b64 s[16:17], s[16:17], 24
	s_sext_i32_i16 s7, s7
	s_waitcnt lgkmcnt(0)
	s_add_u32 s14, s4, s16
	v_mov_b32_e32 v1, v0
	s_addc_u32 s16, s5, s17
	s_lshl_b32 s4, s7, 3
	v_ashrrev_i32_e32 v2, 3, v1
	s_and_b32 s4, s4, 0xffffff80
	v_and_b32_e32 v2, -4, v2
	s_waitcnt vmcnt(2)
	v_add_u32_e32 v4, s4, v2
	s_lshl_b32 s4, s18, 7
	s_ashr_i32 s5, s4, 31
	s_lshl_b64 s[4:5], s[4:5], 2
	s_add_u32 s4, s14, s4
	v_lshlrev_b32_e32 v1, 4, v1
	s_addc_u32 s5, s16, s5
	v_and_b32_e32 v2, 0x1f0, v1
	v_ashrrev_i32_e32 v5, 31, v4
	v_lshl_add_u64 v[6:7], s[4:5], 0, v[2:3]
	s_waitcnt vmcnt(1)
	v_lshlrev_b64 v[8:9], 13, v[4:5]
	v_lshl_add_u64 v[12:13], v[6:7], 0, v[8:9]
	v_or_b32_e32 v8, 1, v4
	v_ashrrev_i32_e32 v9, 31, v8
	v_lshlrev_b64 v[8:9], 13, v[8:9]
	v_lshl_add_u64 v[8:9], v[6:7], 0, v[8:9]
	global_load_dwordx4 v[20:23], v[12:13], off nt
	global_load_dwordx4 v[24:27], v[8:9], off nt
	v_or_b32_e32 v8, 2, v4
	v_or_b32_e32 v4, 3, v4
	v_ashrrev_i32_e32 v9, 31, v8
	v_ashrrev_i32_e32 v5, 31, v4
	v_lshlrev_b64 v[8:9], 13, v[8:9]
	v_lshlrev_b64 v[4:5], 13, v[4:5]
	v_lshl_add_u64 v[8:9], v[6:7], 0, v[8:9]
	v_lshl_add_u64 v[4:5], v[6:7], 0, v[4:5]
	global_load_dwordx4 v[28:31], v[8:9], off nt
	global_load_dwordx4 v[32:35], v[4:5], off nt
	v_add_co_u32_e32 v4, vcc, s94, v12
	s_mov_b32 s19, 0x82000
	s_nop 0
	v_addc_co_u32_e32 v5, vcc, 0, v13, vcc
	v_add_co_u32_e32 v8, vcc, s19, v12
	s_mov_b32 s4, 0x84000
	s_nop 0
	v_addc_co_u32_e32 v9, vcc, 0, v13, vcc
	v_add_co_u32_e32 v14, vcc, s4, v12
	s_mov_b32 s4, 0x86000
	s_nop 0
	v_addc_co_u32_e32 v15, vcc, 0, v13, vcc
	s_add_i32 s7, s6, 0x1e70
	v_add_co_u32_e32 v16, vcc, s4, v12
	s_and_b32 s4, s7, 0xfffff000
	s_add_i32 s5, s6, 0x2e6f
	s_cmpk_lt_u32 s5, 0x1fff
	s_cselect_b32 s5, s64, 0x80
	s_cmpk_lg_i32 s4, 0x2000
	s_cselect_b32 s4, s5, 0x88
	s_add_u32 s4, s0, s4
	s_addc_u32 s5, s1, 0
	s_ashr_i32 s14, s7, 31
	s_lshr_b32 s14, s14, 20
	s_add_i32 s14, s7, s14
	s_and_b32 s14, s14, 0xf000
	s_sub_i32 s7, s7, s14
	s_sext_i32_i16 s14, s7
	s_lshr_b32 s14, s14, 15
	s_bfe_u32 s16, s14, 0x4000c
	s_add_i32 s16, s7, s16
	s_and_b32 s16, s16, 0xfff0
	s_sub_i32 s16, s7, s16
	s_bfe_u32 s14, s14, 0x80008
	s_sext_i32_i16 s18, s16
	s_add_i32 s16, s7, s14
	v_addc_co_u32_e32 v17, vcc, 0, v13, vcc
	s_sext_i32_i16 s14, s16
	s_and_b32 s16, s16, 0xff00
	global_load_dwordx4 v[4:7], v[4:5], off nt
	s_nop 0
	global_load_dwordx4 v[8:11], v[8:9], off nt
	s_nop 0
	global_load_dwordx4 v[12:15], v[14:15], off nt
	s_nop 0
	global_load_dwordx4 v[16:19], v[16:17], off nt
	s_sub_i32 s7, s7, s16
	s_load_dwordx2 s[4:5], s[4:5], 0x0
	s_sext_i32_i16 s16, s7
	s_lshr_b32 s14, s14, 8
	s_bfe_u32 s16, s16, 0x4001b
	s_add_i32 s7, s7, s16
	s_bfe_i64 s[16:17], s[14:15], 0x100000
	s_lshl_b64 s[16:17], s[16:17], 24
	s_sext_i32_i16 s7, s7
	s_waitcnt lgkmcnt(0)
	s_add_u32 s14, s4, s16
	v_mov_b32_e32 v1, v0
	s_addc_u32 s16, s5, s17
	s_lshl_b32 s4, s7, 3
	v_ashrrev_i32_e32 v2, 3, v1
	s_and_b32 s4, s4, 0xffffff80
	v_and_b32_e32 v2, -4, v2
	v_add_u32_e32 v44, s4, v2
	s_lshl_b32 s4, s18, 7
	s_ashr_i32 s5, s4, 31
	s_lshl_b64 s[4:5], s[4:5], 2
	s_add_u32 s4, s14, s4
	v_lshlrev_b32_e32 v1, 4, v1
	s_addc_u32 s5, s16, s5
	v_and_b32_e32 v2, 0x1f0, v1
	v_ashrrev_i32_e32 v45, 31, v44
	v_lshl_add_u64 v[46:47], s[4:5], 0, v[2:3]
	v_lshlrev_b64 v[36:37], 13, v[44:45]
	v_lshl_add_u64 v[48:49], v[46:47], 0, v[36:37]
	v_or_b32_e32 v36, 1, v44
	v_or_b32_e32 v50, 2, v44
	v_or_b32_e32 v44, 3, v44
	v_ashrrev_i32_e32 v37, 31, v36
	v_ashrrev_i32_e32 v51, 31, v50
	v_ashrrev_i32_e32 v45, 31, v44
	v_lshlrev_b64 v[36:37], 13, v[36:37]
	v_lshlrev_b64 v[50:51], 13, v[50:51]
	v_lshlrev_b64 v[44:45], 13, v[44:45]
	v_lshl_add_u64 v[40:41], v[46:47], 0, v[36:37]
	v_lshl_add_u64 v[50:51], v[46:47], 0, v[50:51]
	v_lshl_add_u64 v[44:45], v[46:47], 0, v[44:45]
	global_load_dwordx4 v[36:39], v[48:49], off nt
	s_nop 0
	global_load_dwordx4 v[40:43], v[40:41], off nt
	s_nop 0
	global_load_dwordx4 v[72:75], v[50:51], off nt
	global_load_dwordx4 v[76:79], v[44:45], off nt
	v_add_co_u32_e32 v44, vcc, s94, v48
	s_mov_b32 s4, 0
	s_nop 0
	v_addc_co_u32_e32 v45, vcc, 0, v49, vcc
	v_add_co_u32_e32 v46, vcc, s19, v48
	s_add_i32 s5, s6, 0x2e8f
	s_nop 0
	v_addc_co_u32_e32 v47, vcc, 0, v49, vcc
	global_load_dwordx4 v[84:87], v[44:45], off nt
	global_load_dwordx4 v[88:91], v[46:47], off nt
	v_add_co_u32_e32 v44, vcc, 0x84000, v48
	s_nop 1
	v_addc_co_u32_e32 v45, vcc, 0, v49, vcc
	v_add_co_u32_e32 v46, vcc, 0x86000, v48
	s_nop 1
	v_addc_co_u32_e32 v47, vcc, 0, v49, vcc
	global_load_dwordx4 v[92:95], v[44:45], off nt
	global_load_dwordx4 v[96:99], v[46:47], off nt
	s_waitcnt vmcnt(8)
	s_branch .LBB0_787
; DEVI int opaque_tid() { int t = threadIdx.x; asm volatile("" : "+v"(t)); return t; }
; DEVI unsigned cvt4_fp8(float a, float b, float c, float d) { int w = 0; w = __builtin_amdgcn_cvt_pk_fp8_f32(a, b, w, false); w = __builtin_amdgcn_cvt_pk_fp8_f32(c, d, w, true); return (unsigned)w; }
; DEVI void cvt8_finish(const Params& p, int L, int t, const CvtIn& in, char* smem) {
;     const int which = t / 4096, r = t % 4096, le = L * 16 + r / 256, kt = (r % 256) / 16, nt = r % 16;
;     unsigned char* dst = (which == 2) ? (unsigned char*)(p.ws + WS_WDN) + (size_t)le * 2048 * 2048 + (size_t)(nt * 128) * 2048
;                                       : (unsigned char*)(p.ws + WS_WGU) + (size_t)le * 4096 * 2048 + (size_t)(nt * 256 + which * 128) * 2048;
;     unsigned char* T = (unsigned char*)smem;
;     const int tid = opaque_tid(), nq = tid & 31, kq0 = tid >> 5;
; #pragma unroll
;     for (int it = 0; it < 2; ++it) { const int kq = kq0 + it * 16;
; #pragma unroll
;         for (int j = 0; j < 4; ++j) *(unsigned*)(T + (nq * 4 + j) * 144 + kq * 4) =
;             cvt4_fp8(in.v[it * 4][j] * W8_SCALE, in.v[it * 4 + 1][j] * W8_SCALE, in.v[it * 4 + 2][j] * W8_SCALE, in.v[it * 4 + 3][j] * W8_SCALE); }
;     __syncthreads();
; #pragma unroll
;     for (int i = 0; i < 2; ++i) { const int nl = (tid >> 3) + 64 * i, kc = (tid & 7) * 16;
;         *(u32x4*)(dst + (size_t)nl * 2048 + kt * 128 + kc) = *(const u32x4*)(T + nl * 144 + kc); }
;     __syncthreads();
; }
.LBB0_786:
	v_mul_f32_e32 v20, 0x42800000, v20
	v_mul_f32_e32 v24, 0x42800000, v24
	v_mov_b32_e32 v101, v3
	v_cvt_pk_fp8_f32 v101, v20, v24
	v_mul_f32_e32 v24, 0x42800000, v28
	v_mul_f32_e32 v28, 0x42800000, v32
	v_mov_b32_e32 v1, v0
	v_cvt_pk_fp8_f32 v101, v24, v28 op_sel:[0,0,1]
	v_mul_f32_e32 v21, 0x42800000, v21
	v_mul_f32_e32 v24, 0x42800000, v25
	v_mov_b32_e32 v25, v3
	v_cvt_pk_fp8_f32 v25, v21, v24
	v_lshlrev_b32_e32 v2, 2, v1
	v_and_b32_e32 v2, 0x7c, v2
	v_ashrrev_i32_e32 v100, 3, v1
	v_and_b32_e32 v20, -4, v100
	v_mul_u32_u24_e32 v2, 0x90, v2
	v_add3_u32 v2, 0, v20, v2
	v_mul_f32_e32 v20, 0x42800000, v29
	v_mul_f32_e32 v21, 0x42800000, v33
	v_cvt_pk_fp8_f32 v25, v20, v21 op_sel:[0,0,1]
	v_mul_f32_e32 v20, 0x42800000, v22
	v_mul_f32_e32 v21, 0x42800000, v26
	v_mov_b32_e32 v26, v3
	v_cvt_pk_fp8_f32 v26, v20, v21
	v_mul_f32_e32 v20, 0x42800000, v23
	v_mul_f32_e32 v21, 0x42800000, v27
	v_mov_b32_e32 v23, v3
	v_cvt_pk_fp8_f32 v23, v20, v21
	v_mul_f32_e32 v20, 0x42800000, v31
	v_mul_f32_e32 v21, 0x42800000, v35
	v_mul_f32_e32 v4, 0x42800000, v4
	v_cvt_pk_fp8_f32 v23, v20, v21 op_sel:[0,0,1]
	v_mul_f32_e32 v8, 0x42800000, v8
	v_mov_b32_e32 v20, v3
	v_cvt_pk_fp8_f32 v20, v4, v8
	v_mul_f32_e32 v4, 0x42800000, v5
	v_mul_f32_e32 v5, 0x42800000, v9
	v_mov_b32_e32 v8, v3
	v_cvt_pk_fp8_f32 v8, v4, v5
	s_lshl_b32 s14, s14, 8
	v_mul_f32_e32 v4, 0x42800000, v13
	v_mul_f32_e32 v5, 0x42800000, v17
	s_sub_i32 s7, s7, s14
	v_cvt_pk_fp8_f32 v8, v4, v5 op_sel:[0,0,1]
	v_mul_f32_e32 v4, 0x42800000, v6
	v_mul_f32_e32 v5, 0x42800000, v10
	v_mov_b32_e32 v10, v3
	s_sext_i32_i16 s14, s7
	v_cvt_pk_fp8_f32 v10, v4, v5
	v_mul_f32_e32 v4, 0x42800000, v7
	v_mul_f32_e32 v5, 0x42800000, v11
	v_mov_b32_e32 v7, v3
	s_bfe_u32 s14, s14, 0x4001b
	v_mul_f32_e32 v12, 0x42800000, v12
	v_mul_f32_e32 v16, 0x42800000, v16
	v_cvt_pk_fp8_f32 v7, v4, v5
	s_add_i32 s7, s7, s14
	v_cvt_pk_fp8_f32 v20, v12, v16 op_sel:[0,0,1]
	s_sext_i32_i16 s7, s7
	v_mul_f32_e32 v22, 0x42800000, v30
	v_mul_f32_e32 v24, 0x42800000, v34
	v_mul_f32_e32 v6, 0x42800000, v14
	v_mul_f32_e32 v9, 0x42800000, v18
	v_cvt_pk_fp8_f32 v26, v22, v24 op_sel:[0,0,1]
	v_cvt_pk_fp8_f32 v10, v6, v9 op_sel:[0,0,1]
	v_mul_f32_e32 v4, 0x42800000, v15
	v_mul_f32_e32 v5, 0x42800000, v19
	s_lshl_b32 s7, s7, 3
	v_cvt_pk_fp8_f32 v7, v4, v5 op_sel:[0,0,1]
	v_lshlrev_b32_e32 v1, 4, v1
	s_and_b32 s7, s7, 0xffffff80
	ds_write2_b32 v2, v101, v20 offset1:16
	ds_write2_b32 v2, v25, v8 offset0:36 offset1:52
	ds_write2_b32 v2, v26, v10 offset0:72 offset1:88
	ds_write2_b32 v2, v23, v7 offset0:108 offset1:124
	v_and_b32_e32 v2, 0x70, v1
	s_ashr_i32 s14, s7, 31
	v_mul_lo_u32 v1, v100, s91
	s_add_u32 s16, s16, s7
	v_add3_u32 v1, 0, v2, v1
	s_waitcnt lgkmcnt(0)
	s_barrier
	s_addc_u32 s17, s17, s14
	ds_read_b128 v[4:7], v1
	v_ashrrev_i32_e32 v101, 31, v100
	v_lshl_add_u64 v[8:9], s[16:17], 0, v[2:3]
	v_lshlrev_b64 v[10:11], 11, v[100:101]
	v_lshl_add_u64 v[12:13], v[8:9], 0, v[10:11]
	ds_read_b128 v[8:11], v1 offset:9216
	s_waitcnt lgkmcnt(1)
	global_store_dwordx4 v[12:13], v[4:7], off
	s_add_i32 s4, s4, 1
	s_add_i32 s5, s5, 32
	v_add_co_u32_e32 v4, vcc, 0x20000, v12
	s_nop 0
	v_addc_co_u32_e32 v5, vcc, 0, v13, vcc
	s_waitcnt lgkmcnt(0)
	global_store_dwordx4 v[4:5], v[8:11], off
	s_cmp_lg_u32 s4, 62
	s_cbranch_scc1 .Lstrm3_cont
	s_barrier
	s_branch .LBB0_793
.Lstrm3_cont:
	s_cmp_gt_u32 s4, 60
	s_cbranch_scc1 .Lstrm3_w2
	s_waitcnt vmcnt(10)
	s_branch .Lstrm3_wd

; DEVI int opaque_tid() { int t = threadIdx.x; asm volatile("" : "+v"(t)); return t; }
; DEVI void cvt8_load(const Params& p, int L, int t, CvtIn& in) {
;     const int which = t / 4096, r = t % 4096, le = L * 16 + r / 256, kt = (r % 256) / 16, nt = r % 16;
;     const float* src = (which == 2 ? p.w_down : (which == 0 ? p.w_gate : p.w_up)) + (size_t)le * 2048 * 2048;
;     const int tid = opaque_tid(), nq = tid & 31, kq0 = tid >> 5;
; #pragma unroll
;     for (int it = 0; it < 2; ++it)
; #pragma unroll
;         for (int kk = 0; kk < 4; ++kk) in.v[it * 4 + kk] = __builtin_nontemporal_load((const f32x4*)(src + (size_t)(kt * 128 + (kq0 + it * 16) * 4 + kk) * 2048 + nt * 128 + nq * 4));
; }
; DEVI void cvt8_stream3(const Params& p, int L, int t0, int step, int count, char* smem) {
;     ...
;     for (int i = 0; i < count; ++i) { CvtIn c;
;         if (i + 2 < count) cvt8_load(p, L, t0 + (i + 2) * step, c);
.LBB0_787:
	s_cmp_gt_u32 s4, 59
	s_cbranch_scc1 .LBB0_789
	s_bitcmp1_b32 s4, 0
	s_cbranch_scc0 .Lstrm3_lb
	s_add_i32 s7, s5, 0xfffff001
	s_and_b32 s14, s7, 0xfffff000
	s_cmpk_lt_u32 s5, 0x1fff
	s_cselect_b32 s16, s64, 0x80
	s_cmpk_lg_i32 s14, 0x2000
	s_cselect_b32 s14, s16, 0x88
	s_add_u32 s16, s0, s14
	s_addc_u32 s17, s1, 0
	s_ashr_i32 s14, s7, 31
	s_lshr_b32 s14, s14, 20
	s_add_i32 s14, s7, s14
	s_and_b32 s14, s14, 0xf000
	s_sub_i32 s7, s7, s14
	s_sext_i32_i16 s14, s7
	s_lshr_b32 s14, s14, 15
	s_bfe_u32 s18, s14, 0x4000c
	s_add_i32 s18, s7, s18
	s_and_b32 s18, s18, 0xfff0
	s_sub_i32 s18, s7, s18
	s_bfe_u32 s14, s14, 0x80008
	s_sext_i32_i16 s23, s18
	s_add_i32 s18, s7, s14
	s_sext_i32_i16 s14, s18
	s_and_b32 s18, s18, 0xff00
	s_sub_i32 s7, s7, s18
	s_load_dwordx2 s[16:17], s[16:17], 0x0
	s_sext_i32_i16 s18, s7
	s_lshr_b32 s14, s14, 8
	s_bfe_u32 s18, s18, 0x4001b
	s_add_i32 s7, s7, s18
	s_bfe_i64 s[18:19], s[14:15], 0x100000
	s_lshl_b64 s[18:19], s[18:19], 24
	s_waitcnt lgkmcnt(0)
	s_add_u32 s14, s16, s18
	s_sext_i32_i16 s7, s7
	s_addc_u32 s18, s17, s19
	v_mov_b32_e32 v1, v0
	s_lshl_b32 s16, s23, 7
	s_lshl_b32 s7, s7, 3
	v_ashrrev_i32_e32 v2, 3, v1
	s_ashr_i32 s17, s16, 31
	s_and_b32 s7, s7, 0xffffff80
	v_and_b32_e32 v2, -4, v2
	s_lshl_b64 s[16:17], s[16:17], 2
	v_add_u32_e32 v72, s7, v2
	s_add_u32 s16, s14, s16
	v_lshlrev_b32_e32 v1, 4, v1
	s_addc_u32 s17, s18, s17
	v_and_b32_e32 v2, 0x1f0, v1
	v_ashrrev_i32_e32 v73, 31, v72
	v_lshl_add_u64 v[74:75], s[16:17], 0, v[2:3]
	v_lshlrev_b64 v[36:37], 13, v[72:73]
	v_lshl_add_u64 v[92:93], v[74:75], 0, v[36:37]
	v_add_co_u32_e32 v84, vcc, s94, v92
	v_or_b32_e32 v36, 1, v72
	s_nop 0
	v_addc_co_u32_e32 v85, vcc, 0, v93, vcc
	v_add_co_u32_e32 v88, vcc, 0x82000, v92
	v_or_b32_e32 v76, 2, v72
	s_nop 0
	v_addc_co_u32_e32 v89, vcc, 0, v93, vcc
	v_or_b32_e32 v72, 3, v72
	v_add_co_u32_e32 v94, vcc, 0x84000, v92
	v_ashrrev_i32_e32 v37, 31, v36
	v_ashrrev_i32_e32 v77, 31, v76
	v_ashrrev_i32_e32 v73, 31, v72
	v_addc_co_u32_e32 v95, vcc, 0, v93, vcc
	v_lshlrev_b64 v[36:37], 13, v[36:37]
	v_lshlrev_b64 v[76:77], 13, v[76:77]
	v_lshlrev_b64 v[72:73], 13, v[72:73]
	v_add_co_u32_e32 v96, vcc, 0x86000, v92
	v_lshl_add_u64 v[40:41], v[74:75], 0, v[36:37]
	v_lshl_add_u64 v[76:77], v[74:75], 0, v[76:77]
	v_lshl_add_u64 v[78:79], v[74:75], 0, v[72:73]
	v_addc_co_u32_e32 v97, vcc, 0, v93, vcc
	global_load_dwordx4 v[36:39], v[92:93], off nt
	s_nop 0
	global_load_dwordx4 v[40:43], v[40:41], off nt
	s_nop 0
	global_load_dwordx4 v[72:75], v[76:77], off nt
	s_nop 0
	global_load_dwordx4 v[76:79], v[78:79], off nt
	s_nop 0
	global_load_dwordx4 v[84:87], v[84:85], off nt
	s_nop 0
	global_load_dwordx4 v[88:91], v[88:89], off nt
	s_nop 0
	global_load_dwordx4 v[92:95], v[94:95], off nt
	s_nop 0
	global_load_dwordx4 v[96:99], v[96:97], off nt
	s_branch .LBB0_789
.Lstrm3_lb:
	s_add_i32 s7, s5, 0xfffff001
	s_and_b32 s14, s7, 0xfffff000
	s_cmpk_lt_u32 s5, 0x1fff
	s_cselect_b32 s16, s64, 0x80
	s_cmpk_lg_i32 s14, 0x2000
	s_cselect_b32 s14, s16, 0x88
	s_add_u32 s16, s0, s14
	s_addc_u32 s17, s1, 0
	s_ashr_i32 s14, s7, 31
	s_lshr_b32 s14, s14, 20
	s_add_i32 s14, s7, s14
	s_and_b32 s14, s14, 0xf000
	s_sub_i32 s7, s7, s14
	s_sext_i32_i16 s14, s7
	s_lshr_b32 s14, s14, 15
	s_bfe_u32 s18, s14, 0x4000c
	s_add_i32 s18, s7, s18
	s_and_b32 s18, s18, 0xfff0
	s_sub_i32 s18, s7, s18
	s_bfe_u32 s14, s14, 0x80008
	s_sext_i32_i16 s23, s18
	s_add_i32 s18, s7, s14
	s_sext_i32_i16 s14, s18
	s_and_b32 s18, s18, 0xff00
	s_sub_i32 s7, s7, s18
	s_load_dwordx2 s[16:17], s[16:17], 0x0
	s_sext_i32_i16 s18, s7
	s_lshr_b32 s14, s14, 8
	s_bfe_u32 s18, s18, 0x4001b
	s_add_i32 s7, s7, s18
	s_bfe_i64 s[18:19], s[14:15], 0x100000
	s_lshl_b64 s[18:19], s[18:19], 24
	s_waitcnt lgkmcnt(0)
	s_add_u32 s14, s16, s18
	s_sext_i32_i16 s7, s7
	s_addc_u32 s18, s17, s19
	v_mov_b32_e32 v1, v0
	s_lshl_b32 s16, s23, 7
	s_lshl_b32 s7, s7, 3
	v_ashrrev_i32_e32 v2, 3, v1
	s_ashr_i32 s17, s16, 31
	s_and_b32 s7, s7, 0xffffff80
	v_and_b32_e32 v2, -4, v2
	s_lshl_b64 s[16:17], s[16:17], 2
	v_add_u32_e32 v64, s7, v2
	s_add_u32 s16, s14, s16
	v_lshlrev_b32_e32 v1, 4, v1
	s_addc_u32 s17, s18, s17
	v_and_b32_e32 v2, 0x1f0, v1
	v_ashrrev_i32_e32 v65, 31, v64
	v_lshl_add_u64 v[66:67], s[16:17], 0, v[2:3]
	v_lshlrev_b64 v[80:81], 13, v[64:65]
	v_lshl_add_u64 v[48:49], v[66:67], 0, v[80:81]
	v_add_co_u32_e32 v56, vcc, s94, v48
	v_or_b32_e32 v80, 1, v64
	s_nop 0
	v_addc_co_u32_e32 v57, vcc, 0, v49, vcc
	v_add_co_u32_e32 v52, vcc, 0x82000, v48
	v_or_b32_e32 v60, 2, v64
	s_nop 0
	v_addc_co_u32_e32 v53, vcc, 0, v49, vcc
	v_or_b32_e32 v64, 3, v64
	v_add_co_u32_e32 v50, vcc, 0x84000, v48
	v_ashrrev_i32_e32 v81, 31, v80
	v_ashrrev_i32_e32 v61, 31, v60
	v_ashrrev_i32_e32 v65, 31, v64
	v_addc_co_u32_e32 v51, vcc, 0, v49, vcc
	v_lshlrev_b64 v[80:81], 13, v[80:81]
	v_lshlrev_b64 v[60:61], 13, v[60:61]
	v_lshlrev_b64 v[64:65], 13, v[64:65]
	v_add_co_u32_e32 v44, vcc, 0x86000, v48
	v_lshl_add_u64 v[68:69], v[66:67], 0, v[80:81]
	v_lshl_add_u64 v[60:61], v[66:67], 0, v[60:61]
	v_lshl_add_u64 v[62:63], v[66:67], 0, v[64:65]
	v_addc_co_u32_e32 v45, vcc, 0, v49, vcc
	global_load_dwordx4 v[80:83], v[48:49], off nt
	s_nop 0
	global_load_dwordx4 v[68:71], v[68:69], off nt
	s_nop 0
	global_load_dwordx4 v[64:67], v[60:61], off nt
	s_nop 0
	global_load_dwordx4 v[60:63], v[62:63], off nt
	s_nop 0
	global_load_dwordx4 v[56:59], v[56:57], off nt
	s_nop 0
	global_load_dwordx4 v[52:55], v[52:53], off nt
	s_nop 0
	global_load_dwordx4 v[48:51], v[50:51], off nt
	s_nop 0
	global_load_dwordx4 v[44:47], v[44:45], off nt

; DEVI int opaque_tid() { int t = threadIdx.x; asm volatile("" : "+v"(t)); return t; }
; DEVI void cvt8_load(const Params& p, int L, int t, CvtIn& in) {
;     const int which = t / 4096, r = t % 4096, le = L * 16 + r / 256, kt = (r % 256) / 16, nt = r % 16;
;     const float* src = (which == 2 ? p.w_down : (which == 0 ? p.w_gate : p.w_up)) + (size_t)le * 2048 * 2048;
;     const int tid = opaque_tid(), nq = tid & 31, kq0 = tid >> 5;
; #pragma unroll
;     for (int it = 0; it < 2; ++it)
; #pragma unroll
;         for (int kk = 0; kk < 4; ++kk) in.v[it * 4 + kk] = __builtin_nontemporal_load((const f32x4*)(src + (size_t)(kt * 128 + (kq0 + it * 16) * 4 + kk) * 2048 + nt * 128 + nq * 4));
; }
; DEVI void cvt8_stream3(const Params& p, int L, int t0, int step, int count, char* smem) {
;     if (count <= 0) return;
;     CvtIn a, b; cvt8_load(p, L, t0, a);
;     if (count > 1) cvt8_load(p, L, t0 + step, b);
.LBB0_793:
	s_add_i32 s7, s6, 0x1710
	s_and_b32 s4, s7, 0xfffff000
	s_add_i32 s5, s6, 0x270f
	s_cmpk_lt_u32 s5, 0x1fff
	s_cselect_b32 s5, s64, 0x80
	s_cmpk_lg_i32 s4, 0x2000
	s_cselect_b32 s4, s5, 0x88
	s_add_u32 s4, s0, s4
	s_addc_u32 s5, s1, 0
	s_ashr_i32 s14, s7, 31
	s_lshr_b32 s14, s14, 20
	s_add_i32 s14, s7, s14
	s_and_b32 s14, s14, 0xf000
	s_sub_i32 s7, s7, s14
	s_sext_i32_i16 s14, s7
	s_lshr_b32 s14, s14, 15
	s_bfe_u32 s16, s14, 0x4000c
	s_add_i32 s16, s7, s16
	s_and_b32 s16, s16, 0xfff0
	s_bfe_u32 s14, s14, 0x80008
	s_sub_i32 s16, s7, s16
	s_add_i32 s14, s7, s14
	s_sext_i32_i16 s18, s16
	s_sext_i32_i16 s16, s14
	s_and_b32 s14, s14, 0xff00
	s_load_dwordx2 s[4:5], s[4:5], 0x0
	s_ashr_i32 s16, s16, 8
	s_sub_i32 s7, s7, s14
	s_sext_i32_i16 s14, s7
	s_add_i32 s16, s16, 16
	s_bfe_u32 s14, s14, 0x4001b
	s_and_b32 s52, s16, 0xffff
	s_add_i32 s7, s7, s14
	s_lshl_b64 s[16:17], s[52:53], 24
	s_sext_i32_i16 s7, s7
	s_waitcnt lgkmcnt(0)
	s_add_u32 s14, s4, s16
	v_mov_b32_e32 v1, v0
	s_addc_u32 s16, s5, s17
	s_lshl_b32 s4, s7, 3
	v_ashrrev_i32_e32 v2, 3, v1
	s_and_b32 s4, s4, 0xffffff80
	v_and_b32_e32 v2, -4, v2
	v_add_u32_e32 v4, s4, v2
	s_lshl_b32 s4, s18, 7
	s_ashr_i32 s5, s4, 31
	s_lshl_b64 s[4:5], s[4:5], 2
	s_add_u32 s4, s14, s4
	v_lshlrev_b32_e32 v1, 4, v1
	s_addc_u32 s5, s16, s5
	v_and_b32_e32 v2, 0x1f0, v1
	v_ashrrev_i32_e32 v5, 31, v4
	v_lshl_add_u64 v[6:7], s[4:5], 0, v[2:3]
	v_lshlrev_b64 v[8:9], 13, v[4:5]
	v_lshl_add_u64 v[12:13], v[6:7], 0, v[8:9]
	v_or_b32_e32 v8, 1, v4
	v_ashrrev_i32_e32 v9, 31, v8
	v_lshlrev_b64 v[8:9], 13, v[8:9]
	v_lshl_add_u64 v[8:9], v[6:7], 0, v[8:9]
	global_load_dwordx4 v[20:23], v[12:13], off nt
	global_load_dwordx4 v[24:27], v[8:9], off nt
	v_or_b32_e32 v8, 2, v4
	v_or_b32_e32 v4, 3, v4
	v_ashrrev_i32_e32 v9, 31, v8
	v_ashrrev_i32_e32 v5, 31, v4
	v_lshlrev_b64 v[8:9], 13, v[8:9]
	v_lshlrev_b64 v[4:5], 13, v[4:5]
	v_lshl_add_u64 v[8:9], v[6:7], 0, v[8:9]
	v_lshl_add_u64 v[4:5], v[6:7], 0, v[4:5]
	global_load_dwordx4 v[28:31], v[8:9], off nt
	global_load_dwordx4 v[32:35], v[4:5], off nt
	v_add_co_u32_e32 v4, vcc, s94, v12
	s_mov_b32 s4, 0x82000
	s_nop 0
	v_addc_co_u32_e32 v5, vcc, 0, v13, vcc
	v_add_co_u32_e32 v8, vcc, s4, v12
	s_mov_b32 s4, 0x84000
	s_nop 0
	v_addc_co_u32_e32 v9, vcc, 0, v13, vcc
	v_add_co_u32_e32 v14, vcc, s4, v12
	s_mov_b32 s4, 0x86000
	s_nop 0
	v_addc_co_u32_e32 v15, vcc, 0, v13, vcc
	s_add_i32 s7, s6, 0x1730
	v_add_co_u32_e32 v16, vcc, s4, v12
	s_and_b32 s4, s7, 0xfffff000
	s_add_i32 s5, s6, 0x272f
	s_cmpk_lt_u32 s5, 0x1fff
	s_cselect_b32 s5, s64, 0x80
	s_cmpk_lg_i32 s4, 0x2000
	s_cselect_b32 s4, s5, 0x88
	s_add_u32 s4, s0, s4
	s_addc_u32 s5, s1, 0
	s_ashr_i32 s14, s7, 31
	s_lshr_b32 s14, s14, 20
	s_add_i32 s14, s7, s14
	s_and_b32 s14, s14, 0xf000
	s_sub_i32 s7, s7, s14
	s_sext_i32_i16 s14, s7
	s_lshr_b32 s14, s14, 15
	s_bfe_u32 s16, s14, 0x4000c
	s_add_i32 s16, s7, s16
	s_and_b32 s16, s16, 0xfff0
	s_bfe_u32 s14, s14, 0x80008
	v_addc_co_u32_e32 v17, vcc, 0, v13, vcc
	s_sub_i32 s16, s7, s16
	s_add_i32 s14, s7, s14
	global_load_dwordx4 v[4:7], v[4:5], off nt
	s_nop 0
	global_load_dwordx4 v[8:11], v[8:9], off nt
	s_nop 0
	global_load_dwordx4 v[12:15], v[14:15], off nt
	s_nop 0
	global_load_dwordx4 v[16:19], v[16:17], off nt
	s_sext_i32_i16 s18, s16
	s_sext_i32_i16 s16, s14
	s_and_b32 s14, s14, 0xff00
	s_load_dwordx2 s[4:5], s[4:5], 0x0
	s_ashr_i32 s16, s16, 8
	s_sub_i32 s7, s7, s14
	s_sext_i32_i16 s14, s7
	s_add_i32 s16, s16, 16
	s_bfe_u32 s14, s14, 0x4001b
	s_and_b32 s52, s16, 0xffff
	s_add_i32 s7, s7, s14
	s_lshl_b64 s[16:17], s[52:53], 24
	s_sext_i32_i16 s7, s7
	s_waitcnt lgkmcnt(0)
	s_add_u32 s14, s4, s16
	v_mov_b32_e32 v1, v0
	s_addc_u32 s16, s5, s17
	s_lshl_b32 s4, s7, 3
	v_ashrrev_i32_e32 v2, 3, v1
	s_and_b32 s4, s4, 0xffffff80
	v_and_b32_e32 v2, -4, v2
	v_add_u32_e32 v44, s4, v2
	s_lshl_b32 s4, s18, 7
	s_ashr_i32 s5, s4, 31
	s_lshl_b64 s[4:5], s[4:5], 2
	s_add_u32 s4, s14, s4
	v_lshlrev_b32_e32 v1, 4, v1
	s_addc_u32 s5, s16, s5
	v_and_b32_e32 v2, 0x1f0, v1
	v_ashrrev_i32_e32 v45, 31, v44
	v_lshl_add_u64 v[46:47], s[4:5], 0, v[2:3]
	s_waitcnt vmcnt(17)
	v_lshlrev_b64 v[36:37], 13, v[44:45]
	v_lshl_add_u64 v[48:49], v[46:47], 0, v[36:37]
	v_or_b32_e32 v36, 1, v44
	v_or_b32_e32 v50, 2, v44
	v_or_b32_e32 v44, 3, v44
	v_ashrrev_i32_e32 v37, 31, v36
	v_ashrrev_i32_e32 v51, 31, v50
	v_ashrrev_i32_e32 v45, 31, v44
	v_lshlrev_b64 v[36:37], 13, v[36:37]
	v_lshlrev_b64 v[50:51], 13, v[50:51]
	v_lshlrev_b64 v[44:45], 13, v[44:45]
	s_waitcnt vmcnt(16)
	v_lshl_add_u64 v[40:41], v[46:47], 0, v[36:37]
	v_lshl_add_u64 v[50:51], v[46:47], 0, v[50:51]
	v_lshl_add_u64 v[44:45], v[46:47], 0, v[44:45]
	global_load_dwordx4 v[36:39], v[48:49], off nt
	s_nop 0
	global_load_dwordx4 v[40:43], v[40:41], off nt
	s_nop 0
	global_load_dwordx4 v[72:75], v[50:51], off nt
	global_load_dwordx4 v[76:79], v[44:45], off nt
	v_add_co_u32_e32 v44, vcc, s94, v48
	s_mov_b32 s4, 0
	s_nop 0
	v_addc_co_u32_e32 v45, vcc, 0, v49, vcc
	v_add_co_u32_e32 v46, vcc, 0x82000, v48
	s_add_i32 s5, s6, 0x274f
	s_nop 0
	v_addc_co_u32_e32 v47, vcc, 0, v49, vcc
	global_load_dwordx4 v[84:87], v[44:45], off nt
	global_load_dwordx4 v[88:91], v[46:47], off nt
	v_add_co_u32_e32 v44, vcc, 0x84000, v48
	s_nop 1
	v_addc_co_u32_e32 v45, vcc, 0, v49, vcc
	v_add_co_u32_e32 v46, vcc, 0x86000, v48
	s_nop 1
	v_addc_co_u32_e32 v47, vcc, 0, v49, vcc
	global_load_dwordx4 v[92:95], v[44:45], off nt
	global_load_dwordx4 v[96:99], v[46:47], off nt
	s_waitcnt vmcnt(8)
	s_branch .LBB0_795
; DEVI int opaque_tid() { int t = threadIdx.x; asm volatile("" : "+v"(t)); return t; }
; DEVI unsigned cvt4_fp8(float a, float b, float c, float d) { int w = 0; w = __builtin_amdgcn_cvt_pk_fp8_f32(a, b, w, false); w = __builtin_amdgcn_cvt_pk_fp8_f32(c, d, w, true); return (unsigned)w; }
; DEVI void cvt8_finish(const Params& p, int L, int t, const CvtIn& in, char* smem) {
;     const int which = t / 4096, r = t % 4096, le = L * 16 + r / 256, kt = (r % 256) / 16, nt = r % 16;
;     unsigned char* dst = (which == 2) ? (unsigned char*)(p.ws + WS_WDN) + (size_t)le * 2048 * 2048 + (size_t)(nt * 128) * 2048
;                                       : (unsigned char*)(p.ws + WS_WGU) + (size_t)le * 4096 * 2048 + (size_t)(nt * 256 + which * 128) * 2048;
;     unsigned char* T = (unsigned char*)smem;
;     const int tid = opaque_tid(), nq = tid & 31, kq0 = tid >> 5;
; #pragma unroll
;     for (int it = 0; it < 2; ++it) { const int kq = kq0 + it * 16;
; #pragma unroll
;         for (int j = 0; j < 4; ++j) *(unsigned*)(T + (nq * 4 + j) * 144 + kq * 4) =
;             cvt4_fp8(in.v[it * 4][j] * W8_SCALE, in.v[it * 4 + 1][j] * W8_SCALE, in.v[it * 4 + 2][j] * W8_SCALE, in.v[it * 4 + 3][j] * W8_SCALE); }
;     __syncthreads();
; #pragma unroll
;     for (int i = 0; i < 2; ++i) { const int nl = (tid >> 3) + 64 * i, kc = (tid & 7) * 16;
;         *(u32x4*)(dst + (size_t)nl * 2048 + kt * 128 + kc) = *(const u32x4*)(T + nl * 144 + kc); }
;     __syncthreads();
; }
.LBB0_794:
	v_mul_f32_e32 v20, 0x42800000, v20
	v_mul_f32_e32 v24, 0x42800000, v24
	v_mov_b32_e32 v101, v3
	v_cvt_pk_fp8_f32 v101, v20, v24
	v_mul_f32_e32 v24, 0x42800000, v28
	v_mul_f32_e32 v28, 0x42800000, v32
	v_mov_b32_e32 v1, v0
	v_cvt_pk_fp8_f32 v101, v24, v28 op_sel:[0,0,1]
	v_mul_f32_e32 v21, 0x42800000, v21
	v_mul_f32_e32 v24, 0x42800000, v25
	v_mov_b32_e32 v25, v3
	v_cvt_pk_fp8_f32 v25, v21, v24
	v_lshlrev_b32_e32 v2, 2, v1
	v_and_b32_e32 v2, 0x7c, v2
	v_ashrrev_i32_e32 v100, 3, v1
	v_and_b32_e32 v20, -4, v100
	v_mul_u32_u24_e32 v2, 0x90, v2
	v_add3_u32 v2, 0, v20, v2
	v_mul_f32_e32 v20, 0x42800000, v29
	v_mul_f32_e32 v21, 0x42800000, v33
	v_cvt_pk_fp8_f32 v25, v20, v21 op_sel:[0,0,1]
	v_mul_f32_e32 v20, 0x42800000, v22
	v_mul_f32_e32 v21, 0x42800000, v26
	v_mov_b32_e32 v26, v3
	v_cvt_pk_fp8_f32 v26, v20, v21
	v_mul_f32_e32 v20, 0x42800000, v23
	v_mul_f32_e32 v21, 0x42800000, v27
	v_mov_b32_e32 v23, v3
	v_cvt_pk_fp8_f32 v23, v20, v21
	v_mul_f32_e32 v20, 0x42800000, v31
	v_mul_f32_e32 v21, 0x42800000, v35
	v_mul_f32_e32 v4, 0x42800000, v4
	v_cvt_pk_fp8_f32 v23, v20, v21 op_sel:[0,0,1]
	v_mul_f32_e32 v8, 0x42800000, v8
	v_mov_b32_e32 v20, v3
	v_cvt_pk_fp8_f32 v20, v4, v8
	v_mul_f32_e32 v4, 0x42800000, v5
	v_mul_f32_e32 v5, 0x42800000, v9
	v_mov_b32_e32 v8, v3
	v_cvt_pk_fp8_f32 v8, v4, v5
	s_lshl_b32 s7, s7, 8
	v_mul_f32_e32 v4, 0x42800000, v13
	v_mul_f32_e32 v5, 0x42800000, v17
	s_sub_i32 s6, s6, s7
	v_cvt_pk_fp8_f32 v8, v4, v5 op_sel:[0,0,1]
	v_mul_f32_e32 v4, 0x42800000, v6
	v_mul_f32_e32 v5, 0x42800000, v10
	v_mov_b32_e32 v10, v3
	s_sext_i32_i16 s7, s6
	v_cvt_pk_fp8_f32 v10, v4, v5
	v_mul_f32_e32 v4, 0x42800000, v7
	v_mul_f32_e32 v5, 0x42800000, v11
	v_mov_b32_e32 v7, v3
	s_bfe_u32 s7, s7, 0x4001b
	v_mul_f32_e32 v12, 0x42800000, v12
	v_mul_f32_e32 v16, 0x42800000, v16
	v_cvt_pk_fp8_f32 v7, v4, v5
	s_add_i32 s6, s6, s7
	v_cvt_pk_fp8_f32 v20, v12, v16 op_sel:[0,0,1]
	s_sext_i32_i16 s6, s6
	v_mul_f32_e32 v22, 0x42800000, v30
	v_mul_f32_e32 v24, 0x42800000, v34
	v_mul_f32_e32 v6, 0x42800000, v14
	v_mul_f32_e32 v9, 0x42800000, v18
	v_cvt_pk_fp8_f32 v26, v22, v24 op_sel:[0,0,1]
	v_cvt_pk_fp8_f32 v10, v6, v9 op_sel:[0,0,1]
	v_mul_f32_e32 v4, 0x42800000, v15
	v_mul_f32_e32 v5, 0x42800000, v19
	s_lshl_b32 s6, s6, 3
	v_cvt_pk_fp8_f32 v7, v4, v5 op_sel:[0,0,1]
	v_lshlrev_b32_e32 v1, 4, v1
	s_and_b32 s6, s6, 0xffffff80
	ds_write2_b32 v2, v101, v20 offset1:16
	ds_write2_b32 v2, v25, v8 offset0:36 offset1:52
	ds_write2_b32 v2, v26, v10 offset0:72 offset1:88
	ds_write2_b32 v2, v23, v7 offset0:108 offset1:124
	v_and_b32_e32 v2, 0x70, v1
	s_ashr_i32 s7, s6, 31
	v_mul_lo_u32 v1, v100, s91
	s_add_u32 s6, s16, s6
	v_add3_u32 v1, 0, v2, v1
	s_waitcnt lgkmcnt(0)
	s_barrier
	s_addc_u32 s7, s17, s7
	ds_read_b128 v[4:7], v1
	v_ashrrev_i32_e32 v101, 31, v100
	v_lshl_add_u64 v[8:9], s[6:7], 0, v[2:3]
	v_lshlrev_b64 v[10:11], 11, v[100:101]
	v_lshl_add_u64 v[12:13], v[8:9], 0, v[10:11]
	ds_read_b128 v[8:11], v1 offset:9216
	s_waitcnt lgkmcnt(1)
	global_store_dwordx4 v[12:13], v[4:7], off
	s_add_i32 s4, s4, 1
	s_add_i32 s5, s5, 32
	v_add_co_u32_e32 v4, vcc, 0x20000, v12
	s_nop 0
	v_addc_co_u32_e32 v5, vcc, 0, v13, vcc
	s_waitcnt lgkmcnt(0)
	global_store_dwordx4 v[4:5], v[8:11], off
	s_cmp_eq_u32 s4, 34
	s_cbranch_scc0 .Lstrm4_cont
	s_barrier
	s_branch .LBB0_801
.Lstrm4_cont:
	s_cmp_gt_u32 s4, 32
	s_cbranch_scc1 .Lstrm4_w2
	s_waitcnt vmcnt(10)
	s_branch .Lstrm4_wd

; DEVI int opaque_tid() { int t = threadIdx.x; asm volatile("" : "+v"(t)); return t; }
; DEVI void cvt8_load(const Params& p, int L, int t, CvtIn& in) {
;     const int which = t / 4096, r = t % 4096, le = L * 16 + r / 256, kt = (r % 256) / 16, nt = r % 16;
;     const float* src = (which == 2 ? p.w_down : (which == 0 ? p.w_gate : p.w_up)) + (size_t)le * 2048 * 2048;
;     const int tid = opaque_tid(), nq = tid & 31, kq0 = tid >> 5;
; #pragma unroll
;     for (int it = 0; it < 2; ++it)
; #pragma unroll
;         for (int kk = 0; kk < 4; ++kk) in.v[it * 4 + kk] = __builtin_nontemporal_load((const f32x4*)(src + (size_t)(kt * 128 + (kq0 + it * 16) * 4 + kk) * 2048 + nt * 128 + nq * 4));
; }
; DEVI void cvt8_stream3(const Params& p, int L, int t0, int step, int count, char* smem) {
;     ...
;     for (int i = 0; i < count; ++i) { CvtIn c;
;         if (i + 2 < count) cvt8_load(p, L, t0 + (i + 2) * step, c);
.LBB0_795:
	s_cmp_gt_u32 s4, 31
	s_cbranch_scc1 .LBB0_797
	s_bitcmp1_b32 s4, 0
	s_cbranch_scc0 .Lstrm4_lb
	s_add_i32 s14, s5, 0xfffff001
	s_and_b32 s6, s14, 0xfffff000
	s_cmpk_lt_u32 s5, 0x1fff
	s_cselect_b32 s7, s64, 0x80
	s_cmpk_lg_i32 s6, 0x2000
	s_cselect_b32 s6, s7, 0x88
	s_add_u32 s6, s0, s6
	s_addc_u32 s7, s1, 0
	s_ashr_i32 s16, s14, 31
	s_lshr_b32 s16, s16, 20
	s_add_i32 s16, s14, s16
	s_and_b32 s16, s16, 0xf000
	s_sub_i32 s14, s14, s16
	s_sext_i32_i16 s16, s14
	s_lshr_b32 s16, s16, 15
	s_bfe_u32 s17, s16, 0x4000c
	s_add_i32 s17, s14, s17
	s_and_b32 s17, s17, 0xfff0
	s_bfe_u32 s16, s16, 0x80008
	s_sub_i32 s17, s14, s17
	s_add_i32 s16, s14, s16
	s_sext_i32_i16 s18, s17
	s_sext_i32_i16 s17, s16
	s_and_b32 s16, s16, 0xff00
	s_load_dwordx2 s[6:7], s[6:7], 0x0
	s_ashr_i32 s17, s17, 8
	s_sub_i32 s14, s14, s16
	s_sext_i32_i16 s16, s14
	s_add_i32 s17, s17, 16
	s_bfe_u32 s16, s16, 0x4001b
	s_and_b32 s52, s17, 0xffff
	s_add_i32 s14, s14, s16
	s_lshl_b64 s[16:17], s[52:53], 24
	s_sext_i32_i16 s14, s14
	s_waitcnt lgkmcnt(0)
	s_add_u32 s16, s6, s16
	v_mov_b32_e32 v1, v0
	s_addc_u32 s17, s7, s17
	s_lshl_b32 s6, s14, 3
	v_ashrrev_i32_e32 v2, 3, v1
	s_and_b32 s6, s6, 0xffffff80
	v_and_b32_e32 v2, -4, v2
	v_add_u32_e32 v72, s6, v2
	s_lshl_b32 s6, s18, 7
	s_ashr_i32 s7, s6, 31
	s_lshl_b64 s[6:7], s[6:7], 2
	s_add_u32 s6, s16, s6
	v_lshlrev_b32_e32 v1, 4, v1
	s_addc_u32 s7, s17, s7
	v_and_b32_e32 v2, 0x1f0, v1
	v_ashrrev_i32_e32 v73, 31, v72
	v_lshl_add_u64 v[74:75], s[6:7], 0, v[2:3]
	v_lshlrev_b64 v[36:37], 13, v[72:73]
	v_lshl_add_u64 v[92:93], v[74:75], 0, v[36:37]
	v_add_co_u32_e32 v84, vcc, s94, v92
	v_or_b32_e32 v36, 1, v72
	s_nop 0
	v_addc_co_u32_e32 v85, vcc, 0, v93, vcc
	v_add_co_u32_e32 v88, vcc, 0x82000, v92
	v_or_b32_e32 v76, 2, v72
	s_nop 0
	v_addc_co_u32_e32 v89, vcc, 0, v93, vcc
	v_or_b32_e32 v72, 3, v72
	v_add_co_u32_e32 v94, vcc, 0x84000, v92
	v_ashrrev_i32_e32 v37, 31, v36
	v_ashrrev_i32_e32 v77, 31, v76
	v_ashrrev_i32_e32 v73, 31, v72
	v_addc_co_u32_e32 v95, vcc, 0, v93, vcc
	v_lshlrev_b64 v[36:37], 13, v[36:37]
	v_lshlrev_b64 v[76:77], 13, v[76:77]
	v_lshlrev_b64 v[72:73], 13, v[72:73]
	v_add_co_u32_e32 v96, vcc, 0x86000, v92
	v_lshl_add_u64 v[40:41], v[74:75], 0, v[36:37]
	v_lshl_add_u64 v[76:77], v[74:75], 0, v[76:77]
	v_lshl_add_u64 v[78:79], v[74:75], 0, v[72:73]
	v_addc_co_u32_e32 v97, vcc, 0, v93, vcc
	global_load_dwordx4 v[36:39], v[92:93], off nt
	s_nop 0
	global_load_dwordx4 v[40:43], v[40:41], off nt
	s_nop 0
	global_load_dwordx4 v[72:75], v[76:77], off nt
	s_nop 0
	global_load_dwordx4 v[76:79], v[78:79], off nt
	s_nop 0
	global_load_dwordx4 v[84:87], v[84:85], off nt
	s_nop 0
	global_load_dwordx4 v[88:91], v[88:89], off nt
	s_nop 0
	global_load_dwordx4 v[92:95], v[94:95], off nt
	s_nop 0
	global_load_dwordx4 v[96:99], v[96:97], off nt
	s_branch .LBB0_797
.Lstrm4_lb:
	s_add_i32 s14, s5, 0xfffff001
	s_and_b32 s6, s14, 0xfffff000
	s_cmpk_lt_u32 s5, 0x1fff
	s_cselect_b32 s7, s64, 0x80
	s_cmpk_lg_i32 s6, 0x2000
	s_cselect_b32 s6, s7, 0x88
	s_add_u32 s6, s0, s6
	s_addc_u32 s7, s1, 0
	s_ashr_i32 s16, s14, 31
	s_lshr_b32 s16, s16, 20
	s_add_i32 s16, s14, s16
	s_and_b32 s16, s16, 0xf000
	s_sub_i32 s14, s14, s16
	s_sext_i32_i16 s16, s14
	s_lshr_b32 s16, s16, 15
	s_bfe_u32 s17, s16, 0x4000c
	s_add_i32 s17, s14, s17
	s_and_b32 s17, s17, 0xfff0
	s_bfe_u32 s16, s16, 0x80008
	s_sub_i32 s17, s14, s17
	s_add_i32 s16, s14, s16
	s_sext_i32_i16 s18, s17
	s_sext_i32_i16 s17, s16
	s_and_b32 s16, s16, 0xff00
	s_load_dwordx2 s[6:7], s[6:7], 0x0
	s_ashr_i32 s17, s17, 8
	s_sub_i32 s14, s14, s16
	s_sext_i32_i16 s16, s14
	s_add_i32 s17, s17, 16
	s_bfe_u32 s16, s16, 0x4001b
	s_and_b32 s52, s17, 0xffff
	s_add_i32 s14, s14, s16
	s_lshl_b64 s[16:17], s[52:53], 24
	s_sext_i32_i16 s14, s14
	s_waitcnt lgkmcnt(0)
	s_add_u32 s16, s6, s16
	v_mov_b32_e32 v1, v0
	s_addc_u32 s17, s7, s17
	s_lshl_b32 s6, s14, 3
	v_ashrrev_i32_e32 v2, 3, v1
	s_and_b32 s6, s6, 0xffffff80
	v_and_b32_e32 v2, -4, v2
	v_add_u32_e32 v64, s6, v2
	s_lshl_b32 s6, s18, 7
	s_ashr_i32 s7, s6, 31
	s_lshl_b64 s[6:7], s[6:7], 2
	s_add_u32 s6, s16, s6
	v_lshlrev_b32_e32 v1, 4, v1
	s_addc_u32 s7, s17, s7
	v_and_b32_e32 v2, 0x1f0, v1
	v_ashrrev_i32_e32 v65, 31, v64
	v_lshl_add_u64 v[66:67], s[6:7], 0, v[2:3]
	v_lshlrev_b64 v[80:81], 13, v[64:65]
	v_lshl_add_u64 v[48:49], v[66:67], 0, v[80:81]
	v_add_co_u32_e32 v56, vcc, s94, v48
	v_or_b32_e32 v80, 1, v64
	s_nop 0
	v_addc_co_u32_e32 v57, vcc, 0, v49, vcc
	v_add_co_u32_e32 v52, vcc, 0x82000, v48
	v_or_b32_e32 v60, 2, v64
	s_nop 0
	v_addc_co_u32_e32 v53, vcc, 0, v49, vcc
	v_or_b32_e32 v64, 3, v64
	v_add_co_u32_e32 v50, vcc, 0x84000, v48
	v_ashrrev_i32_e32 v81, 31, v80
	v_ashrrev_i32_e32 v61, 31, v60
	v_ashrrev_i32_e32 v65, 31, v64
	v_addc_co_u32_e32 v51, vcc, 0, v49, vcc
	v_lshlrev_b64 v[80:81], 13, v[80:81]
	v_lshlrev_b64 v[60:61], 13, v[60:61]
	v_lshlrev_b64 v[64:65], 13, v[64:65]
	v_add_co_u32_e32 v44, vcc, 0x86000, v48
	v_lshl_add_u64 v[68:69], v[66:67], 0, v[80:81]
	v_lshl_add_u64 v[60:61], v[66:67], 0, v[60:61]
	v_lshl_add_u64 v[62:63], v[66:67], 0, v[64:65]
	v_addc_co_u32_e32 v45, vcc, 0, v49, vcc
	global_load_dwordx4 v[80:83], v[48:49], off nt
	s_nop 0
	global_load_dwordx4 v[68:71], v[68:69], off nt
	s_nop 0
	global_load_dwordx4 v[64:67], v[60:61], off nt
	s_nop 0
	global_load_dwordx4 v[60:63], v[62:63], off nt
	s_nop 0
	global_load_dwordx4 v[56:59], v[56:57], off nt
	s_nop 0
	global_load_dwordx4 v[52:55], v[52:53], off nt
	s_nop 0
	global_load_dwordx4 v[48:51], v[50:51], off nt
	s_nop 0
	global_load_dwordx4 v[44:47], v[44:45], off nt

; DEVI int opaque_tid() { int t = threadIdx.x; asm volatile("" : "+v"(t)); return t; }
; DEVI void cvt8_load(const Params& p, int L, int t, CvtIn& in) {
;     const int which = t / 4096, r = t % 4096, le = L * 16 + r / 256, kt = (r % 256) / 16, nt = r % 16;
;     const float* src = (which == 2 ? p.w_down : (which == 0 ? p.w_gate : p.w_up)) + (size_t)le * 2048 * 2048;
;     const int tid = opaque_tid(), nq = tid & 31, kq0 = tid >> 5;
; #pragma unroll
;     for (int it = 0; it < 2; ++it)
; #pragma unroll
;         for (int kk = 0; kk < 4; ++kk) in.v[it * 4 + kk] = __builtin_nontemporal_load((const f32x4*)(src + (size_t)(kt * 128 + (kq0 + it * 16) * 4 + kk) * 2048 + nt * 128 + nq * 4));
; }
; DEVI void cvt8_stream3(const Params& p, int L, int t0, int step, int count, char* smem) {
;     if (count <= 0) return;
;     CvtIn a, b; cvt8_load(p, L, t0, a);
;     if (count > 1) cvt8_load(p, L, t0 + step, b);
.LBB0_972:
	s_waitcnt lgkmcnt(0)
	s_cmpk_eq_i32 s14, 0x100
	v_readlane_b32 s6, v254, 49
	s_cselect_b64 s[4:5], -1, 0
	v_readlane_b32 s7, v254, 50
	s_and_b64 s[4:5], s[6:7], s[4:5]
	s_andn2_b64 vcc, exec, s[4:5]
	s_cbranch_vccnz .LBB0_982
	s_mov_b32 s4, s2
	s_cmp_lt_i32 s4, 32
	s_cbranch_scc1 .LBB0_982
	s_mov_b32 s5, s2
	s_add_i32 s4, s5, 0x850
	s_and_b32 s6, s4, 0xfffff000
	s_add_i32 s7, s5, 0x184f
	s_cmpk_lt_u32 s7, 0x1fff
	s_cselect_b32 s7, s64, 0x80
	s_cmpk_lg_i32 s6, 0x2000
	s_cselect_b32 s6, s7, 0x88
	s_add_u32 s6, s0, s6
	s_addc_u32 s7, s1, 0
	s_ashr_i32 s15, s4, 31
	s_lshr_b32 s15, s15, 20
	s_add_i32 s15, s4, s15
	s_and_b32 s15, s15, 0xf000
	s_sub_i32 s15, s4, s15
	s_sext_i32_i16 s4, s15
	s_lshr_b32 s4, s4, 15
	s_bfe_u32 s16, s4, 0x4000c
	s_add_i32 s16, s15, s16
	s_and_b32 s16, s16, 0xfff0
	s_sub_i32 s16, s15, s16
	s_bfe_u32 s4, s4, 0x80008
	s_sext_i32_i16 s18, s16
	s_add_i32 s16, s15, s4
	s_sext_i32_i16 s4, s16
	s_and_b32 s16, s16, 0xff00
	s_sub_i32 s15, s15, s16
	s_load_dwordx2 s[6:7], s[6:7], 0x0
	s_sext_i32_i16 s16, s15
	s_lshr_b32 s4, s4, 8
	s_bfe_u32 s16, s16, 0x4001b
	s_add_i32 s15, s15, s16
	s_bfe_i64 s[16:17], s[4:5], 0x100000
	s_lshl_b64 s[16:17], s[16:17], 24
	s_sext_i32_i16 s15, s15
	s_waitcnt lgkmcnt(0)
	s_add_u32 s4, s6, s16
	v_mov_b32_e32 v1, v0
	s_addc_u32 s16, s7, s17
	s_lshl_b32 s6, s15, 3
	v_ashrrev_i32_e32 v2, 3, v1
	s_and_b32 s6, s6, 0xffffff80
	v_and_b32_e32 v2, -4, v2
	s_waitcnt vmcnt(0)
	v_add_u32_e32 v4, s6, v2
	s_lshl_b32 s6, s18, 7
	s_ashr_i32 s7, s6, 31
	s_lshl_b64 s[6:7], s[6:7], 2
	s_add_u32 s6, s4, s6
	v_lshlrev_b32_e32 v1, 4, v1
	s_addc_u32 s7, s16, s7
	v_and_b32_e32 v2, 0x1f0, v1
	v_ashrrev_i32_e32 v5, 31, v4
	v_lshl_add_u64 v[6:7], s[6:7], 0, v[2:3]
	v_lshlrev_b64 v[8:9], 13, v[4:5]
	v_lshl_add_u64 v[12:13], v[6:7], 0, v[8:9]
	v_or_b32_e32 v8, 1, v4
	v_ashrrev_i32_e32 v9, 31, v8
	v_lshlrev_b64 v[8:9], 13, v[8:9]
	v_lshl_add_u64 v[8:9], v[6:7], 0, v[8:9]
	global_load_dwordx4 v[20:23], v[12:13], off nt
	global_load_dwordx4 v[24:27], v[8:9], off nt
	v_or_b32_e32 v8, 2, v4
	v_or_b32_e32 v4, 3, v4
	v_ashrrev_i32_e32 v9, 31, v8
	v_ashrrev_i32_e32 v5, 31, v4
	v_lshlrev_b64 v[8:9], 13, v[8:9]
	v_lshlrev_b64 v[4:5], 13, v[4:5]
	v_lshl_add_u64 v[8:9], v[6:7], 0, v[8:9]
	v_lshl_add_u64 v[4:5], v[6:7], 0, v[4:5]
	global_load_dwordx4 v[28:31], v[8:9], off nt
	global_load_dwordx4 v[32:35], v[4:5], off nt
	v_add_co_u32_e32 v4, vcc, s94, v12
	s_mov_b32 s19, 0x82000
	s_nop 0
	v_addc_co_u32_e32 v5, vcc, 0, v13, vcc
	v_add_co_u32_e32 v8, vcc, s19, v12
	s_mov_b32 s4, 0x84000
	s_nop 0
	v_addc_co_u32_e32 v9, vcc, 0, v13, vcc
	v_add_co_u32_e32 v14, vcc, s4, v12
	s_mov_b32 s4, 0x86000
	s_nop 0
	v_addc_co_u32_e32 v15, vcc, 0, v13, vcc
	v_add_co_u32_e32 v16, vcc, s4, v12
	s_add_i32 s4, s5, 0x930
	s_and_b32 s6, s4, 0xfffff000
	s_add_i32 s7, s5, 0x192f
	s_cmpk_lt_u32 s7, 0x1fff
	s_cselect_b32 s7, s64, 0x80
	s_cmpk_lg_i32 s6, 0x2000
	s_cselect_b32 s6, s7, 0x88
	s_add_u32 s6, s0, s6
	s_addc_u32 s7, s1, 0
	s_ashr_i32 s15, s4, 31
	s_lshr_b32 s15, s15, 20
	s_add_i32 s15, s4, s15
	s_and_b32 s15, s15, 0xf000
	s_sub_i32 s15, s4, s15
	s_sext_i32_i16 s4, s15
	s_lshr_b32 s4, s4, 15
	s_bfe_u32 s16, s4, 0x4000c
	s_add_i32 s16, s15, s16
	s_and_b32 s16, s16, 0xfff0
	s_sub_i32 s16, s15, s16
	s_bfe_u32 s4, s4, 0x80008
	s_sext_i32_i16 s18, s16
	s_add_i32 s16, s15, s4
	v_addc_co_u32_e32 v17, vcc, 0, v13, vcc
	s_sext_i32_i16 s4, s16
	s_and_b32 s16, s16, 0xff00
	global_load_dwordx4 v[4:7], v[4:5], off nt
	s_nop 0
	global_load_dwordx4 v[8:11], v[8:9], off nt
	s_nop 0
	global_load_dwordx4 v[12:15], v[14:15], off nt
	s_nop 0
	global_load_dwordx4 v[16:19], v[16:17], off nt
	s_sub_i32 s15, s15, s16
	s_load_dwordx2 s[6:7], s[6:7], 0x0
	s_sext_i32_i16 s16, s15
	s_lshr_b32 s4, s4, 8
	s_bfe_u32 s16, s16, 0x4001b
	s_add_i32 s15, s15, s16
	s_bfe_i64 s[16:17], s[4:5], 0x100000
	s_lshl_b64 s[16:17], s[16:17], 24
	s_sext_i32_i16 s15, s15
	s_waitcnt lgkmcnt(0)
	s_add_u32 s4, s6, s16
	v_mov_b32_e32 v1, v0
	s_addc_u32 s16, s7, s17
	s_lshl_b32 s6, s15, 3
	v_ashrrev_i32_e32 v2, 3, v1
	s_and_b32 s6, s6, 0xffffff80
	v_and_b32_e32 v2, -4, v2
	v_add_u32_e32 v44, s6, v2
	s_lshl_b32 s6, s18, 7
	s_ashr_i32 s7, s6, 31
	s_lshl_b64 s[6:7], s[6:7], 2
	s_add_u32 s6, s4, s6
	v_lshlrev_b32_e32 v1, 4, v1
	s_addc_u32 s7, s16, s7
	v_and_b32_e32 v2, 0x1f0, v1
	v_ashrrev_i32_e32 v45, 31, v44
	v_lshl_add_u64 v[46:47], s[6:7], 0, v[2:3]
	v_lshlrev_b64 v[36:37], 13, v[44:45]
	v_lshl_add_u64 v[48:49], v[46:47], 0, v[36:37]
	v_or_b32_e32 v36, 1, v44
	v_or_b32_e32 v50, 2, v44
	v_or_b32_e32 v44, 3, v44
	v_ashrrev_i32_e32 v37, 31, v36
	v_ashrrev_i32_e32 v51, 31, v50
	v_ashrrev_i32_e32 v45, 31, v44
	v_lshlrev_b64 v[36:37], 13, v[36:37]
	v_lshlrev_b64 v[50:51], 13, v[50:51]
	v_lshlrev_b64 v[44:45], 13, v[44:45]
	v_lshl_add_u64 v[40:41], v[46:47], 0, v[36:37]
	v_lshl_add_u64 v[50:51], v[46:47], 0, v[50:51]
	v_lshl_add_u64 v[44:45], v[46:47], 0, v[44:45]
	global_load_dwordx4 v[36:39], v[48:49], off nt
	s_nop 0
	global_load_dwordx4 v[40:43], v[40:41], off nt
	s_nop 0
	global_load_dwordx4 v[72:75], v[50:51], off nt
	global_load_dwordx4 v[76:79], v[44:45], off nt
	v_add_co_u32_e32 v44, vcc, s94, v48
	s_mov_b32 s4, 0
	s_nop 0
	v_addc_co_u32_e32 v45, vcc, 0, v49, vcc
	v_add_co_u32_e32 v46, vcc, s19, v48
	s_addk_i32 s5, 0x1a0f
	s_nop 0
	v_addc_co_u32_e32 v47, vcc, 0, v49, vcc
	global_load_dwordx4 v[84:87], v[44:45], off nt
	global_load_dwordx4 v[88:91], v[46:47], off nt
	v_add_co_u32_e32 v44, vcc, 0x84000, v48
	s_nop 1
	v_addc_co_u32_e32 v45, vcc, 0, v49, vcc
	v_add_co_u32_e32 v46, vcc, 0x86000, v48
	s_nop 1
	v_addc_co_u32_e32 v47, vcc, 0, v49, vcc
	global_load_dwordx4 v[92:95], v[44:45], off nt
	global_load_dwordx4 v[96:99], v[46:47], off nt
	s_waitcnt vmcnt(8)
	s_branch .LBB0_976
; DEVI int opaque_tid() { int t = threadIdx.x; asm volatile("" : "+v"(t)); return t; }
; DEVI unsigned cvt4_fp8(float a, float b, float c, float d) { int w = 0; w = __builtin_amdgcn_cvt_pk_fp8_f32(a, b, w, false); w = __builtin_amdgcn_cvt_pk_fp8_f32(c, d, w, true); return (unsigned)w; }
; DEVI void cvt8_finish(const Params& p, int L, int t, const CvtIn& in, char* smem) {
;     const int which = t / 4096, r = t % 4096, le = L * 16 + r / 256, kt = (r % 256) / 16, nt = r % 16;
;     unsigned char* dst = (which == 2) ? (unsigned char*)(p.ws + WS_WDN) + (size_t)le * 2048 * 2048 + (size_t)(nt * 128) * 2048
;                                       : (unsigned char*)(p.ws + WS_WGU) + (size_t)le * 4096 * 2048 + (size_t)(nt * 256 + which * 128) * 2048;
;     unsigned char* T = (unsigned char*)smem;
;     const int tid = opaque_tid(), nq = tid & 31, kq0 = tid >> 5;
; #pragma unroll
;     for (int it = 0; it < 2; ++it) { const int kq = kq0 + it * 16;
; #pragma unroll
;         for (int j = 0; j < 4; ++j) *(unsigned*)(T + (nq * 4 + j) * 144 + kq * 4) =
;             cvt4_fp8(in.v[it * 4][j] * W8_SCALE, in.v[it * 4 + 1][j] * W8_SCALE, in.v[it * 4 + 2][j] * W8_SCALE, in.v[it * 4 + 3][j] * W8_SCALE); }
;     __syncthreads();
; #pragma unroll
;     for (int i = 0; i < 2; ++i) { const int nl = (tid >> 3) + 64 * i, kc = (tid & 7) * 16;
;         *(u32x4*)(dst + (size_t)nl * 2048 + kt * 128 + kc) = *(const u32x4*)(T + nl * 144 + kc); }
;     __syncthreads();
; }
.LBB0_975:
	v_mul_f32_e32 v20, 0x42800000, v20
	v_mul_f32_e32 v24, 0x42800000, v24
	v_mov_b32_e32 v101, v3
	v_cvt_pk_fp8_f32 v101, v20, v24
	v_mul_f32_e32 v24, 0x42800000, v28
	v_mul_f32_e32 v28, 0x42800000, v32
	v_mov_b32_e32 v1, v0
	v_cvt_pk_fp8_f32 v101, v24, v28 op_sel:[0,0,1]
	v_mul_f32_e32 v21, 0x42800000, v21
	v_mul_f32_e32 v24, 0x42800000, v25
	v_mov_b32_e32 v25, v3
	v_cvt_pk_fp8_f32 v25, v21, v24
	v_lshlrev_b32_e32 v2, 2, v1
	v_and_b32_e32 v2, 0x7c, v2
	v_ashrrev_i32_e32 v100, 3, v1
	v_and_b32_e32 v20, -4, v100
	v_mul_u32_u24_e32 v2, 0x90, v2
	v_add3_u32 v2, 0, v20, v2
	v_mul_f32_e32 v20, 0x42800000, v29
	v_mul_f32_e32 v21, 0x42800000, v33
	v_cvt_pk_fp8_f32 v25, v20, v21 op_sel:[0,0,1]
	v_mul_f32_e32 v20, 0x42800000, v22
	v_mul_f32_e32 v21, 0x42800000, v26
	v_mov_b32_e32 v26, v3
	v_cvt_pk_fp8_f32 v26, v20, v21
	v_mul_f32_e32 v20, 0x42800000, v23
	v_mul_f32_e32 v21, 0x42800000, v27
	v_mov_b32_e32 v23, v3
	v_cvt_pk_fp8_f32 v23, v20, v21
	v_mul_f32_e32 v20, 0x42800000, v31
	v_mul_f32_e32 v21, 0x42800000, v35
	v_mul_f32_e32 v4, 0x42800000, v4
	v_cvt_pk_fp8_f32 v23, v20, v21 op_sel:[0,0,1]
	v_mul_f32_e32 v8, 0x42800000, v8
	v_mov_b32_e32 v20, v3
	v_cvt_pk_fp8_f32 v20, v4, v8
	v_mul_f32_e32 v4, 0x42800000, v5
	v_mul_f32_e32 v5, 0x42800000, v9
	v_mov_b32_e32 v8, v3
	v_cvt_pk_fp8_f32 v8, v4, v5
	s_lshl_b32 s7, s7, 8
	v_mul_f32_e32 v4, 0x42800000, v13
	v_mul_f32_e32 v5, 0x42800000, v17
	s_sub_i32 s6, s6, s7
	v_cvt_pk_fp8_f32 v8, v4, v5 op_sel:[0,0,1]
	v_mul_f32_e32 v4, 0x42800000, v6
	v_mul_f32_e32 v5, 0x42800000, v10
	v_mov_b32_e32 v10, v3
	s_sext_i32_i16 s7, s6
	v_cvt_pk_fp8_f32 v10, v4, v5
	v_mul_f32_e32 v4, 0x42800000, v7
	v_mul_f32_e32 v5, 0x42800000, v11
	v_mov_b32_e32 v7, v3
	s_bfe_u32 s7, s7, 0x4001b
	v_mul_f32_e32 v12, 0x42800000, v12
	v_mul_f32_e32 v16, 0x42800000, v16
	v_cvt_pk_fp8_f32 v7, v4, v5
	s_add_i32 s6, s6, s7
	v_cvt_pk_fp8_f32 v20, v12, v16 op_sel:[0,0,1]
	s_sext_i32_i16 s6, s6
	v_mul_f32_e32 v22, 0x42800000, v30
	v_mul_f32_e32 v24, 0x42800000, v34
	v_mul_f32_e32 v6, 0x42800000, v14
	v_mul_f32_e32 v9, 0x42800000, v18
	v_cvt_pk_fp8_f32 v26, v22, v24 op_sel:[0,0,1]
	v_cvt_pk_fp8_f32 v10, v6, v9 op_sel:[0,0,1]
	v_mul_f32_e32 v4, 0x42800000, v15
	v_mul_f32_e32 v5, 0x42800000, v19
	s_lshl_b32 s6, s6, 3
	v_cvt_pk_fp8_f32 v7, v4, v5 op_sel:[0,0,1]
	v_lshlrev_b32_e32 v1, 4, v1
	s_and_b32 s6, s6, 0xffffff80
	ds_write2_b32 v2, v101, v20 offset1:16
	ds_write2_b32 v2, v25, v8 offset0:36 offset1:52
	ds_write2_b32 v2, v26, v10 offset0:72 offset1:88
	ds_write2_b32 v2, v23, v7 offset0:108 offset1:124
	v_and_b32_e32 v2, 0x70, v1
	s_ashr_i32 s7, s6, 31
	v_mul_lo_u32 v1, v100, s91
	s_add_u32 s6, s16, s6
	v_add3_u32 v1, 0, v2, v1
	s_waitcnt lgkmcnt(0)
	s_barrier
	s_addc_u32 s7, s17, s7
	ds_read_b128 v[4:7], v1
	v_ashrrev_i32_e32 v101, 31, v100
	v_lshl_add_u64 v[8:9], s[6:7], 0, v[2:3]
	v_lshlrev_b64 v[10:11], 11, v[100:101]
	v_lshl_add_u64 v[12:13], v[8:9], 0, v[10:11]
	ds_read_b128 v[8:11], v1 offset:9216
	s_waitcnt lgkmcnt(1)
	global_store_dwordx4 v[12:13], v[4:7], off
	s_add_i32 s4, s4, 1
	s_addk_i32 s5, 0xe0
	v_add_co_u32_e32 v4, vcc, 0x20000, v12
	s_nop 0
	v_addc_co_u32_e32 v5, vcc, 0, v13, vcc
	s_waitcnt lgkmcnt(0)
	global_store_dwordx4 v[4:5], v[8:11], off
	s_cmp_lg_u32 s4, 14
	s_cbranch_scc1 .Lstrm5_cont
	s_barrier
	s_branch .LBB0_982
.Lstrm5_cont:
	s_cmp_gt_u32 s4, 12
	s_cbranch_scc1 .Lstrm5_w2
	s_waitcnt vmcnt(10)
	s_branch .Lstrm5_wd

; DEVI int opaque_tid() { int t = threadIdx.x; asm volatile("" : "+v"(t)); return t; }
; DEVI void cvt8_load(const Params& p, int L, int t, CvtIn& in) {
;     const int which = t / 4096, r = t % 4096, le = L * 16 + r / 256, kt = (r % 256) / 16, nt = r % 16;
;     const float* src = (which == 2 ? p.w_down : (which == 0 ? p.w_gate : p.w_up)) + (size_t)le * 2048 * 2048;
;     const int tid = opaque_tid(), nq = tid & 31, kq0 = tid >> 5;
; #pragma unroll
;     for (int it = 0; it < 2; ++it)
; #pragma unroll
;         for (int kk = 0; kk < 4; ++kk) in.v[it * 4 + kk] = __builtin_nontemporal_load((const f32x4*)(src + (size_t)(kt * 128 + (kq0 + it * 16) * 4 + kk) * 2048 + nt * 128 + nq * 4));
; }
; DEVI void cvt8_stream3(const Params& p, int L, int t0, int step, int count, char* smem) {
;     ...
;     for (int i = 0; i < count; ++i) { CvtIn c;
;         if (i + 2 < count) cvt8_load(p, L, t0 + (i + 2) * step, c);
.LBB0_976:
	s_cmp_gt_u32 s4, 11
	s_cbranch_scc1 .LBB0_978
	s_bitcmp1_b32 s4, 0
	s_cbranch_scc0 .Lstrm5_lb
	s_add_i32 s15, s5, 0xfffff001
	s_and_b32 s6, s15, 0xfffff000
	s_cmpk_lt_u32 s5, 0x1fff
	s_cselect_b32 s7, s64, 0x80
	s_cmpk_lg_i32 s6, 0x2000
	s_cselect_b32 s6, s7, 0x88
	s_add_u32 s6, s0, s6
	s_addc_u32 s7, s1, 0
	s_ashr_i32 s16, s15, 31
	s_lshr_b32 s16, s16, 20
	s_add_i32 s16, s15, s16
	s_and_b32 s16, s16, 0xf000
	s_sub_i32 s15, s15, s16
	s_sext_i32_i16 s16, s15
	s_lshr_b32 s16, s16, 15
	s_bfe_u32 s17, s16, 0x4000c
	s_add_i32 s17, s15, s17
	s_and_b32 s17, s17, 0xfff0
	s_sub_i32 s17, s15, s17
	s_bfe_u32 s16, s16, 0x80008
	s_sext_i32_i16 s18, s17
	s_add_i32 s17, s15, s16
	s_sext_i32_i16 s16, s17
	s_and_b32 s17, s17, 0xff00
	s_sub_i32 s15, s15, s17
	s_load_dwordx2 s[6:7], s[6:7], 0x0
	s_sext_i32_i16 s17, s15
	s_lshr_b32 s16, s16, 8
	s_bfe_u32 s17, s17, 0x4001b
	s_add_i32 s15, s15, s17
	s_bfe_i64 s[16:17], s[16:17], 0x100000
	s_lshl_b64 s[16:17], s[16:17], 24
	s_sext_i32_i16 s15, s15
	s_waitcnt lgkmcnt(0)
	s_add_u32 s16, s6, s16
	v_mov_b32_e32 v1, v0
	s_addc_u32 s17, s7, s17
	s_lshl_b32 s6, s15, 3
	v_ashrrev_i32_e32 v2, 3, v1
	s_and_b32 s6, s6, 0xffffff80
	v_and_b32_e32 v2, -4, v2
	v_add_u32_e32 v72, s6, v2
	s_lshl_b32 s6, s18, 7
	s_ashr_i32 s7, s6, 31
	s_lshl_b64 s[6:7], s[6:7], 2
	s_add_u32 s6, s16, s6
	v_lshlrev_b32_e32 v1, 4, v1
	s_addc_u32 s7, s17, s7
	v_and_b32_e32 v2, 0x1f0, v1
	v_ashrrev_i32_e32 v73, 31, v72
	v_lshl_add_u64 v[74:75], s[6:7], 0, v[2:3]
	v_lshlrev_b64 v[36:37], 13, v[72:73]
	v_lshl_add_u64 v[92:93], v[74:75], 0, v[36:37]
	v_add_co_u32_e32 v84, vcc, s94, v92
	v_or_b32_e32 v36, 1, v72
	s_nop 0
	v_addc_co_u32_e32 v85, vcc, 0, v93, vcc
	v_add_co_u32_e32 v88, vcc, 0x82000, v92
	v_or_b32_e32 v76, 2, v72
	s_nop 0
	v_addc_co_u32_e32 v89, vcc, 0, v93, vcc
	v_or_b32_e32 v72, 3, v72
	v_add_co_u32_e32 v94, vcc, 0x84000, v92
	v_ashrrev_i32_e32 v37, 31, v36
	v_ashrrev_i32_e32 v77, 31, v76
	v_ashrrev_i32_e32 v73, 31, v72
	v_addc_co_u32_e32 v95, vcc, 0, v93, vcc
	v_lshlrev_b64 v[36:37], 13, v[36:37]
	v_lshlrev_b64 v[76:77], 13, v[76:77]
	v_lshlrev_b64 v[72:73], 13, v[72:73]
	v_add_co_u32_e32 v96, vcc, 0x86000, v92
	v_lshl_add_u64 v[40:41], v[74:75], 0, v[36:37]
	v_lshl_add_u64 v[76:77], v[74:75], 0, v[76:77]
	v_lshl_add_u64 v[78:79], v[74:75], 0, v[72:73]
	v_addc_co_u32_e32 v97, vcc, 0, v93, vcc
	global_load_dwordx4 v[36:39], v[92:93], off nt
	s_nop 0
	global_load_dwordx4 v[40:43], v[40:41], off nt
	s_nop 0
	global_load_dwordx4 v[72:75], v[76:77], off nt
	s_nop 0
	global_load_dwordx4 v[76:79], v[78:79], off nt
	s_nop 0
	global_load_dwordx4 v[84:87], v[84:85], off nt
	s_nop 0
	global_load_dwordx4 v[88:91], v[88:89], off nt
	s_nop 0
	global_load_dwordx4 v[92:95], v[94:95], off nt
	s_nop 0
	global_load_dwordx4 v[96:99], v[96:97], off nt
	s_branch .LBB0_978
.Lstrm5_lb:
	s_add_i32 s15, s5, 0xfffff001
	s_and_b32 s6, s15, 0xfffff000
	s_cmpk_lt_u32 s5, 0x1fff
	s_cselect_b32 s7, s64, 0x80
	s_cmpk_lg_i32 s6, 0x2000
	s_cselect_b32 s6, s7, 0x88
	s_add_u32 s6, s0, s6
	s_addc_u32 s7, s1, 0
	s_ashr_i32 s16, s15, 31
	s_lshr_b32 s16, s16, 20
	s_add_i32 s16, s15, s16
	s_and_b32 s16, s16, 0xf000
	s_sub_i32 s15, s15, s16
	s_sext_i32_i16 s16, s15
	s_lshr_b32 s16, s16, 15
	s_bfe_u32 s17, s16, 0x4000c
	s_add_i32 s17, s15, s17
	s_and_b32 s17, s17, 0xfff0
	s_sub_i32 s17, s15, s17
	s_bfe_u32 s16, s16, 0x80008
	s_sext_i32_i16 s18, s17
	s_add_i32 s17, s15, s16
	s_sext_i32_i16 s16, s17
	s_and_b32 s17, s17, 0xff00
	s_sub_i32 s15, s15, s17
	s_load_dwordx2 s[6:7], s[6:7], 0x0
	s_sext_i32_i16 s17, s15
	s_lshr_b32 s16, s16, 8
	s_bfe_u32 s17, s17, 0x4001b
	s_add_i32 s15, s15, s17
	s_bfe_i64 s[16:17], s[16:17], 0x100000
	s_lshl_b64 s[16:17], s[16:17], 24
	s_sext_i32_i16 s15, s15
	s_waitcnt lgkmcnt(0)
	s_add_u32 s16, s6, s16
	v_mov_b32_e32 v1, v0
	s_addc_u32 s17, s7, s17
	s_lshl_b32 s6, s15, 3
	v_ashrrev_i32_e32 v2, 3, v1
	s_and_b32 s6, s6, 0xffffff80
	v_and_b32_e32 v2, -4, v2
	v_add_u32_e32 v64, s6, v2
	s_lshl_b32 s6, s18, 7
	s_ashr_i32 s7, s6, 31
	s_lshl_b64 s[6:7], s[6:7], 2
	s_add_u32 s6, s16, s6
	v_lshlrev_b32_e32 v1, 4, v1
	s_addc_u32 s7, s17, s7
	v_and_b32_e32 v2, 0x1f0, v1
	v_ashrrev_i32_e32 v65, 31, v64
	v_lshl_add_u64 v[66:67], s[6:7], 0, v[2:3]
	v_lshlrev_b64 v[80:81], 13, v[64:65]
	v_lshl_add_u64 v[48:49], v[66:67], 0, v[80:81]
	v_add_co_u32_e32 v56, vcc, s94, v48
	v_or_b32_e32 v80, 1, v64
	s_nop 0
	v_addc_co_u32_e32 v57, vcc, 0, v49, vcc
	v_add_co_u32_e32 v52, vcc, 0x82000, v48
	v_or_b32_e32 v60, 2, v64
	s_nop 0
	v_addc_co_u32_e32 v53, vcc, 0, v49, vcc
	v_or_b32_e32 v64, 3, v64
	v_add_co_u32_e32 v50, vcc, 0x84000, v48
	v_ashrrev_i32_e32 v81, 31, v80
	v_ashrrev_i32_e32 v61, 31, v60
	v_ashrrev_i32_e32 v65, 31, v64
	v_addc_co_u32_e32 v51, vcc, 0, v49, vcc
	v_lshlrev_b64 v[80:81], 13, v[80:81]
	v_lshlrev_b64 v[60:61], 13, v[60:61]
	v_lshlrev_b64 v[64:65], 13, v[64:65]
	v_add_co_u32_e32 v44, vcc, 0x86000, v48
	v_lshl_add_u64 v[68:69], v[66:67], 0, v[80:81]
	v_lshl_add_u64 v[60:61], v[66:67], 0, v[60:61]
	v_lshl_add_u64 v[62:63], v[66:67], 0, v[64:65]
	v_addc_co_u32_e32 v45, vcc, 0, v49, vcc
	global_load_dwordx4 v[80:83], v[48:49], off nt
	s_nop 0
	global_load_dwordx4 v[68:71], v[68:69], off nt
	s_nop 0
	global_load_dwordx4 v[64:67], v[60:61], off nt
	s_nop 0
	global_load_dwordx4 v[60:63], v[62:63], off nt
	s_nop 0
	global_load_dwordx4 v[56:59], v[56:57], off nt
	s_nop 0
	global_load_dwordx4 v[52:55], v[52:53], off nt
	s_nop 0
	global_load_dwordx4 v[48:51], v[50:51], off nt
	s_nop 0
	global_load_dwordx4 v[44:47], v[44:45], off nt

; DEVI int opaque_tid() { int t = threadIdx.x; asm volatile("" : "+v"(t)); return t; }
; DEVI void cvt8_load(const Params& p, int L, int t, CvtIn& in) {
;     const int which = t / 4096, r = t % 4096, le = L * 16 + r / 256, kt = (r % 256) / 16, nt = r % 16;
;     const float* src = (which == 2 ? p.w_down : (which == 0 ? p.w_gate : p.w_up)) + (size_t)le * 2048 * 2048;
;     const int tid = opaque_tid(), nq = tid & 31, kq0 = tid >> 5;
; #pragma unroll
;     for (int it = 0; it < 2; ++it)
; #pragma unroll
;         for (int kk = 0; kk < 4; ++kk) in.v[it * 4 + kk] = __builtin_nontemporal_load((const f32x4*)(src + (size_t)(kt * 128 + (kq0 + it * 16) * 4 + kk) * 2048 + nt * 128 + nq * 4));
; }
; DEVI void cvt8_stream3(const Params& p, int L, int t0, int step, int count, char* smem) {
;     if (count <= 0) return;
;     CvtIn a, b; cvt8_load(p, L, t0, a);
;     if (count > 1) cvt8_load(p, L, t0 + step, b);
.LBB0_1164:
	s_waitcnt lgkmcnt(0)
	s_cmpk_lg_i32 s6, 0x100
	s_cbranch_scc1 .LBB0_1174
	s_mov_b32 s7, s2
	s_cmp_lt_i32 s7, 64
	s_cbranch_scc1 .LBB0_1174
	v_readlane_b32 s4, v254, 49
	v_readlane_b32 s5, v254, 50
	s_and_b64 s[4:5], s[4:5], exec
	s_movk_i32 s4, 0x1470
	s_cselect_b32 s4, s4, 0xd30
	s_add_i32 s4, s7, s4
	s_and_b32 s5, s4, 0xfffff000
	s_cmpk_lt_u32 s4, 0x1000
	s_cselect_b32 s14, s64, 0x80
	s_cmpk_lg_i32 s5, 0x2000
	s_cselect_b32 s5, s14, 0x88
	s_add_u32 s14, s0, s5
	s_addc_u32 s15, s1, 0
	s_load_dwordx2 s[14:15], s[14:15], 0x0
	v_readlane_b32 s16, v254, 61
	s_lshl_b32 s5, s16, 4
	s_bfe_u32 s16, s4, 0x40008
	s_or_b32 s16, s16, s5
	s_lshl_b32 s16, s16, 24
	s_waitcnt lgkmcnt(0)
	s_add_u32 s14, s14, s16
	v_mov_b32_e32 v1, v0
	s_addc_u32 s15, s15, 0
	s_lshl_b32 s16, s4, 3
	v_ashrrev_i32_e32 v2, 3, v1
	s_lshl_b32 s7, s7, 9
	s_and_b32 s16, s16, 0x780
	v_and_b32_e32 v2, -4, v2
	s_and_b32 s7, s7, 0x1e00
	v_add_u32_e32 v4, s16, v2
	s_add_u32 s14, s14, s7
	v_lshlrev_b32_e32 v1, 4, v1
	s_addc_u32 s15, s15, 0
	v_and_b32_e32 v2, 0x1f0, v1
	v_ashrrev_i32_e32 v5, 31, v4
	v_lshl_add_u64 v[6:7], s[14:15], 0, v[2:3]
	v_lshlrev_b64 v[8:9], 13, v[4:5]
	v_lshl_add_u64 v[28:29], v[6:7], 0, v[8:9]
	v_or_b32_e32 v8, 1, v4
	v_ashrrev_i32_e32 v9, 31, v8
	v_lshlrev_b64 v[8:9], 13, v[8:9]
	v_lshl_add_u64 v[8:9], v[6:7], 0, v[8:9]
	global_load_dwordx4 v[12:15], v[28:29], off nt
	global_load_dwordx4 v[16:19], v[8:9], off nt
	v_or_b32_e32 v8, 2, v4
	v_or_b32_e32 v4, 3, v4
	v_ashrrev_i32_e32 v9, 31, v8
	v_ashrrev_i32_e32 v5, 31, v4
	v_lshlrev_b64 v[8:9], 13, v[8:9]
	v_lshlrev_b64 v[4:5], 13, v[4:5]
	v_lshl_add_u64 v[8:9], v[6:7], 0, v[8:9]
	v_lshl_add_u64 v[4:5], v[6:7], 0, v[4:5]
	global_load_dwordx4 v[20:23], v[8:9], off nt
	global_load_dwordx4 v[24:27], v[4:5], off nt
	v_add_co_u32_e32 v4, vcc, s94, v28
	s_mov_b32 s14, 0x82000
	s_nop 0
	v_addc_co_u32_e32 v5, vcc, 0, v29, vcc
	v_add_co_u32_e32 v8, vcc, s14, v28
	s_mov_b32 s14, 0x84000
	s_nop 0
	v_addc_co_u32_e32 v9, vcc, 0, v29, vcc
	v_add_co_u32_e32 v30, vcc, s14, v28
	s_mov_b32 s14, 0x86000
	s_nop 0
	v_addc_co_u32_e32 v31, vcc, 0, v29, vcc
	s_add_i32 s16, s4, 0xc0
	v_add_co_u32_e32 v32, vcc, s14, v28
	s_and_b32 s14, s16, 0xfffff000
	s_cmpk_lt_u32 s4, 0xf40
	s_cselect_b32 s15, s64, 0x80
	s_cmpk_lg_i32 s14, 0x2000
	s_cselect_b32 s14, s15, 0x88
	s_add_u32 s14, s0, s14
	s_addc_u32 s15, s1, 0
	global_load_dwordx4 v[4:7], v[4:5], off nt
	s_nop 0
	global_load_dwordx4 v[8:11], v[8:9], off nt
	s_load_dwordx2 s[14:15], s[14:15], 0x0
	v_readlane_b32 s17, v254, 62
	s_bfe_u32 s17, s16, 0x40008
	s_or_b32 s17, s17, s5
	s_lshl_b32 s17, s17, 24
	v_addc_co_u32_e32 v33, vcc, 0, v29, vcc
	s_waitcnt lgkmcnt(0)
	s_add_u32 s14, s14, s17
	v_mov_b32_e32 v1, v0
	global_load_dwordx4 v[28:31], v[30:31], off nt
	s_nop 0
	global_load_dwordx4 v[32:35], v[32:33], off nt
	s_addc_u32 s15, s15, 0
	s_lshl_b32 s16, s16, 3
	v_ashrrev_i32_e32 v2, 3, v1
	s_and_b32 s16, s16, 0x780
	v_and_b32_e32 v2, -4, v2
	v_add_u32_e32 v44, s16, v2
	s_add_u32 s14, s14, s7
	v_lshlrev_b32_e32 v1, 4, v1
	s_addc_u32 s15, s15, 0
	v_and_b32_e32 v2, 0x1f0, v1
	v_ashrrev_i32_e32 v45, 31, v44
	v_lshl_add_u64 v[46:47], s[14:15], 0, v[2:3]
	v_lshlrev_b64 v[36:37], 13, v[44:45]
	v_lshl_add_u64 v[48:49], v[46:47], 0, v[36:37]
	v_or_b32_e32 v36, 1, v44
	v_or_b32_e32 v50, 2, v44
	v_or_b32_e32 v44, 3, v44
	v_ashrrev_i32_e32 v37, 31, v36
	v_ashrrev_i32_e32 v51, 31, v50
	v_ashrrev_i32_e32 v45, 31, v44
	v_lshlrev_b64 v[36:37], 13, v[36:37]
	v_lshlrev_b64 v[50:51], 13, v[50:51]
	v_lshlrev_b64 v[44:45], 13, v[44:45]
	v_lshl_add_u64 v[40:41], v[46:47], 0, v[36:37]
	v_lshl_add_u64 v[50:51], v[46:47], 0, v[50:51]
	v_lshl_add_u64 v[44:45], v[46:47], 0, v[44:45]
	global_load_dwordx4 v[36:39], v[48:49], off nt
	s_nop 0
	global_load_dwordx4 v[40:43], v[40:41], off nt
	s_nop 0
	global_load_dwordx4 v[72:75], v[50:51], off nt
	global_load_dwordx4 v[76:79], v[44:45], off nt
	v_add_co_u32_e32 v44, vcc, s94, v48
	s_mov_b32 s7, 0
	s_nop 0
	v_addc_co_u32_e32 v45, vcc, 0, v49, vcc
	v_add_co_u32_e32 v46, vcc, 0x82000, v48
	s_nop 1
	v_addc_co_u32_e32 v47, vcc, 0, v49, vcc
	global_load_dwordx4 v[84:87], v[44:45], off nt
	global_load_dwordx4 v[88:91], v[46:47], off nt
	v_add_co_u32_e32 v44, vcc, 0x84000, v48
	s_nop 1
	v_addc_co_u32_e32 v45, vcc, 0, v49, vcc
	v_add_co_u32_e32 v46, vcc, 0x86000, v48
	s_nop 1
	v_addc_co_u32_e32 v47, vcc, 0, v49, vcc
	global_load_dwordx4 v[92:95], v[44:45], off nt
	global_load_dwordx4 v[96:99], v[46:47], off nt
	s_waitcnt vmcnt(8)
	s_branch .LBB0_1168
; DEVI int opaque_tid() { int t = threadIdx.x; asm volatile("" : "+v"(t)); return t; }
; DEVI unsigned cvt4_fp8(float a, float b, float c, float d) { int w = 0; w = __builtin_amdgcn_cvt_pk_fp8_f32(a, b, w, false); w = __builtin_amdgcn_cvt_pk_fp8_f32(c, d, w, true); return (unsigned)w; }
; DEVI void cvt8_finish(const Params& p, int L, int t, const CvtIn& in, char* smem) {
;     const int which = t / 4096, r = t % 4096, le = L * 16 + r / 256, kt = (r % 256) / 16, nt = r % 16;
;     unsigned char* dst = (which == 2) ? (unsigned char*)(p.ws + WS_WDN) + (size_t)le * 2048 * 2048 + (size_t)(nt * 128) * 2048
;                                       : (unsigned char*)(p.ws + WS_WGU) + (size_t)le * 4096 * 2048 + (size_t)(nt * 256 + which * 128) * 2048;
;     unsigned char* T = (unsigned char*)smem;
;     const int tid = opaque_tid(), nq = tid & 31, kq0 = tid >> 5;
; #pragma unroll
;     for (int it = 0; it < 2; ++it) { const int kq = kq0 + it * 16;
; #pragma unroll
;         for (int j = 0; j < 4; ++j) *(unsigned*)(T + (nq * 4 + j) * 144 + kq * 4) =
;             cvt4_fp8(in.v[it * 4][j] * W8_SCALE, in.v[it * 4 + 1][j] * W8_SCALE, in.v[it * 4 + 2][j] * W8_SCALE, in.v[it * 4 + 3][j] * W8_SCALE); }
;     __syncthreads();
; #pragma unroll
;     for (int i = 0; i < 2; ++i) { const int nl = (tid >> 3) + 64 * i, kc = (tid & 7) * 16;
;         *(u32x4*)(dst + (size_t)nl * 2048 + kt * 128 + kc) = *(const u32x4*)(T + nl * 144 + kc); }
;     __syncthreads();
; }
.LBB0_1167:
	v_mul_f32_e32 v12, 0x42800000, v12
	v_mul_f32_e32 v16, 0x42800000, v16
	v_mov_b32_e32 v101, v3
	v_cvt_pk_fp8_f32 v101, v12, v16
	v_mul_f32_e32 v16, 0x42800000, v20
	v_mul_f32_e32 v20, 0x42800000, v24
	v_mov_b32_e32 v1, v0
	v_cvt_pk_fp8_f32 v101, v16, v20 op_sel:[0,0,1]
	v_mul_f32_e32 v13, 0x42800000, v13
	v_mul_f32_e32 v16, 0x42800000, v17
	v_mov_b32_e32 v17, v3
	v_cvt_pk_fp8_f32 v17, v13, v16
	v_lshlrev_b32_e32 v2, 2, v1
	v_and_b32_e32 v2, 0x7c, v2
	v_ashrrev_i32_e32 v100, 3, v1
	v_and_b32_e32 v12, -4, v100
	v_mul_u32_u24_e32 v2, 0x90, v2
	v_add3_u32 v2, 0, v12, v2
	v_mul_f32_e32 v12, 0x42800000, v21
	v_mul_f32_e32 v13, 0x42800000, v25
	v_cvt_pk_fp8_f32 v17, v12, v13 op_sel:[0,0,1]
	v_mul_f32_e32 v12, 0x42800000, v14
	v_mul_f32_e32 v13, 0x42800000, v18
	v_mov_b32_e32 v18, v3
	v_cvt_pk_fp8_f32 v18, v12, v13
	v_mul_f32_e32 v14, 0x42800000, v22
	v_mul_f32_e32 v16, 0x42800000, v26
	v_mul_f32_e32 v4, 0x42800000, v4
	v_cvt_pk_fp8_f32 v18, v14, v16 op_sel:[0,0,1]
	v_mul_f32_e32 v8, 0x42800000, v8
	v_mov_b32_e32 v14, v3
	v_cvt_pk_fp8_f32 v14, v4, v8
	v_mul_f32_e32 v4, 0x42800000, v5
	v_mul_f32_e32 v5, 0x42800000, v9
	v_mov_b32_e32 v8, v3
	v_cvt_pk_fp8_f32 v8, v4, v5
	v_mul_f32_e32 v12, 0x42800000, v15
	v_mul_f32_e32 v13, 0x42800000, v19
	v_mov_b32_e32 v15, v3
	s_lshr_b32 s15, s15, 8
	v_cvt_pk_fp8_f32 v15, v12, v13
	s_lshl_b32 s15, s15, 8
	v_mul_f32_e32 v4, 0x42800000, v29
	v_mul_f32_e32 v5, 0x42800000, v33
	s_sub_i32 s14, s14, s15
	v_cvt_pk_fp8_f32 v8, v4, v5 op_sel:[0,0,1]
	v_mul_f32_e32 v4, 0x42800000, v6
	v_mul_f32_e32 v5, 0x42800000, v10
	v_mov_b32_e32 v10, v3
	s_sext_i32_i16 s15, s14
	v_mul_f32_e32 v12, 0x42800000, v23
	v_mul_f32_e32 v13, 0x42800000, v27
	v_cvt_pk_fp8_f32 v10, v4, v5
	v_mul_f32_e32 v4, 0x42800000, v7
	v_mul_f32_e32 v5, 0x42800000, v11
	v_mov_b32_e32 v7, v3
	s_bfe_u32 s15, s15, 0x4001b
	v_cvt_pk_fp8_f32 v15, v12, v13 op_sel:[0,0,1]
	v_mul_f32_e32 v12, 0x42800000, v28
	v_mul_f32_e32 v13, 0x42800000, v32
	v_cvt_pk_fp8_f32 v7, v4, v5
	s_add_i32 s14, s14, s15
	v_cvt_pk_fp8_f32 v14, v12, v13 op_sel:[0,0,1]
	s_sext_i32_i16 s14, s14
	v_mul_f32_e32 v6, 0x42800000, v30
	v_mul_f32_e32 v9, 0x42800000, v34
	v_cvt_pk_fp8_f32 v10, v6, v9 op_sel:[0,0,1]
	v_mul_f32_e32 v4, 0x42800000, v31
	v_mul_f32_e32 v5, 0x42800000, v35
	s_lshl_b32 s14, s14, 3
	v_cvt_pk_fp8_f32 v7, v4, v5 op_sel:[0,0,1]
	v_lshlrev_b32_e32 v1, 4, v1
	s_and_b32 s14, s14, 0xffffff80
	ds_write2_b32 v2, v101, v14 offset1:16
	ds_write2_b32 v2, v17, v8 offset0:36 offset1:52
	ds_write2_b32 v2, v18, v10 offset0:72 offset1:88
	ds_write2_b32 v2, v15, v7 offset0:108 offset1:124
	v_and_b32_e32 v2, 0x70, v1
	s_ashr_i32 s15, s14, 31
	v_mul_lo_u32 v1, v100, s91
	s_add_u32 s14, s16, s14
	v_add3_u32 v1, 0, v2, v1
	s_waitcnt lgkmcnt(0)
	s_barrier
	s_addc_u32 s15, s17, s15
	ds_read_b128 v[4:7], v1
	v_ashrrev_i32_e32 v101, 31, v100
	v_lshl_add_u64 v[8:9], s[14:15], 0, v[2:3]
	v_lshlrev_b64 v[10:11], 11, v[100:101]
	v_lshl_add_u64 v[12:13], v[8:9], 0, v[10:11]
	ds_read_b128 v[8:11], v1 offset:9216
	s_waitcnt lgkmcnt(1)
	global_store_dwordx4 v[12:13], v[4:7], off
	s_add_i32 s7, s7, 1
	s_addk_i32 s4, 0xc0
	v_add_co_u32_e32 v4, vcc, 0x20000, v12
	s_nop 0
	v_addc_co_u32_e32 v5, vcc, 0, v13, vcc
	s_waitcnt lgkmcnt(0)
	global_store_dwordx4 v[4:5], v[8:11], off
	s_cmp_lg_u32 s7, 14
	s_cbranch_scc1 .Lstrm6_cont
	s_barrier
	s_branch .LBB0_1174
.Lstrm6_cont:
	s_cmp_gt_u32 s7, 12
	s_cbranch_scc1 .Lstrm6_w2
	s_waitcnt vmcnt(10)
	s_branch .Lstrm6_wd

; DEVI void cvt8_stream3(const Params& p, int L, int t0, int step, int count, char* smem) {
;     ...
;     for (int i = 0; i < count; ++i) { CvtIn c;
;         if (i + 2 < count) cvt8_load(p, L, t0 + (i + 2) * step, c);
;         cvt8_finish(p, L, t0 + i * step, a, smem);
;         a = b; b = c; }
.Lstrm6_wd:
	s_bitcmp1_b32 s7, 0
	s_cbranch_scc1 .Lstrm6_cc
	v_mov_b64_e32 v[16:17], v[68:69]
	v_mov_b64_e32 v[12:13], v[80:81]
	v_mov_b64_e32 v[20:21], v[64:65]
	v_mov_b64_e32 v[24:25], v[60:61]
	v_mov_b64_e32 v[4:5], v[56:57]
	v_mov_b64_e32 v[8:9], v[52:53]
	v_mov_b64_e32 v[28:29], v[48:49]
	v_mov_b64_e32 v[32:33], v[44:45]
	v_mov_b64_e32 v[14:15], v[82:83]
	v_mov_b64_e32 v[18:19], v[70:71]
	v_mov_b64_e32 v[22:23], v[66:67]
	v_mov_b64_e32 v[26:27], v[62:63]
	v_mov_b64_e32 v[6:7], v[58:59]
	v_mov_b64_e32 v[10:11], v[54:55]
	v_mov_b64_e32 v[30:31], v[50:51]
	v_mov_b64_e32 v[34:35], v[46:47]
	s_branch .Lstrm6_cd
.Lstrm6_cc:
	v_mov_b64_e32 v[4:5], v[84:85]
	v_mov_b64_e32 v[6:7], v[86:87]
	v_mov_b64_e32 v[8:9], v[88:89]
	v_mov_b64_e32 v[10:11], v[90:91]
	v_mov_b64_e32 v[12:13], v[36:37]
	v_mov_b64_e32 v[14:15], v[38:39]
	v_mov_b64_e32 v[16:17], v[40:41]
	v_mov_b64_e32 v[18:19], v[42:43]
	v_mov_b64_e32 v[20:21], v[72:73]
	v_mov_b64_e32 v[22:23], v[74:75]
	v_mov_b64_e32 v[24:25], v[76:77]
	v_mov_b64_e32 v[26:27], v[78:79]
	v_mov_b64_e32 v[28:29], v[92:93]
	v_mov_b64_e32 v[30:31], v[94:95]
	v_mov_b64_e32 v[32:33], v[96:97]
	v_mov_b64_e32 v[34:35], v[98:99]

; DEVI int opaque_tid() { int t = threadIdx.x; asm volatile("" : "+v"(t)); return t; }
; DEVI void cvt8_load(const Params& p, int L, int t, CvtIn& in) {
;     const int which = t / 4096, r = t % 4096, le = L * 16 + r / 256, kt = (r % 256) / 16, nt = r % 16;
;     const float* src = (which == 2 ? p.w_down : (which == 0 ? p.w_gate : p.w_up)) + (size_t)le * 2048 * 2048;
;     const int tid = opaque_tid(), nq = tid & 31, kq0 = tid >> 5;
; #pragma unroll
;     for (int it = 0; it < 2; ++it)
; #pragma unroll
;         for (int kk = 0; kk < 4; ++kk) in.v[it * 4 + kk] = __builtin_nontemporal_load((const f32x4*)(src + (size_t)(kt * 128 + (kq0 + it * 16) * 4 + kk) * 2048 + nt * 128 + nq * 4));
; }
; DEVI void cvt8_stream3(const Params& p, int L, int t0, int step, int count, char* smem) {
;     ...
;     for (int i = 0; i < count; ++i) { CvtIn c;
;         if (i + 2 < count) cvt8_load(p, L, t0 + (i + 2) * step, c);
.LBB0_1168:
	s_cmp_gt_u32 s7, 11
	s_cbranch_scc1 .LBB0_1170
	s_bitcmp1_b32 s7, 0
	s_cbranch_scc0 .Lstrm6_lb
	s_add_i32 s16, s4, 0x180
	s_and_b32 s14, s16, 0xfffff000
	s_cmpk_lt_u32 s16, 0x1000
	s_cselect_b32 s15, s64, 0x80
	s_cmpk_lg_i32 s14, 0x2000
	s_cselect_b32 s14, s15, 0x88
	s_add_u32 s14, s0, s14
	s_addc_u32 s15, s1, 0
	s_ashr_i32 s17, s16, 31
	s_lshr_b32 s17, s17, 20
	s_add_i32 s17, s16, s17
	s_and_b32 s17, s17, 0xf000
	s_sub_i32 s16, s16, s17
	s_sext_i32_i16 s17, s16
	s_lshr_b32 s17, s17, 15
	s_bfe_u32 s18, s17, 0x4000c
	s_bfe_u32 s17, s17, 0x80008
	s_add_i32 s18, s16, s18
	s_add_i32 s17, s16, s17
	s_and_b32 s18, s18, 0xfff0
	s_sext_i32_i16 s19, s17
	s_and_b32 s17, s17, 0xff00
	s_sub_i32 s18, s16, s18
	s_sub_i32 s16, s16, s17
	s_sext_i32_i16 s17, s16
	s_bfe_u32 s17, s17, 0x4001b
	s_add_i32 s16, s16, s17
	s_load_dwordx2 s[14:15], s[14:15], 0x0
	s_sext_i32_i16 s23, s16
	s_ashr_i32 s16, s19, 8
	s_add_i32 s16, s5, s16
	s_ashr_i32 s17, s16, 31
	s_lshl_b64 s[16:17], s[16:17], 24
	s_waitcnt lgkmcnt(0)
	s_add_u32 s16, s14, s16
	v_mov_b32_e32 v1, v0
	s_addc_u32 s17, s15, s17
	s_lshl_b32 s14, s23, 3
	v_ashrrev_i32_e32 v2, 3, v1
	s_sext_i32_i16 s18, s18
	s_and_b32 s14, s14, 0xffffff80
	v_and_b32_e32 v2, -4, v2
	v_add_u32_e32 v72, s14, v2
	s_lshl_b32 s14, s18, 7
	s_ashr_i32 s15, s14, 31
	s_lshl_b64 s[14:15], s[14:15], 2
	s_add_u32 s14, s16, s14
	v_lshlrev_b32_e32 v1, 4, v1
	s_addc_u32 s15, s17, s15
	v_and_b32_e32 v2, 0x1f0, v1
	v_ashrrev_i32_e32 v73, 31, v72
	v_lshl_add_u64 v[74:75], s[14:15], 0, v[2:3]
	v_lshlrev_b64 v[36:37], 13, v[72:73]
	v_lshl_add_u64 v[92:93], v[74:75], 0, v[36:37]
	v_add_co_u32_e32 v84, vcc, s94, v92
	v_or_b32_e32 v36, 1, v72
	s_nop 0
	v_addc_co_u32_e32 v85, vcc, 0, v93, vcc
	v_add_co_u32_e32 v88, vcc, 0x82000, v92
	v_or_b32_e32 v76, 2, v72
	s_nop 0
	v_addc_co_u32_e32 v89, vcc, 0, v93, vcc
	v_or_b32_e32 v72, 3, v72
	v_add_co_u32_e32 v94, vcc, 0x84000, v92
	v_ashrrev_i32_e32 v37, 31, v36
	v_ashrrev_i32_e32 v77, 31, v76
	v_ashrrev_i32_e32 v73, 31, v72
	v_addc_co_u32_e32 v95, vcc, 0, v93, vcc
	v_lshlrev_b64 v[36:37], 13, v[36:37]
	v_lshlrev_b64 v[76:77], 13, v[76:77]
	v_lshlrev_b64 v[72:73], 13, v[72:73]
	v_add_co_u32_e32 v96, vcc, 0x86000, v92
	v_lshl_add_u64 v[40:41], v[74:75], 0, v[36:37]
	v_lshl_add_u64 v[76:77], v[74:75], 0, v[76:77]
	v_lshl_add_u64 v[78:79], v[74:75], 0, v[72:73]
	v_addc_co_u32_e32 v97, vcc, 0, v93, vcc
	global_load_dwordx4 v[36:39], v[92:93], off nt
	s_nop 0
	global_load_dwordx4 v[40:43], v[40:41], off nt
	s_nop 0
	global_load_dwordx4 v[72:75], v[76:77], off nt
	s_nop 0
	global_load_dwordx4 v[76:79], v[78:79], off nt
	s_nop 0
	global_load_dwordx4 v[84:87], v[84:85], off nt
	s_nop 0
	global_load_dwordx4 v[88:91], v[88:89], off nt
	s_nop 0
	global_load_dwordx4 v[92:95], v[94:95], off nt
	s_nop 0
	global_load_dwordx4 v[96:99], v[96:97], off nt
	s_branch .LBB0_1170
.Lstrm6_lb:
	s_add_i32 s16, s4, 0x180
	s_and_b32 s14, s16, 0xfffff000
	s_cmpk_lt_u32 s16, 0x1000
	s_cselect_b32 s15, s64, 0x80
	s_cmpk_lg_i32 s14, 0x2000
	s_cselect_b32 s14, s15, 0x88
	s_add_u32 s14, s0, s14
	s_addc_u32 s15, s1, 0
	s_ashr_i32 s17, s16, 31
	s_lshr_b32 s17, s17, 20
	s_add_i32 s17, s16, s17
	s_and_b32 s17, s17, 0xf000
	s_sub_i32 s16, s16, s17
	s_sext_i32_i16 s17, s16
	s_lshr_b32 s17, s17, 15
	s_bfe_u32 s18, s17, 0x4000c
	s_bfe_u32 s17, s17, 0x80008
	s_add_i32 s18, s16, s18
	s_add_i32 s17, s16, s17
	s_and_b32 s18, s18, 0xfff0
	s_sext_i32_i16 s19, s17
	s_and_b32 s17, s17, 0xff00
	s_sub_i32 s18, s16, s18
	s_sub_i32 s16, s16, s17
	s_sext_i32_i16 s17, s16
	s_bfe_u32 s17, s17, 0x4001b
	s_add_i32 s16, s16, s17
	s_load_dwordx2 s[14:15], s[14:15], 0x0
	s_sext_i32_i16 s23, s16
	s_ashr_i32 s16, s19, 8
	s_add_i32 s16, s5, s16
	s_ashr_i32 s17, s16, 31
	s_lshl_b64 s[16:17], s[16:17], 24
	s_waitcnt lgkmcnt(0)
	s_add_u32 s16, s14, s16
	v_mov_b32_e32 v1, v0
	s_addc_u32 s17, s15, s17
	s_lshl_b32 s14, s23, 3
	v_ashrrev_i32_e32 v2, 3, v1
	s_sext_i32_i16 s18, s18
	s_and_b32 s14, s14, 0xffffff80
	v_and_b32_e32 v2, -4, v2
	v_add_u32_e32 v64, s14, v2
	s_lshl_b32 s14, s18, 7
	s_ashr_i32 s15, s14, 31
	s_lshl_b64 s[14:15], s[14:15], 2
	s_add_u32 s14, s16, s14
	v_lshlrev_b32_e32 v1, 4, v1
	s_addc_u32 s15, s17, s15
	v_and_b32_e32 v2, 0x1f0, v1
	v_ashrrev_i32_e32 v65, 31, v64
	v_lshl_add_u64 v[66:67], s[14:15], 0, v[2:3]
	v_lshlrev_b64 v[80:81], 13, v[64:65]
	v_lshl_add_u64 v[48:49], v[66:67], 0, v[80:81]
	v_add_co_u32_e32 v56, vcc, s94, v48
	v_or_b32_e32 v80, 1, v64
	s_nop 0
	v_addc_co_u32_e32 v57, vcc, 0, v49, vcc
	v_add_co_u32_e32 v52, vcc, 0x82000, v48
	v_or_b32_e32 v60, 2, v64
	s_nop 0
	v_addc_co_u32_e32 v53, vcc, 0, v49, vcc
	v_or_b32_e32 v64, 3, v64
	v_add_co_u32_e32 v50, vcc, 0x84000, v48
	v_ashrrev_i32_e32 v81, 31, v80
	v_ashrrev_i32_e32 v61, 31, v60
	v_ashrrev_i32_e32 v65, 31, v64
	v_addc_co_u32_e32 v51, vcc, 0, v49, vcc
	v_lshlrev_b64 v[80:81], 13, v[80:81]
	v_lshlrev_b64 v[60:61], 13, v[60:61]
	v_lshlrev_b64 v[64:65], 13, v[64:65]
	v_add_co_u32_e32 v44, vcc, 0x86000, v48
	v_lshl_add_u64 v[68:69], v[66:67], 0, v[80:81]
	v_lshl_add_u64 v[60:61], v[66:67], 0, v[60:61]
	v_lshl_add_u64 v[62:63], v[66:67], 0, v[64:65]
	v_addc_co_u32_e32 v45, vcc, 0, v49, vcc
	global_load_dwordx4 v[80:83], v[48:49], off nt
	s_nop 0
	global_load_dwordx4 v[68:71], v[68:69], off nt
	s_nop 0
	global_load_dwordx4 v[64:67], v[60:61], off nt
	s_nop 0
	global_load_dwordx4 v[60:63], v[62:63], off nt
	s_nop 0
	global_load_dwordx4 v[56:59], v[56:57], off nt
	s_nop 0
	global_load_dwordx4 v[52:55], v[52:53], off nt
	s_nop 0
	global_load_dwordx4 v[48:51], v[50:51], off nt
	s_nop 0
	global_load_dwordx4 v[44:47], v[44:45], off nt

; DEVI int opaque_tid() { int t = threadIdx.x; asm volatile("" : "+v"(t)); return t; }
; DEVI void cvt8_load(const Params& p, int L, int t, CvtIn& in) {
;     const int which = t / 4096, r = t % 4096, le = L * 16 + r / 256, kt = (r % 256) / 16, nt = r % 16;
;     const float* src = (which == 2 ? p.w_down : (which == 0 ? p.w_gate : p.w_up)) + (size_t)le * 2048 * 2048;
;     const int tid = opaque_tid(), nq = tid & 31, kq0 = tid >> 5;
; #pragma unroll
;     for (int it = 0; it < 2; ++it)
; #pragma unroll
;         for (int kk = 0; kk < 4; ++kk) in.v[it * 4 + kk] = __builtin_nontemporal_load((const f32x4*)(src + (size_t)(kt * 128 + (kq0 + it * 16) * 4 + kk) * 2048 + nt * 128 + nq * 4));
; }
; DEVI void cvt8_stream3(const Params& p, int L, int t0, int step, int count, char* smem) {
;     if (count <= 0) return;
;     CvtIn a, b; cvt8_load(p, L, t0, a);
;     if (count > 1) cvt8_load(p, L, t0 + step, b);
.LBB0_1397:
	s_waitcnt lgkmcnt(0)
	s_cmpk_eq_i32 s18, 0x100
	v_readlane_b32 s6, v254, 49
	s_cselect_b64 s[4:5], -1, 0
	v_readlane_b32 s7, v254, 50
	s_and_b64 s[4:5], s[6:7], s[4:5]
	v_readlane_b32 s60, v254, 59
	s_andn2_b64 vcc, exec, s[4:5]
	v_readlane_b32 s61, v254, 60
	s_cbranch_vccnz .LBB0_1407
	s_mov_b32 s4, s2
	s_cmpk_lt_i32 s4, 0x80
	s_cbranch_scc1 .LBB0_1407
	s_mov_b32 s5, s2
	s_add_i32 s4, s5, 0xffffff80
	s_and_b32 s6, s4, 0xfffff000
	s_add_i32 s7, s5, 0xf7f
	s_cmpk_lt_u32 s7, 0x1fff
	s_cselect_b32 s7, s64, 0x80
	s_cmpk_lg_i32 s6, 0x2000
	s_cselect_b32 s6, s7, 0x88
	s_add_u32 s6, s0, s6
	s_addc_u32 s7, s1, 0
	s_ashr_i32 s14, s4, 31
	s_lshr_b32 s14, s14, 20
	s_add_i32 s14, s4, s14
	s_and_b32 s14, s14, 0xf000
	s_sub_i32 s14, s4, s14
	s_sext_i32_i16 s15, s14
	s_lshr_b32 s15, s15, 15
	s_bfe_u32 s16, s15, 0x4000c
	s_bfe_u32 s15, s15, 0x80008
	s_add_i32 s16, s14, s16
	s_add_i32 s15, s14, s15
	s_and_b32 s16, s16, 0xfff0
	s_sext_i32_i16 s17, s15
	s_and_b32 s15, s15, 0xff00
	s_sub_i32 s16, s14, s16
	s_sub_i32 s14, s14, s15
	s_load_dwordx2 s[6:7], s[6:7], 0x0
	s_ashr_i32 s17, s17, 8
	s_sext_i32_i16 s15, s14
	s_bfe_u32 s15, s15, 0x4001b
	s_add_i32 s17, s17, 16
	s_add_i32 s14, s14, s15
	s_and_b32 s52, s17, 0xffff
	s_sext_i32_i16 s19, s14
	s_lshl_b64 s[14:15], s[52:53], 24
	s_waitcnt lgkmcnt(0)
	s_add_u32 s14, s6, s14
	v_mov_b32_e32 v1, v0
	s_addc_u32 s15, s7, s15
	s_lshl_b32 s6, s19, 3
	v_ashrrev_i32_e32 v2, 3, v1
	s_sext_i32_i16 s16, s16
	s_and_b32 s6, s6, 0xffffff80
	v_and_b32_e32 v2, -4, v2
	s_waitcnt vmcnt(0)
	v_add_u32_e32 v4, s6, v2
	s_lshl_b32 s6, s16, 7
	s_ashr_i32 s7, s6, 31
	s_lshl_b64 s[6:7], s[6:7], 2
	s_add_u32 s6, s14, s6
	v_lshlrev_b32_e32 v1, 4, v1
	s_addc_u32 s7, s15, s7
	v_and_b32_e32 v2, 0x1f0, v1
	v_ashrrev_i32_e32 v5, 31, v4
	v_lshl_add_u64 v[6:7], s[6:7], 0, v[2:3]
	v_lshlrev_b64 v[8:9], 13, v[4:5]
	v_lshl_add_u64 v[12:13], v[6:7], 0, v[8:9]
	v_or_b32_e32 v8, 1, v4
	v_ashrrev_i32_e32 v9, 31, v8
	v_lshlrev_b64 v[8:9], 13, v[8:9]
	v_lshl_add_u64 v[8:9], v[6:7], 0, v[8:9]
	global_load_dwordx4 v[20:23], v[12:13], off nt
	global_load_dwordx4 v[24:27], v[8:9], off nt
	v_or_b32_e32 v8, 2, v4
	v_or_b32_e32 v4, 3, v4
	v_ashrrev_i32_e32 v9, 31, v8
	v_ashrrev_i32_e32 v5, 31, v4
	v_lshlrev_b64 v[8:9], 13, v[8:9]
	v_lshlrev_b64 v[4:5], 13, v[4:5]
	v_lshl_add_u64 v[8:9], v[6:7], 0, v[8:9]
	v_lshl_add_u64 v[4:5], v[6:7], 0, v[4:5]
	global_load_dwordx4 v[28:31], v[8:9], off nt
	global_load_dwordx4 v[32:35], v[4:5], off nt
	v_add_co_u32_e32 v4, vcc, s94, v12
	s_mov_b32 s6, 0x82000
	s_nop 0
	v_addc_co_u32_e32 v5, vcc, 0, v13, vcc
	v_add_co_u32_e32 v8, vcc, s6, v12
	s_mov_b32 s6, 0x84000
	s_nop 0
	v_addc_co_u32_e32 v9, vcc, 0, v13, vcc
	v_add_co_u32_e32 v14, vcc, s6, v12
	s_mov_b32 s6, 0x86000
	s_nop 0
	v_addc_co_u32_e32 v15, vcc, 0, v13, vcc
	v_add_co_u32_e32 v16, vcc, s6, v12
	s_and_b32 s6, s5, 0xfffff000
	s_add_i32 s7, s5, 0xfff
	s_cmpk_lt_u32 s7, 0x1fff
	s_cselect_b32 s7, s64, 0x80
	s_cmpk_lg_i32 s6, 0x2000
	s_cselect_b32 s6, s7, 0x88
	s_add_u32 s6, s0, s6
	s_addc_u32 s7, s1, 0
	s_ashr_i32 s14, s5, 31
	s_lshr_b32 s14, s14, 20
	s_add_i32 s14, s5, s14
	s_and_b32 s14, s14, 0xf000
	s_sub_i32 s5, s5, s14
	s_sext_i32_i16 s14, s5
	s_lshr_b32 s14, s14, 15
	s_bfe_u32 s15, s14, 0x4000c
	s_add_i32 s15, s5, s15
	s_and_b32 s15, s15, 0xfff0
	s_bfe_u32 s14, s14, 0x80008
	v_addc_co_u32_e32 v17, vcc, 0, v13, vcc
	s_sub_i32 s15, s5, s15
	s_add_i32 s14, s5, s14
	global_load_dwordx4 v[4:7], v[4:5], off nt
	s_nop 0
	global_load_dwordx4 v[8:11], v[8:9], off nt
	s_nop 0
	global_load_dwordx4 v[12:15], v[14:15], off nt
	s_nop 0
	global_load_dwordx4 v[16:19], v[16:17], off nt
	s_sext_i32_i16 s16, s15
	s_sext_i32_i16 s15, s14
	s_and_b32 s14, s14, 0xff00
	s_load_dwordx2 s[6:7], s[6:7], 0x0
	s_ashr_i32 s15, s15, 8
	s_sub_i32 s5, s5, s14
	s_sext_i32_i16 s14, s5
	s_add_i32 s15, s15, 16
	s_bfe_u32 s14, s14, 0x4001b
	s_and_b32 s52, s15, 0xffff
	s_add_i32 s5, s5, s14
	s_lshl_b64 s[14:15], s[52:53], 24
	s_waitcnt lgkmcnt(0)
	s_add_u32 s14, s6, s14
	s_sext_i32_i16 s5, s5
	s_addc_u32 s15, s7, s15
	v_mov_b32_e32 v1, v0
	s_lshl_b32 s6, s16, 7
	s_lshl_b32 s5, s5, 3
	v_ashrrev_i32_e32 v2, 3, v1
	s_ashr_i32 s7, s6, 31
	s_and_b32 s5, s5, 0xffffff80
	v_and_b32_e32 v2, -4, v2
	s_lshl_b64 s[6:7], s[6:7], 2
	v_add_u32_e32 v44, s5, v2
	s_add_u32 s6, s14, s6
	v_lshlrev_b32_e32 v1, 4, v1
	s_addc_u32 s7, s15, s7
	v_and_b32_e32 v2, 0x1f0, v1
	v_ashrrev_i32_e32 v45, 31, v44
	v_lshl_add_u64 v[46:47], s[6:7], 0, v[2:3]
	v_lshlrev_b64 v[36:37], 13, v[44:45]
	v_lshl_add_u64 v[48:49], v[46:47], 0, v[36:37]
	v_or_b32_e32 v36, 1, v44
	v_or_b32_e32 v50, 2, v44
	v_or_b32_e32 v44, 3, v44
	v_ashrrev_i32_e32 v37, 31, v36
	v_ashrrev_i32_e32 v51, 31, v50
	v_ashrrev_i32_e32 v45, 31, v44
	v_lshlrev_b64 v[36:37], 13, v[36:37]
	v_lshlrev_b64 v[50:51], 13, v[50:51]
	v_lshlrev_b64 v[44:45], 13, v[44:45]
	v_lshl_add_u64 v[40:41], v[46:47], 0, v[36:37]
	v_lshl_add_u64 v[50:51], v[46:47], 0, v[50:51]
	v_lshl_add_u64 v[44:45], v[46:47], 0, v[44:45]
	global_load_dwordx4 v[36:39], v[48:49], off nt
	s_nop 0
	global_load_dwordx4 v[40:43], v[40:41], off nt
	s_nop 0
	global_load_dwordx4 v[72:75], v[50:51], off nt
	global_load_dwordx4 v[76:79], v[44:45], off nt
	v_add_co_u32_e32 v44, vcc, s94, v48
	s_mov_b32 s5, 0
	s_nop 0
	v_addc_co_u32_e32 v45, vcc, 0, v49, vcc
	v_add_co_u32_e32 v46, vcc, 0x82000, v48
	s_nop 1
	v_addc_co_u32_e32 v47, vcc, 0, v49, vcc
	global_load_dwordx4 v[84:87], v[44:45], off nt
	global_load_dwordx4 v[88:91], v[46:47], off nt
	v_add_co_u32_e32 v44, vcc, 0x84000, v48
	s_nop 1
	v_addc_co_u32_e32 v45, vcc, 0, v49, vcc
	v_add_co_u32_e32 v46, vcc, 0x86000, v48
	s_nop 1
	v_addc_co_u32_e32 v47, vcc, 0, v49, vcc
	global_load_dwordx4 v[92:95], v[44:45], off nt
	global_load_dwordx4 v[96:99], v[46:47], off nt
	s_waitcnt vmcnt(8)
	s_branch .LBB0_1401
; DEVI int opaque_tid() { int t = threadIdx.x; asm volatile("" : "+v"(t)); return t; }
; DEVI unsigned cvt4_fp8(float a, float b, float c, float d) { int w = 0; w = __builtin_amdgcn_cvt_pk_fp8_f32(a, b, w, false); w = __builtin_amdgcn_cvt_pk_fp8_f32(c, d, w, true); return (unsigned)w; }
; DEVI void cvt8_finish(const Params& p, int L, int t, const CvtIn& in, char* smem) {
;     const int which = t / 4096, r = t % 4096, le = L * 16 + r / 256, kt = (r % 256) / 16, nt = r % 16;
;     unsigned char* dst = (which == 2) ? (unsigned char*)(p.ws + WS_WDN) + (size_t)le * 2048 * 2048 + (size_t)(nt * 128) * 2048
;                                       : (unsigned char*)(p.ws + WS_WGU) + (size_t)le * 4096 * 2048 + (size_t)(nt * 256 + which * 128) * 2048;
;     unsigned char* T = (unsigned char*)smem;
;     const int tid = opaque_tid(), nq = tid & 31, kq0 = tid >> 5;
; #pragma unroll
;     for (int it = 0; it < 2; ++it) { const int kq = kq0 + it * 16;
; #pragma unroll
;         for (int j = 0; j < 4; ++j) *(unsigned*)(T + (nq * 4 + j) * 144 + kq * 4) =
;             cvt4_fp8(in.v[it * 4][j] * W8_SCALE, in.v[it * 4 + 1][j] * W8_SCALE, in.v[it * 4 + 2][j] * W8_SCALE, in.v[it * 4 + 3][j] * W8_SCALE); }
;     __syncthreads();
; #pragma unroll
;     for (int i = 0; i < 2; ++i) { const int nl = (tid >> 3) + 64 * i, kc = (tid & 7) * 16;
;         *(u32x4*)(dst + (size_t)nl * 2048 + kt * 128 + kc) = *(const u32x4*)(T + nl * 144 + kc); }
;     __syncthreads();
; }
.LBB0_1400:
	v_mul_f32_e32 v20, 0x42800000, v20
	v_mul_f32_e32 v24, 0x42800000, v24
	v_mov_b32_e32 v101, v3
	v_cvt_pk_fp8_f32 v101, v20, v24
	v_mul_f32_e32 v24, 0x42800000, v28
	v_mul_f32_e32 v28, 0x42800000, v32
	v_mov_b32_e32 v1, v0
	v_cvt_pk_fp8_f32 v101, v24, v28 op_sel:[0,0,1]
	v_mul_f32_e32 v21, 0x42800000, v21
	v_mul_f32_e32 v24, 0x42800000, v25
	v_mov_b32_e32 v25, v3
	v_cvt_pk_fp8_f32 v25, v21, v24
	v_lshlrev_b32_e32 v2, 2, v1
	v_and_b32_e32 v2, 0x7c, v2
	v_ashrrev_i32_e32 v100, 3, v1
	v_and_b32_e32 v20, -4, v100
	v_mul_u32_u24_e32 v2, 0x90, v2
	v_add3_u32 v2, 0, v20, v2
	v_mul_f32_e32 v20, 0x42800000, v29
	v_mul_f32_e32 v21, 0x42800000, v33
	v_cvt_pk_fp8_f32 v25, v20, v21 op_sel:[0,0,1]
	v_mul_f32_e32 v20, 0x42800000, v22
	v_mul_f32_e32 v21, 0x42800000, v26
	v_mov_b32_e32 v26, v3
	v_cvt_pk_fp8_f32 v26, v20, v21
	v_mul_f32_e32 v20, 0x42800000, v23
	v_mul_f32_e32 v21, 0x42800000, v27
	v_mov_b32_e32 v23, v3
	v_cvt_pk_fp8_f32 v23, v20, v21
	v_mul_f32_e32 v20, 0x42800000, v31
	v_mul_f32_e32 v21, 0x42800000, v35
	v_mul_f32_e32 v4, 0x42800000, v4
	v_cvt_pk_fp8_f32 v23, v20, v21 op_sel:[0,0,1]
	v_mul_f32_e32 v8, 0x42800000, v8
	v_mov_b32_e32 v20, v3
	v_cvt_pk_fp8_f32 v20, v4, v8
	v_mul_f32_e32 v4, 0x42800000, v5
	v_mul_f32_e32 v5, 0x42800000, v9
	v_mov_b32_e32 v8, v3
	v_cvt_pk_fp8_f32 v8, v4, v5
	s_lshl_b32 s7, s7, 8
	v_mul_f32_e32 v4, 0x42800000, v13
	v_mul_f32_e32 v5, 0x42800000, v17
	s_sub_i32 s6, s6, s7
	v_cvt_pk_fp8_f32 v8, v4, v5 op_sel:[0,0,1]
	v_mul_f32_e32 v4, 0x42800000, v6
	v_mul_f32_e32 v5, 0x42800000, v10
	v_mov_b32_e32 v10, v3
	s_sext_i32_i16 s7, s6
	v_cvt_pk_fp8_f32 v10, v4, v5
	v_mul_f32_e32 v4, 0x42800000, v7
	v_mul_f32_e32 v5, 0x42800000, v11
	v_mov_b32_e32 v7, v3
	s_bfe_u32 s7, s7, 0x4001b
	v_mul_f32_e32 v12, 0x42800000, v12
	v_mul_f32_e32 v16, 0x42800000, v16
	v_cvt_pk_fp8_f32 v7, v4, v5
	s_add_i32 s6, s6, s7
	v_cvt_pk_fp8_f32 v20, v12, v16 op_sel:[0,0,1]
	s_sext_i32_i16 s6, s6
	v_mul_f32_e32 v22, 0x42800000, v30
	v_mul_f32_e32 v24, 0x42800000, v34
	v_mul_f32_e32 v6, 0x42800000, v14
	v_mul_f32_e32 v9, 0x42800000, v18
	v_cvt_pk_fp8_f32 v26, v22, v24 op_sel:[0,0,1]
	v_cvt_pk_fp8_f32 v10, v6, v9 op_sel:[0,0,1]
	v_mul_f32_e32 v4, 0x42800000, v15
	v_mul_f32_e32 v5, 0x42800000, v19
	s_lshl_b32 s6, s6, 3
	v_cvt_pk_fp8_f32 v7, v4, v5 op_sel:[0,0,1]
	v_lshlrev_b32_e32 v1, 4, v1
	s_and_b32 s6, s6, 0xffffff80
	ds_write2_b32 v2, v101, v20 offset1:16
	ds_write2_b32 v2, v25, v8 offset0:36 offset1:52
	ds_write2_b32 v2, v26, v10 offset0:72 offset1:88
	ds_write2_b32 v2, v23, v7 offset0:108 offset1:124
	v_and_b32_e32 v2, 0x70, v1
	s_ashr_i32 s7, s6, 31
	v_mul_lo_u32 v1, v100, s91
	s_add_u32 s6, s14, s6
	v_add3_u32 v1, 0, v2, v1
	s_waitcnt lgkmcnt(0)
	s_barrier
	s_addc_u32 s7, s15, s7
	ds_read_b128 v[4:7], v1
	v_ashrrev_i32_e32 v101, 31, v100
	v_lshl_add_u64 v[8:9], s[6:7], 0, v[2:3]
	v_lshlrev_b64 v[10:11], 11, v[100:101]
	v_lshl_add_u64 v[12:13], v[8:9], 0, v[10:11]
	ds_read_b128 v[8:11], v1 offset:9216
	s_waitcnt lgkmcnt(1)
	global_store_dwordx4 v[12:13], v[4:7], off
	s_add_i32 s5, s5, 1
	s_addk_i32 s4, 0x80
	v_add_co_u32_e32 v4, vcc, 0x20000, v12
	s_nop 0
	v_addc_co_u32_e32 v5, vcc, 0, v13, vcc
	s_waitcnt lgkmcnt(0)
	global_store_dwordx4 v[4:5], v[8:11], off
	s_cmp_lg_u32 s5, 10
	s_cbranch_scc1 .Lstrm7_cont
	s_barrier
	s_branch .LBB0_1407
.Lstrm7_cont:
	s_cmp_gt_u32 s5, 8
	s_cbranch_scc1 .Lstrm7_w2
	s_waitcnt vmcnt(10)
	s_branch .Lstrm7_wd

; DEVI int opaque_tid() { int t = threadIdx.x; asm volatile("" : "+v"(t)); return t; }
; DEVI void cvt8_load(const Params& p, int L, int t, CvtIn& in) {
;     const int which = t / 4096, r = t % 4096, le = L * 16 + r / 256, kt = (r % 256) / 16, nt = r % 16;
;     const float* src = (which == 2 ? p.w_down : (which == 0 ? p.w_gate : p.w_up)) + (size_t)le * 2048 * 2048;
;     const int tid = opaque_tid(), nq = tid & 31, kq0 = tid >> 5;
; #pragma unroll
;     for (int it = 0; it < 2; ++it)
; #pragma unroll
;         for (int kk = 0; kk < 4; ++kk) in.v[it * 4 + kk] = __builtin_nontemporal_load((const f32x4*)(src + (size_t)(kt * 128 + (kq0 + it * 16) * 4 + kk) * 2048 + nt * 128 + nq * 4));
; }
; DEVI void cvt8_stream3(const Params& p, int L, int t0, int step, int count, char* smem) {
;     if (count <= 0) return;
;     CvtIn a, b; cvt8_load(p, L, t0, a);
;     if (count > 1) cvt8_load(p, L, t0 + step, b);
; #pragma nounroll
;     for (int i = 0; i < count; ++i) { CvtIn c;
;         if (i + 2 < count) cvt8_load(p, L, t0 + (i + 2) * step, c);
;         cvt8_finish(p, L, t0 + i * step, a, smem);
;         a = b; b = c; }
; }
.LBB0_1401:
	s_cmp_gt_u32 s5, 7
	s_cbranch_scc1 .LBB0_1403
	s_bitcmp1_b32 s5, 0
	s_cbranch_scc0 .Lstrm7_lb
	s_add_i32 s14, s4, 0x100
	s_and_b32 s6, s14, 0xfffff000
	s_add_i32 s7, s4, 0x10ff
	s_cmpk_lt_u32 s7, 0x1fff
	s_cselect_b32 s7, s64, 0x80
	s_cmpk_lg_i32 s6, 0x2000
	s_cselect_b32 s6, s7, 0x88
	s_add_u32 s6, s0, s6
	s_addc_u32 s7, s1, 0
	s_ashr_i32 s15, s14, 31
	s_lshr_b32 s15, s15, 20
	s_add_i32 s15, s14, s15
	s_and_b32 s15, s15, 0xf000
	s_sub_i32 s14, s14, s15
	s_sext_i32_i16 s15, s14
	s_lshr_b32 s15, s15, 15
	s_bfe_u32 s16, s15, 0x4000c
	s_bfe_u32 s15, s15, 0x80008
	s_add_i32 s16, s14, s16
	s_add_i32 s15, s14, s15
	s_and_b32 s16, s16, 0xfff0
	s_sext_i32_i16 s17, s15
	s_and_b32 s15, s15, 0xff00
	s_sub_i32 s16, s14, s16
	s_sub_i32 s14, s14, s15
	s_load_dwordx2 s[6:7], s[6:7], 0x0
	s_ashr_i32 s17, s17, 8
	s_sext_i32_i16 s15, s14
	s_bfe_u32 s15, s15, 0x4001b
	s_add_i32 s17, s17, 16
	s_add_i32 s14, s14, s15
	s_and_b32 s52, s17, 0xffff
	s_sext_i32_i16 s19, s14
	s_lshl_b64 s[14:15], s[52:53], 24
	s_waitcnt lgkmcnt(0)
	s_add_u32 s14, s6, s14
	v_mov_b32_e32 v1, v0
	s_addc_u32 s15, s7, s15
	s_lshl_b32 s6, s19, 3
	v_ashrrev_i32_e32 v2, 3, v1
	s_sext_i32_i16 s16, s16
	s_and_b32 s6, s6, 0xffffff80
	v_and_b32_e32 v2, -4, v2
	v_add_u32_e32 v72, s6, v2
	s_lshl_b32 s6, s16, 7
	s_ashr_i32 s7, s6, 31
	s_lshl_b64 s[6:7], s[6:7], 2
	s_add_u32 s6, s14, s6
	v_lshlrev_b32_e32 v1, 4, v1
	s_addc_u32 s7, s15, s7
	v_and_b32_e32 v2, 0x1f0, v1
	v_ashrrev_i32_e32 v73, 31, v72
	v_lshl_add_u64 v[74:75], s[6:7], 0, v[2:3]
	v_lshlrev_b64 v[36:37], 13, v[72:73]
	v_lshl_add_u64 v[92:93], v[74:75], 0, v[36:37]
	v_add_co_u32_e32 v84, vcc, s94, v92
	v_or_b32_e32 v36, 1, v72
	s_nop 0
	v_addc_co_u32_e32 v85, vcc, 0, v93, vcc
	v_add_co_u32_e32 v88, vcc, 0x82000, v92
	v_or_b32_e32 v76, 2, v72
	s_nop 0
	v_addc_co_u32_e32 v89, vcc, 0, v93, vcc
	v_or_b32_e32 v72, 3, v72
	v_add_co_u32_e32 v94, vcc, 0x84000, v92
	v_ashrrev_i32_e32 v37, 31, v36
	v_ashrrev_i32_e32 v77, 31, v76
	v_ashrrev_i32_e32 v73, 31, v72
	v_addc_co_u32_e32 v95, vcc, 0, v93, vcc
	v_lshlrev_b64 v[36:37], 13, v[36:37]
	v_lshlrev_b64 v[76:77], 13, v[76:77]
	v_lshlrev_b64 v[72:73], 13, v[72:73]
	v_add_co_u32_e32 v96, vcc, 0x86000, v92
	v_lshl_add_u64 v[40:41], v[74:75], 0, v[36:37]
	v_lshl_add_u64 v[76:77], v[74:75], 0, v[76:77]
	v_lshl_add_u64 v[78:79], v[74:75], 0, v[72:73]
	v_addc_co_u32_e32 v97, vcc, 0, v93, vcc
	global_load_dwordx4 v[36:39], v[92:93], off nt
	s_nop 0
	global_load_dwordx4 v[40:43], v[40:41], off nt
	s_nop 0
	global_load_dwordx4 v[72:75], v[76:77], off nt
	s_nop 0
	global_load_dwordx4 v[76:79], v[78:79], off nt
	s_nop 0
	global_load_dwordx4 v[84:87], v[84:85], off nt
	s_nop 0
	global_load_dwordx4 v[88:91], v[88:89], off nt
	s_nop 0
	global_load_dwordx4 v[92:95], v[94:95], off nt
	s_nop 0
	global_load_dwordx4 v[96:99], v[96:97], off nt
	s_branch .LBB0_1403
.Lstrm7_lb:
	s_add_i32 s14, s4, 0x100
	s_and_b32 s6, s14, 0xfffff000
	s_add_i32 s7, s4, 0x10ff
	s_cmpk_lt_u32 s7, 0x1fff
	s_cselect_b32 s7, s64, 0x80
	s_cmpk_lg_i32 s6, 0x2000
	s_cselect_b32 s6, s7, 0x88
	s_add_u32 s6, s0, s6
	s_addc_u32 s7, s1, 0
	s_ashr_i32 s15, s14, 31
	s_lshr_b32 s15, s15, 20
	s_add_i32 s15, s14, s15
	s_and_b32 s15, s15, 0xf000
	s_sub_i32 s14, s14, s15
	s_sext_i32_i16 s15, s14
	s_lshr_b32 s15, s15, 15
	s_bfe_u32 s16, s15, 0x4000c
	s_bfe_u32 s15, s15, 0x80008
	s_add_i32 s16, s14, s16
	s_add_i32 s15, s14, s15
	s_and_b32 s16, s16, 0xfff0
	s_sext_i32_i16 s17, s15
	s_and_b32 s15, s15, 0xff00
	s_sub_i32 s16, s14, s16
	s_sub_i32 s14, s14, s15
	s_load_dwordx2 s[6:7], s[6:7], 0x0
	s_ashr_i32 s17, s17, 8
	s_sext_i32_i16 s15, s14
	s_bfe_u32 s15, s15, 0x4001b
	s_add_i32 s17, s17, 16
	s_add_i32 s14, s14, s15
	s_and_b32 s52, s17, 0xffff
	s_sext_i32_i16 s19, s14
	s_lshl_b64 s[14:15], s[52:53], 24
	s_waitcnt lgkmcnt(0)
	s_add_u32 s14, s6, s14
	v_mov_b32_e32 v1, v0
	s_addc_u32 s15, s7, s15
	s_lshl_b32 s6, s19, 3
	v_ashrrev_i32_e32 v2, 3, v1
	s_sext_i32_i16 s16, s16
	s_and_b32 s6, s6, 0xffffff80
	v_and_b32_e32 v2, -4, v2
	v_add_u32_e32 v64, s6, v2
	s_lshl_b32 s6, s16, 7
	s_ashr_i32 s7, s6, 31
	s_lshl_b64 s[6:7], s[6:7], 2
	s_add_u32 s6, s14, s6
	v_lshlrev_b32_e32 v1, 4, v1
	s_addc_u32 s7, s15, s7
	v_and_b32_e32 v2, 0x1f0, v1
	v_ashrrev_i32_e32 v65, 31, v64
	v_lshl_add_u64 v[66:67], s[6:7], 0, v[2:3]
	v_lshlrev_b64 v[80:81], 13, v[64:65]
	v_lshl_add_u64 v[48:49], v[66:67], 0, v[80:81]
	v_add_co_u32_e32 v56, vcc, s94, v48
	v_or_b32_e32 v80, 1, v64
	s_nop 0
	v_addc_co_u32_e32 v57, vcc, 0, v49, vcc
	v_add_co_u32_e32 v52, vcc, 0x82000, v48
	v_or_b32_e32 v60, 2, v64
	s_nop 0
	v_addc_co_u32_e32 v53, vcc, 0, v49, vcc
	v_or_b32_e32 v64, 3, v64
	v_add_co_u32_e32 v50, vcc, 0x84000, v48
	v_ashrrev_i32_e32 v81, 31, v80
	v_ashrrev_i32_e32 v61, 31, v60
	v_ashrrev_i32_e32 v65, 31, v64
	v_addc_co_u32_e32 v51, vcc, 0, v49, vcc
	v_lshlrev_b64 v[80:81], 13, v[80:81]
	v_lshlrev_b64 v[60:61], 13, v[60:61]
	v_lshlrev_b64 v[64:65], 13, v[64:65]
	v_add_co_u32_e32 v44, vcc, 0x86000, v48
	v_lshl_add_u64 v[68:69], v[66:67], 0, v[80:81]
	v_lshl_add_u64 v[60:61], v[66:67], 0, v[60:61]
	v_lshl_add_u64 v[62:63], v[66:67], 0, v[64:65]
	v_addc_co_u32_e32 v45, vcc, 0, v49, vcc
	global_load_dwordx4 v[80:83], v[48:49], off nt
	s_nop 0
	global_load_dwordx4 v[68:71], v[68:69], off nt
	s_nop 0
	global_load_dwordx4 v[64:67], v[60:61], off nt
	s_nop 0
	global_load_dwordx4 v[60:63], v[62:63], off nt
	s_nop 0
	global_load_dwordx4 v[56:59], v[56:57], off nt
	s_nop 0
	global_load_dwordx4 v[52:55], v[52:53], off nt
	s_nop 0
	global_load_dwordx4 v[48:51], v[50:51], off nt
	s_nop 0
	global_load_dwordx4 v[44:47], v[44:45], off nt
